# stack9: wave_sum ds_bpermute hops -> DPP / permlane-swap moves (22 chains in finish + LN phases), on top of stack8
# speedup vs baseline: 1.0066x; 1.0052x over previous
.LBB0_817:
	v_mov_b32_e32 v2, v48
	s_nop 0
	v_ashrrev_i32_e32 v3, 31, v2
	v_lshl_add_u64 v[4:5], s[16:17], 0, v[2:3]
	v_lshlrev_b64 v[46:47], 1, v[4:5]
	v_lshl_add_u64 v[4:5], s[6:7], 0, v[46:47]
	v_lshl_add_u64 v[6:7], s[8:9], 0, v[46:47]
	v_lshl_add_u64 v[8:9], v[2:3], 1, s[12:13]
	global_load_dwordx4 v[60:63], v[4:5], off nt
	global_load_dwordx4 v[38:41], v[4:5], off offset:1024 nt
	global_load_dwordx4 v[64:67], v[6:7], off nt
	global_load_dwordx4 v[42:45], v[6:7], off offset:1024 nt
	global_load_dwordx4 v[68:71], v[8:9], off nt
	global_load_dwordx4 v[34:37], v[8:9], off offset:1024 nt
	global_load_dwordx4 v[26:29], v[4:5], off offset:2048 nt
	global_load_dwordx4 v[14:17], v[4:5], off offset:3072 nt
	global_load_dwordx4 v[30:33], v[6:7], off offset:2048 nt
	global_load_dwordx4 v[18:21], v[6:7], off offset:3072 nt
	global_load_dwordx4 v[22:25], v[8:9], off offset:2048 nt
	global_load_dwordx4 v[10:13], v[8:9], off offset:3072 nt
	v_lshl_add_u64 v[6:7], v[2:3], 2, s[22:23]
	global_load_dwordx4 v[2:5], v[6:7], off offset:16
	s_nop 0
	global_load_dwordx4 v[6:9], v[6:7], off
	s_waitcnt vmcnt(13)
	v_lshlrev_b32_e32 v72, 16, v60
	s_waitcnt vmcnt(11)
	v_lshlrev_b32_e32 v73, 16, v64
	v_and_b32_e32 v64, 0xffff0000, v64
	v_and_b32_e32 v60, 0xffff0000, v60
	v_add_f32_e32 v72, v73, v72
	v_add_f32_e32 v73, v64, v60
	v_lshlrev_b32_e32 v60, 16, v61
	v_lshlrev_b32_e32 v64, 16, v65
	v_add_f32_e32 v74, v64, v60
	v_and_b32_e32 v60, 0xffff0000, v65
	v_and_b32_e32 v61, 0xffff0000, v61
	v_add_f32_e32 v65, v60, v61
	v_lshlrev_b32_e32 v60, 16, v62
	v_lshlrev_b32_e32 v61, 16, v66
	v_add_f32_e32 v75, v61, v60
	v_and_b32_e32 v60, 0xffff0000, v66
	v_and_b32_e32 v61, 0xffff0000, v62
	v_add_f32_e32 v76, v60, v61
	v_lshlrev_b32_e32 v60, 16, v63
	v_lshlrev_b32_e32 v61, 16, v67
	v_add_f32_e32 v77, v61, v60
	v_and_b32_e32 v60, 0xffff0000, v67
	v_and_b32_e32 v61, 0xffff0000, v63
	v_add_f32_e32 v78, v60, v61
	v_mul_f32_e32 v60, v72, v72
	v_fmac_f32_e32 v60, v73, v73
	v_fmac_f32_e32 v60, v74, v74
	v_fmac_f32_e32 v60, v65, v65
	v_fmac_f32_e32 v60, v75, v75
	v_cmp_lt_i32_e32 vcc, v51, v50
	v_fmac_f32_e32 v60, v76, v76
	v_fmac_f32_e32 v60, v77, v77
	v_cndmask_b32_e32 v59, v49, v51, vcc
	v_lshlrev_b32_e32 v59, 2, v59
	v_fmac_f32_e32 v60, v78, v78
	s_nop 1
	v_mov_b32_dpp v61, v60 quad_perm:[1,0,3,2] row_mask:0xf bank_mask:0xf
	v_cmp_lt_i32_e32 vcc, v52, v50
	v_lshl_add_u64 v[46:47], s[10:11], 0, v[46:47]
	s_add_i32 s20, s20, s92
	v_cndmask_b32_e32 v62, v49, v52, vcc
	v_lshlrev_b32_e32 v64, 2, v62
	s_waitcnt lgkmcnt(0)
	v_add_f32_e32 v60, v60, v61
	s_nop 1
	v_mov_b32_dpp v61, v60 quad_perm:[2,3,0,1] row_mask:0xf bank_mask:0xf
	v_cmp_lt_i32_e32 vcc, v53, v50
	s_add_u32 s12, s12, s14
	s_addc_u32 s13, s13, s15
	v_cndmask_b32_e32 v62, v49, v53, vcc
	v_lshlrev_b32_e32 v63, 2, v62
	s_waitcnt lgkmcnt(0)
	v_add_f32_e32 v61, v60, v61
	s_nop 1
	v_mov_b32_dpp v62, v61 row_half_mirror row_mask:0xf bank_mask:0xf
	v_cmp_lt_i32_e32 vcc, v54, v50
	s_add_u32 s16, s16, s18
	s_addc_u32 s17, s17, s19
	v_cndmask_b32_e32 v60, v49, v54, vcc
	v_lshlrev_b32_e32 v60, 2, v60
	s_waitcnt lgkmcnt(0)
	v_add_f32_e32 v62, v61, v62
	s_nop 1
	v_mov_b32_dpp v66, v62 row_mirror row_mask:0xf bank_mask:0xf
	v_cmp_lt_i32_e32 vcc, v55, v50
	s_cmpk_lt_i32 s20, 0x4400
	s_waitcnt lgkmcnt(0)
	v_add_f32_e32 v66, v62, v66
	v_cndmask_b32_e32 v61, v49, v55, vcc
	v_lshlrev_b32_e32 v61, 2, v61
	v_mov_b32_e32 v67, v66
	v_mov_b32_e32 v61, v66
	s_nop 1
	v_permlane16_swap_b32_e32 v67, v61
	s_nop 1
	v_mov_b32_dpp v67, v61 quad_perm:[0,1,2,3] row_mask:0x5 bank_mask:0xf
	v_cmp_lt_i32_e32 vcc, v56, v50
	s_waitcnt lgkmcnt(0)
	v_add_f32_e32 v66, v66, v67
	v_cndmask_b32_e32 v62, v49, v56, vcc
	v_lshlrev_b32_e32 v62, 2, v62
	v_mov_b32_e32 v67, v66
	v_mov_b32_e32 v62, v66
	s_nop 1
	v_permlane32_swap_b32_e32 v67, v62
	s_nop 1
	v_mov_b32_dpp v67, v62 quad_perm:[0,1,2,3] row_mask:0x3 bank_mask:0xf
	s_waitcnt lgkmcnt(0)
	v_add_f32_e32 v66, v66, v67
	v_fmamk_f32 v66, v66, 0x3b000000, v57
	v_mul_f32_e32 v67, 0x4f800000, v66
	v_cmp_gt_f32_e32 vcc, s2, v66
	s_nop 1
	v_cndmask_b32_e32 v66, v66, v67, vcc
	v_sqrt_f32_e32 v67, v66
	s_nop 0
	v_add_u32_e32 v79, -1, v67
	v_fma_f32 v80, -v79, v67, v66
	v_cmp_ge_f32_e64 s[0:1], 0, v80
	v_add_u32_e32 v80, 1, v67
	s_nop 0
	v_cndmask_b32_e64 v79, v67, v79, s[0:1]
	v_fma_f32 v67, -v80, v67, v66
	v_cmp_lt_f32_e64 s[0:1], 0, v67
	s_nop 1
	v_cndmask_b32_e64 v67, v79, v80, s[0:1]
	v_mul_f32_e32 v79, 0x37800000, v67
	v_cndmask_b32_e32 v67, v67, v79, vcc
	v_cmp_class_f32_e32 vcc, v66, v58
	s_nop 1
	v_cndmask_b32_e32 v66, v67, v66, vcc
	v_div_scale_f32 v67, s[0:1], v66, v66, 1.0
	v_rcp_f32_e32 v79, v67
	s_nop 0
	v_fma_f32 v80, -v67, v79, 1.0
	v_fmac_f32_e32 v79, v80, v79
	v_div_scale_f32 v80, vcc, 1.0, v66, 1.0
	v_mul_f32_e32 v81, v80, v79
	v_fma_f32 v82, -v67, v81, v80
	v_fmac_f32_e32 v81, v82, v79
	v_fma_f32 v67, -v67, v81, v80
	v_div_fmas_f32 v67, v67, v79, v81
	v_div_fixup_f32 v79, v67, v66, 1.0
	s_waitcnt vmcnt(9)
	v_lshlrev_b32_e32 v66, 16, v68
	v_mul_f32_e32 v80, 0xbfb8aa3b, v66
	v_exp_f32_e32 v80, v80
	v_and_b32_e32 v67, 0xffff0000, v68
	v_mul_f32_e32 v72, v72, v79
	s_waitcnt vmcnt(0)
	v_mul_f32_e32 v72, v6, v72
	v_add_f32_e32 v80, 1.0, v80
	v_div_scale_f32 v83, s[0:1], v80, v80, v66
	v_rcp_f32_e32 v84, v83
	v_lshlrev_b32_e32 v68, 16, v69
	v_and_b32_e32 v69, 0xffff0000, v69
	v_lshlrev_b32_e32 v81, 16, v70
	v_fma_f32 v85, -v83, v84, 1.0
	v_fmac_f32_e32 v84, v85, v84
	v_div_scale_f32 v85, vcc, v66, v80, v66
	v_mul_f32_e32 v86, v85, v84
	v_fma_f32 v87, -v83, v86, v85
	v_fmac_f32_e32 v86, v87, v84
	v_fma_f32 v83, -v83, v86, v85
	v_mul_f32_e32 v85, 0xbfb8aa3b, v67
	v_exp_f32_e32 v85, v85
	v_div_fmas_f32 v83, v83, v84, v86
	v_div_fixup_f32 v66, v83, v80, v66
	v_mul_f32_e32 v66, v66, v72
	v_add_f32_e32 v80, 1.0, v85
	v_div_scale_f32 v83, s[0:1], v80, v80, v67
	v_rcp_f32_e32 v84, v83
	v_mul_f32_e32 v72, v73, v79
	v_mul_f32_e32 v72, v7, v72
	v_mul_f32_e32 v65, v65, v79
	v_fma_f32 v73, -v83, v84, 1.0
	v_fmac_f32_e32 v84, v73, v84
	v_div_scale_f32 v73, vcc, v67, v80, v67
	v_mul_f32_e32 v85, v73, v84
	v_fma_f32 v86, -v83, v85, v73
	v_fmac_f32_e32 v85, v86, v84
	v_fma_f32 v73, -v83, v85, v73
	v_mul_f32_e32 v83, 0xbfb8aa3b, v68
	v_exp_f32_e32 v83, v83
	v_div_fmas_f32 v73, v73, v84, v85
	v_div_fixup_f32 v67, v73, v80, v67
	v_mul_f32_e32 v67, v67, v72
	v_add_f32_e32 v72, 1.0, v83
	v_div_scale_f32 v73, s[0:1], v72, v72, v68
	v_rcp_f32_e32 v80, v73
	v_cvt_pk_bf16_f32 v66, v66, v67
	v_mul_f32_e32 v67, v74, v79
	v_mul_f32_e32 v67, v8, v67
	v_fma_f32 v74, -v73, v80, 1.0
	v_fmac_f32_e32 v80, v74, v80
	v_div_scale_f32 v74, vcc, v68, v72, v68
	v_mul_f32_e32 v83, v74, v80
	v_fma_f32 v84, -v73, v83, v74
	v_fmac_f32_e32 v83, v84, v80
	v_fma_f32 v73, -v73, v83, v74
	v_mul_f32_e32 v74, 0xbfb8aa3b, v69
	v_exp_f32_e32 v74, v74
	v_div_fmas_f32 v73, v73, v80, v83
	v_div_fixup_f32 v68, v73, v72, v68
	v_mul_f32_e32 v67, v68, v67
	v_add_f32_e32 v72, 1.0, v74
	v_div_scale_f32 v73, s[0:1], v72, v72, v69
	v_rcp_f32_e32 v74, v73
	v_mul_f32_e32 v65, v9, v65
	v_and_b32_e32 v70, 0xffff0000, v70
	v_lshlrev_b32_e32 v82, 16, v71
	v_fma_f32 v68, -v73, v74, 1.0
	v_fmac_f32_e32 v74, v68, v74
	v_div_scale_f32 v68, vcc, v69, v72, v69
	v_mul_f32_e32 v80, v68, v74
	v_fma_f32 v83, -v73, v80, v68
	v_fmac_f32_e32 v80, v83, v74
	v_fma_f32 v68, -v73, v80, v68
	v_mul_f32_e32 v73, 0xbfb8aa3b, v81
	v_exp_f32_e32 v73, v73
	v_div_fmas_f32 v68, v68, v74, v80
	v_div_fixup_f32 v68, v68, v72, v69
	v_mul_f32_e32 v65, v68, v65
	v_add_f32_e32 v68, 1.0, v73
	v_div_scale_f32 v69, s[0:1], v68, v68, v81
	v_rcp_f32_e32 v72, v69
	v_cvt_pk_bf16_f32 v67, v67, v65
	v_mul_f32_e32 v65, v75, v79
	v_mul_f32_e32 v65, v2, v65
	v_fma_f32 v73, -v69, v72, 1.0
	v_fmac_f32_e32 v72, v73, v72
	v_div_scale_f32 v73, vcc, v81, v68, v81
	v_mul_f32_e32 v74, v73, v72
	v_fma_f32 v75, -v69, v74, v73
	v_fmac_f32_e32 v74, v75, v72
	v_fma_f32 v69, -v69, v74, v73
	v_mul_f32_e32 v73, 0xbfb8aa3b, v70
	v_exp_f32_e32 v73, v73
	v_div_fmas_f32 v69, v69, v72, v74
	v_div_fixup_f32 v68, v69, v68, v81
	v_mul_f32_e32 v65, v68, v65
	v_add_f32_e32 v69, 1.0, v73
	v_div_scale_f32 v72, s[0:1], v69, v69, v70
	v_rcp_f32_e32 v73, v72
	v_mul_f32_e32 v68, v76, v79
	v_mul_f32_e32 v68, v3, v68
	v_and_b32_e32 v71, 0xffff0000, v71
	v_fma_f32 v74, -v72, v73, 1.0
	v_fmac_f32_e32 v73, v74, v73
	v_div_scale_f32 v74, vcc, v70, v69, v70
	v_mul_f32_e32 v75, v74, v73
	v_fma_f32 v76, -v72, v75, v74
	v_fmac_f32_e32 v75, v76, v73
	v_fma_f32 v72, -v72, v75, v74
	v_mul_f32_e32 v74, 0xbfb8aa3b, v82
	v_exp_f32_e32 v74, v74
	v_div_fmas_f32 v72, v72, v73, v75
	v_div_fixup_f32 v69, v72, v69, v70
	v_mul_f32_e32 v68, v69, v68
	v_add_f32_e32 v69, 1.0, v74
	v_lshlrev_b32_e32 v74, 16, v38
	v_lshlrev_b32_e32 v75, 16, v42
	v_and_b32_e32 v42, 0xffff0000, v42
	v_and_b32_e32 v38, 0xffff0000, v38
	v_add_f32_e32 v74, v75, v74
	v_add_f32_e32 v38, v42, v38
	v_lshlrev_b32_e32 v42, 16, v39
	v_lshlrev_b32_e32 v75, 16, v43
	v_and_b32_e32 v43, 0xffff0000, v43
	v_and_b32_e32 v39, 0xffff0000, v39
	v_add_f32_e32 v42, v75, v42
	v_add_f32_e32 v39, v43, v39
	v_lshlrev_b32_e32 v43, 16, v40
	v_lshlrev_b32_e32 v75, 16, v44
	v_and_b32_e32 v44, 0xffff0000, v44
	v_and_b32_e32 v40, 0xffff0000, v40
	v_add_f32_e32 v43, v75, v43
	v_add_f32_e32 v40, v44, v40
	v_lshlrev_b32_e32 v44, 16, v41
	v_lshlrev_b32_e32 v75, 16, v45
	v_and_b32_e32 v45, 0xffff0000, v45
	v_and_b32_e32 v41, 0xffff0000, v41
	v_add_f32_e32 v41, v45, v41
	v_mul_f32_e32 v45, v74, v74
	v_fmac_f32_e32 v45, v38, v38
	v_fmac_f32_e32 v45, v42, v42
	v_fmac_f32_e32 v45, v39, v39
	v_div_scale_f32 v70, s[0:1], v69, v69, v82
	v_fmac_f32_e32 v45, v43, v43
	v_rcp_f32_e32 v72, v70
	v_add_f32_e32 v44, v75, v44
	v_fmac_f32_e32 v45, v40, v40
	v_fmac_f32_e32 v45, v44, v44
	v_fmac_f32_e32 v45, v41, v41
	s_nop 1
	v_mov_b32_dpp v75, v45 quad_perm:[1,0,3,2] row_mask:0xf bank_mask:0xf
	v_fma_f32 v73, -v70, v72, 1.0
	v_fmac_f32_e32 v72, v73, v72
	v_div_scale_f32 v73, vcc, v82, v69, v82
	v_mul_f32_e32 v76, v73, v72
	v_cvt_pk_bf16_f32 v68, v65, v68
	v_mul_f32_e32 v65, v77, v79
	v_fma_f32 v77, -v70, v76, v73
	v_fmac_f32_e32 v76, v77, v72
	s_waitcnt lgkmcnt(0)
	v_add_f32_e32 v45, v45, v75
	v_fma_f32 v70, -v70, v76, v73
	s_nop 1
	v_mov_b32_dpp v73, v45 quad_perm:[2,3,0,1] row_mask:0xf bank_mask:0xf
	v_div_fmas_f32 v70, v70, v72, v76
	v_mul_f32_e32 v72, 0xbfb8aa3b, v71
	v_exp_f32_e32 v72, v72
	v_div_fixup_f32 v69, v70, v69, v82
	s_waitcnt lgkmcnt(0)
	v_add_f32_e32 v45, v45, v73
	s_nop 1
	v_mov_b32_dpp v73, v45 row_half_mirror row_mask:0xf bank_mask:0xf
	v_add_f32_e32 v70, 1.0, v72
	v_mul_f32_e32 v65, v4, v65
	v_mul_f32_e32 v65, v69, v65
	v_mul_f32_e32 v69, v78, v79
	s_waitcnt lgkmcnt(0)
	v_add_f32_e32 v45, v45, v73
	s_nop 1
	v_mov_b32_dpp v72, v45 row_mirror row_mask:0xf bank_mask:0xf
	v_div_scale_f32 v73, s[0:1], v70, v70, v71
	v_rcp_f32_e32 v75, v73
	v_mul_f32_e32 v69, v5, v69
	s_waitcnt lgkmcnt(0)
	v_add_f32_e32 v45, v45, v72
	v_mov_b32_e32 v72, v45
	v_mov_b32_e32 v61, v45
	s_nop 1
	v_permlane16_swap_b32_e32 v72, v61
	s_nop 1
	v_mov_b32_dpp v72, v61 quad_perm:[0,1,2,3] row_mask:0x5 bank_mask:0xf
	v_fma_f32 v76, -v73, v75, 1.0
	v_fmac_f32_e32 v75, v76, v75
	v_div_scale_f32 v76, vcc, v71, v70, v71
	s_waitcnt lgkmcnt(0)
	v_add_f32_e32 v45, v45, v72
	v_mov_b32_e32 v72, v45
	v_mov_b32_e32 v62, v45
	s_nop 1
	v_permlane32_swap_b32_e32 v72, v62
	s_nop 1
	v_mov_b32_dpp v72, v62 quad_perm:[0,1,2,3] row_mask:0x3 bank_mask:0xf
	v_mul_f32_e32 v77, v76, v75
	v_fma_f32 v78, -v73, v77, v76
	v_fmac_f32_e32 v77, v78, v75
	v_fma_f32 v73, -v73, v77, v76
	s_waitcnt lgkmcnt(0)
	v_add_f32_e32 v45, v45, v72
	v_fmamk_f32 v45, v45, 0x3b000000, v57
	v_mul_f32_e32 v72, 0x4f800000, v45
	v_cmp_gt_f32_e64 s[0:1], s2, v45
	v_div_fmas_f32 v73, v73, v75, v77
	v_div_fixup_f32 v70, v73, v70, v71
	v_cndmask_b32_e64 v45, v45, v72, s[0:1]
	v_sqrt_f32_e32 v72, v45
	v_mul_f32_e32 v69, v70, v69
	v_cvt_pk_bf16_f32 v69, v65, v69
	global_store_dwordx4 v[46:47], v[66:69], off
	v_add_u32_e32 v71, -1, v72
	v_fma_f32 v73, -v71, v72, v45
	v_cmp_ge_f32_e32 vcc, 0, v73
	v_add_u32_e32 v73, 1, v72
	v_lshlrev_b32_e32 v68, 16, v36
	v_cndmask_b32_e32 v71, v72, v71, vcc
	v_fma_f32 v72, -v73, v72, v45
	v_cmp_lt_f32_e32 vcc, 0, v72
	v_and_b32_e32 v36, 0xffff0000, v36
	v_lshlrev_b32_e32 v69, 16, v37
	v_cndmask_b32_e32 v71, v71, v73, vcc
	v_mul_f32_e32 v72, 0x37800000, v71
	v_cndmask_b32_e64 v71, v71, v72, s[0:1]
	v_cmp_class_f32_e32 vcc, v45, v58
	v_and_b32_e32 v37, 0xffff0000, v37
	s_nop 0
	v_cndmask_b32_e32 v45, v71, v45, vcc
	v_div_scale_f32 v71, s[0:1], v45, v45, 1.0
	v_rcp_f32_e32 v72, v71
	s_nop 0
	v_fma_f32 v65, -v71, v72, 1.0
	v_fmac_f32_e32 v72, v65, v72
	v_div_scale_f32 v65, vcc, 1.0, v45, 1.0
	v_mul_f32_e32 v66, v65, v72
	v_fma_f32 v67, -v71, v66, v65
	v_fmac_f32_e32 v66, v67, v72
	v_fma_f32 v65, -v71, v66, v65
	v_div_fmas_f32 v65, v65, v72, v66
	v_div_fixup_f32 v45, v65, v45, 1.0
	v_lshlrev_b32_e32 v65, 16, v34
	v_mul_f32_e32 v67, 0xbfb8aa3b, v65
	v_exp_f32_e32 v67, v67
	v_mul_f32_e32 v72, v74, v45
	v_and_b32_e32 v34, 0xffff0000, v34
	v_mul_f32_e32 v72, v6, v72
	v_add_f32_e32 v67, 1.0, v67
	v_div_scale_f32 v70, s[0:1], v67, v67, v65
	v_rcp_f32_e32 v71, v70
	v_lshlrev_b32_e32 v66, 16, v35
	v_mul_f32_e32 v38, v38, v45
	v_mul_f32_e32 v38, v7, v38
	v_fma_f32 v73, -v70, v71, 1.0
	v_fmac_f32_e32 v71, v73, v71
	v_div_scale_f32 v73, vcc, v65, v67, v65
	v_mul_f32_e32 v74, v73, v71
	v_fma_f32 v75, -v70, v74, v73
	v_fmac_f32_e32 v74, v75, v71
	v_fma_f32 v70, -v70, v74, v73
	v_mul_f32_e32 v73, 0xbfb8aa3b, v34
	v_exp_f32_e32 v73, v73
	v_div_fmas_f32 v70, v70, v71, v74
	v_div_fixup_f32 v65, v70, v67, v65
	v_mul_f32_e32 v65, v65, v72
	v_add_f32_e32 v67, 1.0, v73
	v_div_scale_f32 v70, s[0:1], v67, v67, v34
	v_rcp_f32_e32 v71, v70
	v_and_b32_e32 v35, 0xffff0000, v35
	v_mul_f32_e32 v42, v42, v45
	v_mul_f32_e32 v42, v8, v42
	v_fma_f32 v72, -v70, v71, 1.0
	v_fmac_f32_e32 v71, v72, v71
	v_div_scale_f32 v72, vcc, v34, v67, v34
	v_mul_f32_e32 v73, v72, v71
	v_fma_f32 v74, -v70, v73, v72
	v_fmac_f32_e32 v73, v74, v71
	v_fma_f32 v70, -v70, v73, v72
	v_mul_f32_e32 v72, 0xbfb8aa3b, v66
	v_exp_f32_e32 v72, v72
	v_div_fmas_f32 v70, v70, v71, v73
	v_div_fixup_f32 v34, v70, v67, v34
	v_mul_f32_e32 v34, v34, v38
	v_add_f32_e32 v38, 1.0, v72
	v_div_scale_f32 v67, s[0:1], v38, v38, v66
	v_rcp_f32_e32 v70, v67
	v_cvt_pk_bf16_f32 v34, v65, v34
	v_mul_f32_e32 v39, v39, v45
	v_mul_f32_e32 v39, v9, v39
	v_fma_f32 v65, -v67, v70, 1.0
	v_fmac_f32_e32 v70, v65, v70
	v_div_scale_f32 v65, vcc, v66, v38, v66
	v_mul_f32_e32 v71, v65, v70
	v_fma_f32 v72, -v67, v71, v65
	v_fmac_f32_e32 v71, v72, v70
	v_fma_f32 v65, -v67, v71, v65
	v_mul_f32_e32 v67, 0xbfb8aa3b, v35
	v_exp_f32_e32 v67, v67
	v_div_fmas_f32 v65, v65, v70, v71
	v_div_fixup_f32 v38, v65, v38, v66
	v_mul_f32_e32 v38, v38, v42
	v_add_f32_e32 v65, 1.0, v67
	v_div_scale_f32 v66, s[0:1], v65, v65, v35
	v_rcp_f32_e32 v67, v66
	s_nop 0
	v_fma_f32 v42, -v66, v67, 1.0
	v_fmac_f32_e32 v67, v42, v67
	v_div_scale_f32 v42, vcc, v35, v65, v35
	v_mul_f32_e32 v70, v42, v67
	v_fma_f32 v71, -v66, v70, v42
	v_fmac_f32_e32 v70, v71, v67
	v_fma_f32 v42, -v66, v70, v42
	v_mul_f32_e32 v66, 0xbfb8aa3b, v68
	v_exp_f32_e32 v66, v66
	v_div_fmas_f32 v42, v42, v67, v70
	v_div_fixup_f32 v35, v42, v65, v35
	v_mul_f32_e32 v35, v35, v39
	v_add_f32_e32 v39, 1.0, v66
	v_div_scale_f32 v42, s[0:1], v39, v39, v68
	v_rcp_f32_e32 v65, v42
	v_cvt_pk_bf16_f32 v35, v38, v35
	v_mul_f32_e32 v38, v43, v45
	v_mul_f32_e32 v38, v2, v38
	v_fma_f32 v43, -v42, v65, 1.0
	v_fmac_f32_e32 v65, v43, v65
	v_div_scale_f32 v43, vcc, v68, v39, v68
	v_mul_f32_e32 v66, v43, v65
	v_fma_f32 v67, -v42, v66, v43
	v_fmac_f32_e32 v66, v67, v65
	v_fma_f32 v42, -v42, v66, v43
	v_mul_f32_e32 v43, 0xbfb8aa3b, v36
	v_exp_f32_e32 v43, v43
	v_div_fmas_f32 v42, v42, v65, v66
	v_div_fixup_f32 v39, v42, v39, v68
	v_mul_f32_e32 v38, v39, v38
	v_add_f32_e32 v42, 1.0, v43
	v_div_scale_f32 v43, s[0:1], v42, v42, v36
	v_rcp_f32_e32 v65, v43
	v_mul_f32_e32 v39, v40, v45
	v_mul_f32_e32 v39, v3, v39
	v_fma_f32 v40, -v43, v65, 1.0
	v_fmac_f32_e32 v65, v40, v65
	v_div_scale_f32 v40, vcc, v36, v42, v36
	v_mul_f32_e32 v66, v40, v65
	v_fma_f32 v67, -v43, v66, v40
	v_fmac_f32_e32 v66, v67, v65
	v_fma_f32 v40, -v43, v66, v40
	v_div_fmas_f32 v40, v40, v65, v66
	v_div_fixup_f32 v36, v40, v42, v36
	v_mul_f32_e32 v36, v36, v39
	v_cvt_pk_bf16_f32 v36, v38, v36
	v_mul_f32_e32 v38, v44, v45
	v_lshlrev_b32_e32 v44, 16, v26
	v_lshlrev_b32_e32 v65, 16, v30
	v_and_b32_e32 v30, 0xffff0000, v30
	v_and_b32_e32 v26, 0xffff0000, v26
	v_add_f32_e32 v44, v65, v44
	v_add_f32_e32 v26, v30, v26
	v_lshlrev_b32_e32 v30, 16, v27
	v_lshlrev_b32_e32 v65, 16, v31
	v_and_b32_e32 v31, 0xffff0000, v31
	v_and_b32_e32 v27, 0xffff0000, v27
	v_mul_f32_e32 v43, 0xbfb8aa3b, v69
	v_add_f32_e32 v30, v65, v30
	v_add_f32_e32 v27, v31, v27
	v_lshlrev_b32_e32 v31, 16, v28
	v_lshlrev_b32_e32 v65, 16, v32
	v_and_b32_e32 v32, 0xffff0000, v32
	v_and_b32_e32 v28, 0xffff0000, v28
	v_exp_f32_e32 v43, v43
	v_add_f32_e32 v31, v65, v31
	v_add_f32_e32 v28, v32, v28
	v_lshlrev_b32_e32 v32, 16, v29
	v_lshlrev_b32_e32 v65, 16, v33
	v_and_b32_e32 v33, 0xffff0000, v33
	v_and_b32_e32 v29, 0xffff0000, v29
	v_add_f32_e32 v29, v33, v29
	v_mul_f32_e32 v33, v44, v44
	v_fmac_f32_e32 v33, v26, v26
	v_fmac_f32_e32 v33, v30, v30
	v_add_f32_e32 v39, 1.0, v43
	v_fmac_f32_e32 v33, v27, v27
	v_div_scale_f32 v40, s[0:1], v39, v39, v69
	v_fmac_f32_e32 v33, v31, v31
	v_rcp_f32_e32 v42, v40
	v_add_f32_e32 v32, v65, v32
	v_fmac_f32_e32 v33, v28, v28
	v_fmac_f32_e32 v33, v32, v32
	v_fmac_f32_e32 v33, v29, v29
	s_nop 1
	v_mov_b32_dpp v65, v33 quad_perm:[1,0,3,2] row_mask:0xf bank_mask:0xf
	v_fma_f32 v43, -v40, v42, 1.0
	v_fmac_f32_e32 v42, v43, v42
	v_div_scale_f32 v43, vcc, v69, v39, v69
	v_mul_f32_e32 v66, v43, v42
	v_fma_f32 v67, -v40, v66, v43
	v_fmac_f32_e32 v66, v67, v42
	s_waitcnt lgkmcnt(0)
	v_add_f32_e32 v33, v33, v65
	v_fma_f32 v40, -v40, v66, v43
	s_nop 1
	v_mov_b32_dpp v43, v33 quad_perm:[2,3,0,1] row_mask:0xf bank_mask:0xf
	v_div_fmas_f32 v40, v40, v42, v66
	v_mul_f32_e32 v38, v4, v38
	v_div_fixup_f32 v39, v40, v39, v69
	v_mul_f32_e32 v38, v39, v38
	s_waitcnt lgkmcnt(0)
	v_add_f32_e32 v33, v33, v43
	s_nop 1
	v_mov_b32_dpp v43, v33 row_half_mirror row_mask:0xf bank_mask:0xf
	v_mul_f32_e32 v39, v41, v45
	v_mul_f32_e32 v42, 0xbfb8aa3b, v37
	v_exp_f32_e32 v42, v42
	v_mul_f32_e32 v39, v5, v39
	s_waitcnt lgkmcnt(0)
	v_add_f32_e32 v33, v33, v43
	s_nop 1
	v_mov_b32_dpp v41, v33 row_mirror row_mask:0xf bank_mask:0xf
	v_add_f32_e32 v40, 1.0, v42
	v_div_scale_f32 v42, s[0:1], v40, v40, v37
	v_rcp_f32_e32 v43, v42
	s_waitcnt lgkmcnt(0)
	v_add_f32_e32 v33, v33, v41
	v_mov_b32_e32 v41, v33
	v_mov_b32_e32 v61, v33
	s_nop 1
	v_permlane16_swap_b32_e32 v41, v61
	s_nop 1
	v_mov_b32_dpp v41, v61 quad_perm:[0,1,2,3] row_mask:0x5 bank_mask:0xf
	v_fma_f32 v45, -v42, v43, 1.0
	v_fmac_f32_e32 v43, v45, v43
	v_div_scale_f32 v45, vcc, v37, v40, v37
	s_waitcnt lgkmcnt(0)
	v_add_f32_e32 v33, v33, v41
	v_mov_b32_e32 v41, v33
	v_mov_b32_e32 v62, v33
	s_nop 1
	v_permlane32_swap_b32_e32 v41, v62
	s_nop 1
	v_mov_b32_dpp v41, v62 quad_perm:[0,1,2,3] row_mask:0x3 bank_mask:0xf
	v_mul_f32_e32 v65, v45, v43
	v_fma_f32 v66, -v42, v65, v45
	v_fmac_f32_e32 v65, v66, v43
	v_fma_f32 v42, -v42, v65, v45
	s_waitcnt lgkmcnt(0)
	v_add_f32_e32 v33, v33, v41
	v_fmamk_f32 v33, v33, 0x3b000000, v57
	v_mul_f32_e32 v41, 0x4f800000, v33
	v_cmp_gt_f32_e64 s[0:1], s2, v33
	v_div_fmas_f32 v42, v42, v43, v65
	v_div_fixup_f32 v37, v42, v40, v37
	v_cndmask_b32_e64 v33, v33, v41, s[0:1]
	v_sqrt_f32_e32 v41, v33
	v_mul_f32_e32 v37, v37, v39
	v_cvt_pk_bf16_f32 v37, v38, v37
	global_store_dwordx4 v[46:47], v[34:37], off offset:1024
	v_add_u32_e32 v40, -1, v41
	v_fma_f32 v42, -v40, v41, v33
	v_cmp_ge_f32_e32 vcc, 0, v42
	v_add_u32_e32 v42, 1, v41
	v_lshlrev_b32_e32 v37, 16, v24
	v_cndmask_b32_e32 v40, v41, v40, vcc
	v_fma_f32 v41, -v42, v41, v33
	v_cmp_lt_f32_e32 vcc, 0, v41
	v_and_b32_e32 v24, 0xffff0000, v24
	v_lshlrev_b32_e32 v38, 16, v25
	v_cndmask_b32_e32 v40, v40, v42, vcc
	v_mul_f32_e32 v41, 0x37800000, v40
	v_cndmask_b32_e64 v40, v40, v41, s[0:1]
	v_cmp_class_f32_e32 vcc, v33, v58
	v_and_b32_e32 v25, 0xffff0000, v25
	s_nop 0
	v_cndmask_b32_e32 v33, v40, v33, vcc
	v_div_scale_f32 v40, s[0:1], v33, v33, 1.0
	v_rcp_f32_e32 v41, v40
	s_nop 0
	v_fma_f32 v34, -v40, v41, 1.0
	v_fmac_f32_e32 v41, v34, v41
	v_div_scale_f32 v34, vcc, 1.0, v33, 1.0
	v_mul_f32_e32 v35, v34, v41
	v_fma_f32 v36, -v40, v35, v34
	v_fmac_f32_e32 v35, v36, v41
	v_fma_f32 v34, -v40, v35, v34
	v_div_fmas_f32 v34, v34, v41, v35
	v_div_fixup_f32 v33, v34, v33, 1.0
	v_lshlrev_b32_e32 v34, 16, v22
	v_mul_f32_e32 v36, 0xbfb8aa3b, v34
	v_exp_f32_e32 v36, v36
	v_mul_f32_e32 v41, v44, v33
	v_and_b32_e32 v22, 0xffff0000, v22
	v_mul_f32_e32 v41, v6, v41
	v_add_f32_e32 v36, 1.0, v36
	v_div_scale_f32 v39, s[0:1], v36, v36, v34
	v_rcp_f32_e32 v40, v39
	v_lshlrev_b32_e32 v35, 16, v23
	v_mul_f32_e32 v26, v26, v33
	v_mul_f32_e32 v26, v7, v26
	v_fma_f32 v42, -v39, v40, 1.0
	v_fmac_f32_e32 v40, v42, v40
	v_div_scale_f32 v42, vcc, v34, v36, v34
	v_mul_f32_e32 v43, v42, v40
	v_fma_f32 v44, -v39, v43, v42
	v_fmac_f32_e32 v43, v44, v40
	v_fma_f32 v39, -v39, v43, v42
	v_mul_f32_e32 v42, 0xbfb8aa3b, v22
	v_exp_f32_e32 v42, v42
	v_div_fmas_f32 v39, v39, v40, v43
	v_div_fixup_f32 v34, v39, v36, v34
	v_mul_f32_e32 v34, v34, v41
	v_add_f32_e32 v36, 1.0, v42
	v_div_scale_f32 v39, s[0:1], v36, v36, v22
	v_rcp_f32_e32 v40, v39
	v_and_b32_e32 v23, 0xffff0000, v23
	v_mul_f32_e32 v30, v30, v33
	v_mul_f32_e32 v30, v8, v30
	v_fma_f32 v41, -v39, v40, 1.0
	v_fmac_f32_e32 v40, v41, v40
	v_div_scale_f32 v41, vcc, v22, v36, v22
	v_mul_f32_e32 v42, v41, v40
	v_fma_f32 v43, -v39, v42, v41
	v_fmac_f32_e32 v42, v43, v40
	v_fma_f32 v39, -v39, v42, v41
	v_mul_f32_e32 v41, 0xbfb8aa3b, v35
	v_exp_f32_e32 v41, v41
	v_div_fmas_f32 v39, v39, v40, v42
	v_div_fixup_f32 v22, v39, v36, v22
	v_mul_f32_e32 v22, v22, v26
	v_add_f32_e32 v26, 1.0, v41
	v_div_scale_f32 v36, s[0:1], v26, v26, v35
	v_rcp_f32_e32 v39, v36
	v_cvt_pk_bf16_f32 v22, v34, v22
	v_mul_f32_e32 v27, v27, v33
	v_mul_f32_e32 v27, v9, v27
	v_fma_f32 v34, -v36, v39, 1.0
	v_fmac_f32_e32 v39, v34, v39
	v_div_scale_f32 v34, vcc, v35, v26, v35
	v_mul_f32_e32 v40, v34, v39
	v_fma_f32 v41, -v36, v40, v34
	v_fmac_f32_e32 v40, v41, v39
	v_fma_f32 v34, -v36, v40, v34
	v_mul_f32_e32 v36, 0xbfb8aa3b, v23
	v_exp_f32_e32 v36, v36
	v_div_fmas_f32 v34, v34, v39, v40
	v_div_fixup_f32 v26, v34, v26, v35
	v_mul_f32_e32 v26, v26, v30
	v_add_f32_e32 v34, 1.0, v36
	v_div_scale_f32 v35, s[0:1], v34, v34, v23
	v_rcp_f32_e32 v36, v35
	s_nop 0
	v_fma_f32 v30, -v35, v36, 1.0
	v_fmac_f32_e32 v36, v30, v36
	v_div_scale_f32 v30, vcc, v23, v34, v23
	v_mul_f32_e32 v39, v30, v36
	v_fma_f32 v40, -v35, v39, v30
	v_fmac_f32_e32 v39, v40, v36
	v_fma_f32 v30, -v35, v39, v30
	v_mul_f32_e32 v35, 0xbfb8aa3b, v37
	v_exp_f32_e32 v35, v35
	v_div_fmas_f32 v30, v30, v36, v39
	v_div_fixup_f32 v23, v30, v34, v23
	v_mul_f32_e32 v23, v23, v27
	v_add_f32_e32 v27, 1.0, v35
	v_div_scale_f32 v30, s[0:1], v27, v27, v37
	v_rcp_f32_e32 v34, v30
	v_cvt_pk_bf16_f32 v23, v26, v23
	v_mul_f32_e32 v26, v31, v33
	v_mul_f32_e32 v26, v2, v26
	v_fma_f32 v31, -v30, v34, 1.0
	v_fmac_f32_e32 v34, v31, v34
	v_div_scale_f32 v31, vcc, v37, v27, v37
	v_mul_f32_e32 v35, v31, v34
	v_fma_f32 v36, -v30, v35, v31
	v_fmac_f32_e32 v35, v36, v34
	v_fma_f32 v30, -v30, v35, v31
	v_mul_f32_e32 v31, 0xbfb8aa3b, v24
	v_exp_f32_e32 v31, v31
	v_div_fmas_f32 v30, v30, v34, v35
	v_div_fixup_f32 v27, v30, v27, v37
	v_mul_f32_e32 v26, v27, v26
	v_add_f32_e32 v30, 1.0, v31
	v_div_scale_f32 v31, s[0:1], v30, v30, v24
	v_rcp_f32_e32 v34, v31
	v_mul_f32_e32 v27, v28, v33
	v_mul_f32_e32 v27, v3, v27
	v_fma_f32 v28, -v31, v34, 1.0
	v_fmac_f32_e32 v34, v28, v34
	v_div_scale_f32 v28, vcc, v24, v30, v24
	v_mul_f32_e32 v35, v28, v34
	v_fma_f32 v36, -v31, v35, v28
	v_fmac_f32_e32 v35, v36, v34
	v_fma_f32 v28, -v31, v35, v28
	v_div_fmas_f32 v28, v28, v34, v35
	v_div_fixup_f32 v24, v28, v30, v24
	v_mul_f32_e32 v24, v24, v27
	v_cvt_pk_bf16_f32 v24, v26, v24
	v_mul_f32_e32 v26, v32, v33
	v_lshlrev_b32_e32 v32, 16, v14
	v_lshlrev_b32_e32 v34, 16, v18
	v_and_b32_e32 v18, 0xffff0000, v18
	v_and_b32_e32 v14, 0xffff0000, v14
	v_add_f32_e32 v32, v34, v32
	v_add_f32_e32 v14, v18, v14
	v_lshlrev_b32_e32 v18, 16, v15
	v_lshlrev_b32_e32 v34, 16, v19
	v_and_b32_e32 v19, 0xffff0000, v19
	v_and_b32_e32 v15, 0xffff0000, v15
	v_mul_f32_e32 v31, 0xbfb8aa3b, v38
	v_add_f32_e32 v18, v34, v18
	v_add_f32_e32 v15, v19, v15
	v_lshlrev_b32_e32 v19, 16, v16
	v_lshlrev_b32_e32 v34, 16, v20
	v_and_b32_e32 v20, 0xffff0000, v20
	v_and_b32_e32 v16, 0xffff0000, v16
	v_exp_f32_e32 v31, v31
	v_add_f32_e32 v19, v34, v19
	v_add_f32_e32 v16, v20, v16
	v_lshlrev_b32_e32 v20, 16, v17
	v_lshlrev_b32_e32 v34, 16, v21
	v_and_b32_e32 v21, 0xffff0000, v21
	v_and_b32_e32 v17, 0xffff0000, v17
	v_add_f32_e32 v17, v21, v17
	v_mul_f32_e32 v21, v32, v32
	v_fmac_f32_e32 v21, v14, v14
	v_fmac_f32_e32 v21, v18, v18
	v_add_f32_e32 v27, 1.0, v31
	v_fmac_f32_e32 v21, v15, v15
	v_div_scale_f32 v28, s[0:1], v27, v27, v38
	v_fmac_f32_e32 v21, v19, v19
	v_rcp_f32_e32 v30, v28
	v_add_f32_e32 v20, v34, v20
	v_fmac_f32_e32 v21, v16, v16
	v_fmac_f32_e32 v21, v20, v20
	v_fmac_f32_e32 v21, v17, v17
	s_nop 1
	v_mov_b32_dpp v34, v21 quad_perm:[1,0,3,2] row_mask:0xf bank_mask:0xf
	v_fma_f32 v31, -v28, v30, 1.0
	v_fmac_f32_e32 v30, v31, v30
	v_div_scale_f32 v31, vcc, v38, v27, v38
	v_mul_f32_e32 v35, v31, v30
	v_fma_f32 v36, -v28, v35, v31
	v_fmac_f32_e32 v35, v36, v30
	s_waitcnt lgkmcnt(0)
	v_add_f32_e32 v21, v21, v34
	v_fma_f32 v28, -v28, v35, v31
	s_nop 1
	v_mov_b32_dpp v31, v21 quad_perm:[2,3,0,1] row_mask:0xf bank_mask:0xf
	v_div_fmas_f32 v28, v28, v30, v35
	v_mul_f32_e32 v26, v4, v26
	v_div_fixup_f32 v27, v28, v27, v38
	v_mul_f32_e32 v26, v27, v26
	s_waitcnt lgkmcnt(0)
	v_add_f32_e32 v21, v21, v31
	s_nop 1
	v_mov_b32_dpp v31, v21 row_half_mirror row_mask:0xf bank_mask:0xf
	v_mul_f32_e32 v27, v29, v33
	v_mul_f32_e32 v30, 0xbfb8aa3b, v25
	v_exp_f32_e32 v30, v30
	v_mul_f32_e32 v27, v5, v27
	s_waitcnt lgkmcnt(0)
	v_add_f32_e32 v21, v21, v31
	s_nop 1
	v_mov_b32_dpp v29, v21 row_mirror row_mask:0xf bank_mask:0xf
	v_add_f32_e32 v28, 1.0, v30
	v_div_scale_f32 v30, s[0:1], v28, v28, v25
	v_rcp_f32_e32 v31, v30
	s_waitcnt lgkmcnt(0)
	v_add_f32_e32 v21, v21, v29
	v_mov_b32_e32 v29, v21
	v_mov_b32_e32 v61, v21
	s_nop 1
	v_permlane16_swap_b32_e32 v29, v61
	s_nop 1
	v_mov_b32_dpp v29, v61 quad_perm:[0,1,2,3] row_mask:0x5 bank_mask:0xf
	v_fma_f32 v33, -v30, v31, 1.0
	v_fmac_f32_e32 v31, v33, v31
	v_div_scale_f32 v33, vcc, v25, v28, v25
	s_waitcnt lgkmcnt(0)
	v_add_f32_e32 v21, v21, v29
	v_mov_b32_e32 v29, v21
	v_mov_b32_e32 v62, v21
	s_nop 1
	v_permlane32_swap_b32_e32 v29, v62
	s_nop 1
	v_mov_b32_dpp v29, v62 quad_perm:[0,1,2,3] row_mask:0x3 bank_mask:0xf
	v_mul_f32_e32 v34, v33, v31
	v_fma_f32 v35, -v30, v34, v33
	v_fmac_f32_e32 v34, v35, v31
	v_fma_f32 v30, -v30, v34, v33
	s_waitcnt lgkmcnt(0)
	v_add_f32_e32 v21, v21, v29
	v_fmamk_f32 v21, v21, 0x3b000000, v57
	v_mul_f32_e32 v29, 0x4f800000, v21
	v_cmp_gt_f32_e64 s[0:1], s2, v21
	v_div_fmas_f32 v30, v30, v31, v34
	v_div_fixup_f32 v25, v30, v28, v25
	v_cndmask_b32_e64 v21, v21, v29, s[0:1]
	v_sqrt_f32_e32 v29, v21
	v_mul_f32_e32 v25, v25, v27
	v_cvt_pk_bf16_f32 v25, v26, v25
	global_store_dwordx4 v[46:47], v[22:25], off offset:2048
	v_add_u32_e32 v28, -1, v29
	v_fma_f32 v30, -v28, v29, v21
	v_cmp_ge_f32_e32 vcc, 0, v30
	v_add_u32_e32 v30, 1, v29
	v_lshlrev_b32_e32 v25, 16, v12
	v_cndmask_b32_e32 v28, v29, v28, vcc
	v_fma_f32 v29, -v30, v29, v21
	v_cmp_lt_f32_e32 vcc, 0, v29
	v_and_b32_e32 v12, 0xffff0000, v12
	v_lshlrev_b32_e32 v26, 16, v13
	v_cndmask_b32_e32 v28, v28, v30, vcc
	v_mul_f32_e32 v29, 0x37800000, v28
	v_cndmask_b32_e64 v28, v28, v29, s[0:1]
	v_cmp_class_f32_e32 vcc, v21, v58
	v_and_b32_e32 v13, 0xffff0000, v13
	s_nop 0
	v_cndmask_b32_e32 v21, v28, v21, vcc
	v_div_scale_f32 v28, s[0:1], v21, v21, 1.0
	v_rcp_f32_e32 v29, v28
	s_nop 0
	v_fma_f32 v22, -v28, v29, 1.0
	v_fmac_f32_e32 v29, v22, v29
	v_div_scale_f32 v22, vcc, 1.0, v21, 1.0
	v_mul_f32_e32 v23, v22, v29
	v_fma_f32 v24, -v28, v23, v22
	v_fmac_f32_e32 v23, v24, v29
	v_fma_f32 v22, -v28, v23, v22
	v_div_fmas_f32 v22, v22, v29, v23
	v_div_fixup_f32 v21, v22, v21, 1.0
	v_lshlrev_b32_e32 v22, 16, v10
	v_mul_f32_e32 v24, 0xbfb8aa3b, v22
	v_exp_f32_e32 v24, v24
	v_mul_f32_e32 v29, v32, v21
	v_mul_f32_e32 v6, v6, v29
	v_and_b32_e32 v10, 0xffff0000, v10
	v_add_f32_e32 v24, 1.0, v24
	v_div_scale_f32 v27, s[0:1], v24, v24, v22
	v_rcp_f32_e32 v28, v27
	v_mul_f32_e32 v14, v14, v21
	v_mul_f32_e32 v7, v7, v14
	v_lshlrev_b32_e32 v23, 16, v11
	v_fma_f32 v29, -v27, v28, 1.0
	v_fmac_f32_e32 v28, v29, v28
	v_div_scale_f32 v29, vcc, v22, v24, v22
	v_mul_f32_e32 v30, v29, v28
	v_fma_f32 v31, -v27, v30, v29
	v_fmac_f32_e32 v30, v31, v28
	v_fma_f32 v27, -v27, v30, v29
	v_mul_f32_e32 v29, 0xbfb8aa3b, v10
	v_exp_f32_e32 v29, v29
	v_div_fmas_f32 v27, v27, v28, v30
	v_div_fixup_f32 v22, v27, v24, v22
	v_mul_f32_e32 v6, v22, v6
	v_add_f32_e32 v24, 1.0, v29
	v_div_scale_f32 v27, s[0:1], v24, v24, v10
	v_rcp_f32_e32 v28, v27
	v_and_b32_e32 v11, 0xffff0000, v11
	v_fma_f32 v14, -v27, v28, 1.0
	v_fmac_f32_e32 v28, v14, v28
	v_div_scale_f32 v14, vcc, v10, v24, v10
	v_mul_f32_e32 v22, v14, v28
	v_fma_f32 v29, -v27, v22, v14
	v_fmac_f32_e32 v22, v29, v28
	v_fma_f32 v14, -v27, v22, v14
	v_mul_f32_e32 v27, 0xbfb8aa3b, v23
	v_exp_f32_e32 v27, v27
	v_div_fmas_f32 v14, v14, v28, v22
	v_div_fixup_f32 v10, v14, v24, v10
	v_mul_f32_e32 v7, v10, v7
	v_add_f32_e32 v10, 1.0, v27
	v_div_scale_f32 v14, s[0:1], v10, v10, v23
	v_rcp_f32_e32 v22, v14
	v_cvt_pk_bf16_f32 v6, v6, v7
	v_mul_f32_e32 v7, v18, v21
	v_mul_f32_e32 v7, v8, v7
	v_fma_f32 v8, -v14, v22, 1.0
	v_fmac_f32_e32 v22, v8, v22
	v_div_scale_f32 v8, vcc, v23, v10, v23
	v_mul_f32_e32 v18, v8, v22
	v_fma_f32 v24, -v14, v18, v8
	v_fmac_f32_e32 v18, v24, v22
	v_fma_f32 v8, -v14, v18, v8
	v_mul_f32_e32 v14, 0xbfb8aa3b, v11
	v_exp_f32_e32 v14, v14
	v_div_fmas_f32 v8, v8, v22, v18
	v_div_fixup_f32 v8, v8, v10, v23
	v_mul_f32_e32 v7, v8, v7
	v_add_f32_e32 v10, 1.0, v14
	v_div_scale_f32 v14, s[0:1], v10, v10, v11
	v_rcp_f32_e32 v18, v14
	v_mul_f32_e32 v8, v15, v21
	v_mul_f32_e32 v8, v9, v8
	v_fma_f32 v9, -v14, v18, 1.0
	v_fmac_f32_e32 v18, v9, v18
	v_div_scale_f32 v9, vcc, v11, v10, v11
	v_mul_f32_e32 v15, v9, v18
	v_fma_f32 v22, -v14, v15, v9
	v_fmac_f32_e32 v15, v22, v18
	v_fma_f32 v9, -v14, v15, v9
	v_mul_f32_e32 v14, 0xbfb8aa3b, v25
	v_exp_f32_e32 v14, v14
	v_div_fmas_f32 v9, v9, v18, v15
	v_div_fixup_f32 v9, v9, v10, v11
	v_mul_f32_e32 v8, v9, v8
	v_add_f32_e32 v9, 1.0, v14
	v_div_scale_f32 v10, s[0:1], v9, v9, v25
	v_rcp_f32_e32 v11, v10
	v_cvt_pk_bf16_f32 v7, v7, v8
	v_mul_f32_e32 v8, v19, v21
	v_mul_f32_e32 v2, v2, v8
	v_fma_f32 v8, -v10, v11, 1.0
	v_fmac_f32_e32 v11, v8, v11
	v_div_scale_f32 v8, vcc, v25, v9, v25
	v_mul_f32_e32 v14, v8, v11
	v_fma_f32 v15, -v10, v14, v8
	v_fmac_f32_e32 v14, v15, v11
	v_fma_f32 v8, -v10, v14, v8
	v_mul_f32_e32 v10, 0xbfb8aa3b, v12
	v_exp_f32_e32 v10, v10
	v_div_fmas_f32 v8, v8, v11, v14
	v_div_fixup_f32 v8, v8, v9, v25
	v_mul_f32_e32 v2, v8, v2
	v_add_f32_e32 v9, 1.0, v10
	v_div_scale_f32 v10, s[0:1], v9, v9, v12
	v_rcp_f32_e32 v11, v10
	v_mul_f32_e32 v8, v16, v21
	v_mul_f32_e32 v3, v3, v8
	v_fma_f32 v8, -v10, v11, 1.0
	v_fmac_f32_e32 v11, v8, v11
	v_div_scale_f32 v8, vcc, v12, v9, v12
	v_mul_f32_e32 v14, v8, v11
	v_fma_f32 v15, -v10, v14, v8
	v_fmac_f32_e32 v14, v15, v11
	v_fma_f32 v8, -v10, v14, v8
	v_mul_f32_e32 v10, 0xbfb8aa3b, v26
	v_exp_f32_e32 v10, v10
	v_div_fmas_f32 v8, v8, v11, v14
	v_div_fixup_f32 v8, v8, v9, v12
	v_mul_f32_e32 v3, v8, v3
	v_add_f32_e32 v9, 1.0, v10
	v_div_scale_f32 v10, s[0:1], v9, v9, v26
	v_rcp_f32_e32 v11, v10
	v_cvt_pk_bf16_f32 v8, v2, v3
	v_mul_f32_e32 v2, v20, v21
	v_mul_f32_e32 v2, v4, v2
	v_fma_f32 v3, -v10, v11, 1.0
	v_fmac_f32_e32 v11, v3, v11
	v_div_scale_f32 v3, vcc, v26, v9, v26
	v_mul_f32_e32 v4, v3, v11
	v_fma_f32 v12, -v10, v4, v3
	v_fmac_f32_e32 v4, v12, v11
	v_fma_f32 v3, -v10, v4, v3
	v_mul_f32_e32 v10, 0xbfb8aa3b, v13
	v_exp_f32_e32 v10, v10
	v_div_fmas_f32 v3, v3, v11, v4
	v_div_fixup_f32 v3, v3, v9, v26
	v_mul_f32_e32 v2, v3, v2
	v_add_f32_e32 v4, 1.0, v10
	v_div_scale_f32 v9, s[0:1], v4, v4, v13
	v_rcp_f32_e32 v10, v9
	v_mul_f32_e32 v3, v17, v21
	v_mul_f32_e32 v3, v5, v3
	v_fma_f32 v5, -v9, v10, 1.0
	v_fmac_f32_e32 v10, v5, v10
	v_div_scale_f32 v5, vcc, v13, v4, v13
	v_mul_f32_e32 v11, v5, v10
	v_fma_f32 v12, -v9, v11, v5
	v_fmac_f32_e32 v11, v12, v10
	v_fma_f32 v5, -v9, v11, v5
	v_div_fmas_f32 v5, v5, v10, v11
	v_div_fixup_f32 v4, v5, v4, v13
	v_mul_f32_e32 v3, v4, v3
	v_cvt_pk_bf16_f32 v9, v2, v3
	global_store_dwordx4 v[46:47], v[6:9], off offset:3072
	s_cbranch_scc1 .LBB0_817

.LBB0_966:
	s_ashr_i32 s15, s14, 31
	s_add_i32 s0, s14, 8
	s_lshl_b64 s[16:17], s[14:15], 13
	s_add_u32 s88, s68, s16
	s_addc_u32 s89, s69, s17
	s_ashr_i32 s1, s0, 31
	s_lshl_b64 s[52:53], s[0:1], 13
	s_add_u32 s96, s68, s52
	s_addc_u32 s97, s69, s53
	s_lshl_b64 s[54:55], s[14:15], 12
	v_mov_b32_e32 v50, v164
	s_add_u32 vcc_lo, s49, s54
	s_addc_u32 vcc_hi, s50, s55
	s_lshl_b64 s[56:57], s[0:1], 12
	v_ashrrev_i32_e32 v51, 31, v50
	s_add_u32 s0, s49, s56
	v_lshlrev_b64 v[44:45], 2, v[50:51]
	s_addc_u32 s1, s50, s57
	v_lshl_add_u64 v[2:3], s[88:89], 0, v[44:45]
	v_lshlrev_b64 v[42:43], 1, v[50:51]
	v_lshl_add_u64 v[4:5], s[96:97], 0, v[44:45]
	v_lshl_add_u64 v[52:53], vcc, 0, v[42:43]
	v_lshl_add_u64 v[54:55], s[0:1], 0, v[42:43]
	global_load_dwordx4 v[46:49], v[2:3], off nt
	global_load_dwordx4 v[56:59], v[2:3], off offset:1024 nt
	global_load_dwordx4 v[60:63], v[4:5], off nt
	global_load_dwordx4 v[64:67], v[4:5], off offset:1024 nt
	global_load_dwordx4 v[92:95], v[2:3], off offset:2048 nt
	global_load_dwordx4 v[38:41], v[2:3], off offset:3072 nt
	global_load_dwordx4 v[96:99], v[4:5], off offset:2048 nt
	global_load_dwordx4 v[26:29], v[4:5], off offset:3072 nt
	global_load_dwordx2 v[68:69], v[52:53], off nt
	global_load_dwordx2 v[104:105], v[52:53], off offset:512 nt
	global_load_dwordx2 v[106:107], v[52:53], off offset:1024 nt
	global_load_dwordx2 v[72:73], v[52:53], off offset:1536 nt
	global_load_dwordx2 v[108:109], v[54:55], off nt
	global_load_dwordx2 v[110:111], v[54:55], off offset:512 nt
	global_load_dwordx2 v[112:113], v[54:55], off offset:1024 nt
	global_load_dwordx2 v[70:71], v[54:55], off offset:1536 nt
	v_add_co_u32_e32 v2, vcc, s74, v2
	s_nop 1
	v_addc_co_u32_e32 v3, vcc, 0, v3, vcc
	v_add_co_u32_e32 v4, vcc, s74, v4
	s_nop 1
	v_addc_co_u32_e32 v5, vcc, 0, v5, vcc
	global_load_dwordx4 v[34:37], v[2:3], off nt
	global_load_dwordx4 v[22:25], v[2:3], off offset:1024 nt
	global_load_dwordx4 v[30:33], v[4:5], off nt
	global_load_dwordx4 v[18:21], v[4:5], off offset:1024 nt
	global_load_dwordx4 v[14:17], v[2:3], off offset:2048 nt
	global_load_dwordx4 v[6:9], v[2:3], off offset:3072 nt
	global_load_dwordx4 v[10:13], v[4:5], off offset:2048 nt
	s_nop 0
	global_load_dwordx4 v[2:5], v[4:5], off offset:3072 nt
	s_nop 0
	global_load_dwordx2 v[88:89], v[52:53], off offset:2048 nt
	global_load_dwordx2 v[84:85], v[52:53], off offset:2560 nt
	global_load_dwordx2 v[80:81], v[52:53], off offset:3072 nt
	global_load_dwordx2 v[76:77], v[52:53], off offset:3584 nt
	global_load_dwordx2 v[86:87], v[54:55], off offset:2048 nt
	global_load_dwordx2 v[82:83], v[54:55], off offset:2560 nt
	global_load_dwordx2 v[78:79], v[54:55], off offset:3072 nt
	global_load_dwordx2 v[74:75], v[54:55], off offset:3584 nt
	v_lshl_add_u32 v90, v50, 2, 0
	v_add_u32_e32 v91, 0x14800, v90
	ds_read_b128 v[100:103], v91
	s_waitcnt vmcnt(23)
	v_lshlrev_b32_e32 v50, 16, v68
	v_and_b32_e32 v51, 0xffff0000, v68
	v_lshlrev_b32_e32 v52, 16, v69
	v_and_b32_e32 v53, 0xffff0000, v69
	s_waitcnt lgkmcnt(0)
	v_pk_mul_f32 v[52:53], v[102:103], v[52:53]
	v_pk_mul_f32 v[50:51], v[100:101], v[50:51]
	v_pk_fma_f32 v[48:49], v[48:49], s[44:45], v[52:53] op_sel_hi:[1,0,1]
	v_pk_fma_f32 v[52:53], v[46:47], s[44:45], v[50:51] op_sel_hi:[1,0,1]
	s_waitcnt vmcnt(19)
	v_lshlrev_b32_e32 v46, 16, v108
	v_and_b32_e32 v47, 0xffff0000, v108
	v_lshlrev_b32_e32 v50, 16, v109
	v_and_b32_e32 v51, 0xffff0000, v109
	v_pk_mul_f32 v[50:51], v[102:103], v[50:51]
	v_pk_mul_f32 v[54:55], v[100:101], v[46:47]
	v_pk_fma_f32 v[46:47], v[62:63], s[44:45], v[50:51] op_sel_hi:[1,0,1]
	v_pk_fma_f32 v[50:51], v[60:61], s[44:45], v[54:55] op_sel_hi:[1,0,1]
	ds_read_b128 v[60:63], v91 offset:1024
	v_lshlrev_b32_e32 v68, 16, v105
	v_and_b32_e32 v69, 0xffff0000, v105
	v_lshlrev_b32_e32 v54, 16, v104
	v_and_b32_e32 v55, 0xffff0000, v104
	s_waitcnt lgkmcnt(0)
	v_pk_mul_f32 v[68:69], v[62:63], v[68:69]
	v_pk_mul_f32 v[100:101], v[60:61], v[54:55]
	v_pk_fma_f32 v[54:55], v[58:59], s[44:45], v[68:69] op_sel_hi:[1,0,1]
	s_waitcnt vmcnt(18)
	v_lshlrev_b32_e32 v58, 16, v110
	v_and_b32_e32 v59, 0xffff0000, v110
	v_pk_fma_f32 v[56:57], v[56:57], s[44:45], v[100:101] op_sel_hi:[1,0,1]
	v_lshlrev_b32_e32 v68, 16, v111
	v_and_b32_e32 v69, 0xffff0000, v111
	v_pk_mul_f32 v[58:59], v[60:61], v[58:59]
	v_pk_mul_f32 v[62:63], v[62:63], v[68:69]
	v_pk_fma_f32 v[68:69], v[64:65], s[44:45], v[58:59] op_sel_hi:[1,0,1]
	v_mov_b32_e32 v58, v52
	v_mov_b32_e32 v59, v56
	v_mov_b32_e32 v60, v53
	v_mov_b32_e32 v61, v57
	v_pk_fma_f32 v[66:67], v[66:67], s[44:45], v[62:63] op_sel_hi:[1,0,1]
	v_pk_add_f32 v[58:59], v[58:59], v[60:61]
	v_mov_b32_e32 v60, v49
	v_mov_b32_e32 v61, v55
	v_mov_b32_e32 v62, v48
	v_mov_b32_e32 v63, v54
	v_pk_add_f32 v[60:61], v[60:61], v[62:63]
	v_mov_b32_e32 v62, v47
	v_pk_add_f32 v[58:59], v[58:59], v[60:61]
	v_mov_b32_e32 v60, v51
	v_add_f32_e32 v58, 0, v58
	v_add_f32_e32 v100, v58, v59
	v_mov_b32_e32 v58, v50
	v_mov_b32_e32 v59, v68
	v_mov_b32_e32 v61, v69
	v_pk_add_f32 v[58:59], v[58:59], v[60:61]
	v_mov_b32_e32 v60, v46
	v_mov_b32_e32 v61, v66
	v_mov_b32_e32 v63, v67
	v_pk_add_f32 v[60:61], v[60:61], v[62:63]
	v_lshlrev_b32_e32 v62, 16, v106
	v_pk_add_f32 v[58:59], v[58:59], v[60:61]
	v_and_b32_e32 v63, 0xffff0000, v106
	v_add_f32_e32 v58, 0, v58
	v_add_f32_e32 v102, v58, v59
	ds_read_b128 v[58:61], v91 offset:2048
	v_lshlrev_b32_e32 v64, 16, v107
	v_and_b32_e32 v65, 0xffff0000, v107
	v_lshlrev_b32_e32 v104, 16, v72
	v_and_b32_e32 v105, 0xffff0000, v72
	s_waitcnt lgkmcnt(0)
	v_pk_mul_f32 v[64:65], v[60:61], v[64:65]
	v_pk_mul_f32 v[62:63], v[58:59], v[62:63]
	v_pk_fma_f32 v[64:65], v[94:95], s[44:45], v[64:65] op_sel_hi:[1,0,1]
	v_pk_fma_f32 v[62:63], v[92:93], s[44:45], v[62:63] op_sel_hi:[1,0,1]
	s_waitcnt vmcnt(17)
	v_lshlrev_b32_e32 v92, 16, v112
	v_and_b32_e32 v93, 0xffff0000, v112
	v_lshlrev_b32_e32 v94, 16, v113
	v_and_b32_e32 v95, 0xffff0000, v113
	v_pk_mul_f32 v[60:61], v[60:61], v[94:95]
	v_pk_mul_f32 v[58:59], v[58:59], v[92:93]
	v_mov_b32_e32 v92, v62
	v_mov_b32_e32 v93, v65
	v_pk_mov_b32 v[94:95], v[62:63], v[64:65] op_sel:[1,0]
	v_pk_fma_f32 v[60:61], v[98:99], s[44:45], v[60:61] op_sel_hi:[1,0,1]
	v_pk_fma_f32 v[58:59], v[96:97], s[44:45], v[58:59] op_sel_hi:[1,0,1]
	v_pk_add_f32 v[92:93], v[92:93], v[94:95]
	v_mov_b32_e32 v94, v58
	v_pk_add_f32 v[96:97], v[92:93], v[92:93] op_sel:[0,1] op_sel_hi:[1,0]
	v_pk_mov_b32 v[92:93], v[58:59], v[60:61] op_sel:[1,0]
	v_mov_b32_e32 v95, v61
	v_pk_add_f32 v[92:93], v[92:93], v[94:95]
	v_lshlrev_b32_e32 v72, 16, v73
	v_pk_add_f32 v[98:99], v[92:93], v[92:93] op_sel:[0,1] op_sel_hi:[1,0]
	ds_read_b128 v[92:95], v91 offset:3072
	v_and_b32_e32 v73, 0xffff0000, v73
	s_waitcnt vmcnt(7)
	v_lshlrev_b32_e32 v108, 16, v88
	v_and_b32_e32 v109, 0xffff0000, v88
	v_lshlrev_b32_e32 v88, 16, v89
	s_waitcnt lgkmcnt(0)
	v_pk_mul_f32 v[72:73], v[94:95], v[72:73]
	v_pk_mul_f32 v[104:105], v[92:93], v[104:105]
	v_pk_fma_f32 v[40:41], v[40:41], s[44:45], v[72:73] op_sel_hi:[1,0,1]
	v_lshlrev_b32_e32 v72, 16, v70
	v_and_b32_e32 v73, 0xffff0000, v70
	v_lshlrev_b32_e32 v70, 16, v71
	v_and_b32_e32 v71, 0xffff0000, v71
	v_pk_mul_f32 v[70:71], v[94:95], v[70:71]
	v_pk_mul_f32 v[92:93], v[92:93], v[72:73]
	v_pk_fma_f32 v[72:73], v[28:29], s[44:45], v[70:71] op_sel_hi:[1,0,1]
	v_pk_fma_f32 v[70:71], v[26:27], s[44:45], v[92:93] op_sel_hi:[1,0,1]
	ds_read_b128 v[26:29], v91 offset:4096
	v_and_b32_e32 v89, 0xffff0000, v89
	v_pk_fma_f32 v[38:39], v[38:39], s[44:45], v[104:105] op_sel_hi:[1,0,1]
	v_add_f32_e32 v94, v41, v40
	v_add_f32_e32 v92, v38, v39
	s_waitcnt lgkmcnt(0)
	v_pk_mul_f32 v[88:89], v[28:29], v[88:89]
	v_pk_mul_f32 v[108:109], v[26:27], v[108:109]
	v_pk_fma_f32 v[36:37], v[36:37], s[44:45], v[88:89] op_sel_hi:[1,0,1]
	v_pk_fma_f32 v[34:35], v[34:35], s[44:45], v[108:109] op_sel_hi:[1,0,1]
	s_waitcnt vmcnt(3)
	v_lshlrev_b32_e32 v88, 16, v86
	v_and_b32_e32 v89, 0xffff0000, v86
	v_lshlrev_b32_e32 v86, 16, v87
	v_and_b32_e32 v87, 0xffff0000, v87
	v_pk_mul_f32 v[28:29], v[28:29], v[86:87]
	v_pk_mul_f32 v[26:27], v[26:27], v[88:89]
	v_mov_b32_e32 v101, v34
	v_mov_b32_e32 v97, v35
	v_mov_b32_e32 v93, v37
	v_mov_b32_e32 v95, v36
	v_pk_fma_f32 v[28:29], v[32:33], s[44:45], v[28:29] op_sel_hi:[1,0,1]
	v_pk_fma_f32 v[26:27], v[30:31], s[44:45], v[26:27] op_sel_hi:[1,0,1]
	v_pk_add_f32 v[30:31], v[100:101], v[96:97]
	v_pk_add_f32 v[32:33], v[92:93], v[94:95]
	v_add_f32_e32 v104, v70, v71
	v_add_f32_e32 v106, v72, v73
	v_pk_add_f32 v[30:31], v[30:31], v[32:33]
	v_mov_b32_e32 v103, v26
	v_mov_b32_e32 v99, v27
	v_mov_b32_e32 v105, v28
	v_mov_b32_e32 v107, v29
	v_pk_add_f32 v[32:33], v[30:31], v[30:31] op_sel:[0,1] op_sel_hi:[1,0]
	v_pk_add_f32 v[30:31], v[102:103], v[98:99]
	v_pk_add_f32 v[86:87], v[104:105], v[106:107]
	v_lshlrev_b32_e32 v92, 16, v84
	v_pk_add_f32 v[30:31], v[30:31], v[86:87]
	ds_read_b128 v[86:89], v91 offset:5120
	v_and_b32_e32 v93, 0xffff0000, v84
	v_lshlrev_b32_e32 v84, 16, v85
	v_and_b32_e32 v85, 0xffff0000, v85
	v_lshlrev_b32_e32 v96, 16, v76
	s_waitcnt lgkmcnt(0)
	v_pk_mul_f32 v[84:85], v[88:89], v[84:85]
	v_pk_mul_f32 v[92:93], v[86:87], v[92:93]
	v_pk_fma_f32 v[24:25], v[24:25], s[44:45], v[84:85] op_sel_hi:[1,0,1]
	s_waitcnt vmcnt(2)
	v_lshlrev_b32_e32 v84, 16, v82
	v_and_b32_e32 v85, 0xffff0000, v82
	v_lshlrev_b32_e32 v82, 16, v83
	v_and_b32_e32 v83, 0xffff0000, v83
	v_pk_fma_f32 v[22:23], v[22:23], s[44:45], v[92:93] op_sel_hi:[1,0,1]
	v_pk_mul_f32 v[82:83], v[88:89], v[82:83]
	v_pk_mul_f32 v[84:85], v[86:87], v[84:85]
	v_pk_fma_f32 v[20:21], v[20:21], s[44:45], v[82:83] op_sel_hi:[1,0,1]
	v_pk_fma_f32 v[18:19], v[18:19], s[44:45], v[84:85] op_sel_hi:[1,0,1]
	v_mov_b32_e32 v82, v22
	v_mov_b32_e32 v83, v25
	v_pk_mov_b32 v[84:85], v[22:23], v[24:25] op_sel:[1,0]
	v_lshlrev_b32_e32 v92, 16, v80
	v_pk_add_f32 v[82:83], v[82:83], v[84:85]
	v_mov_b32_e32 v84, v18
	v_pk_add_f32 v[86:87], v[82:83], v[82:83] op_sel:[0,1] op_sel_hi:[1,0]
	v_pk_mov_b32 v[82:83], v[18:19], v[20:21] op_sel:[1,0]
	v_mov_b32_e32 v85, v21
	v_pk_add_f32 v[82:83], v[82:83], v[84:85]
	v_and_b32_e32 v93, 0xffff0000, v80
	v_pk_add_f32 v[88:89], v[82:83], v[82:83] op_sel:[0,1] op_sel_hi:[1,0]
	ds_read_b128 v[82:85], v91 offset:6144
	v_lshlrev_b32_e32 v80, 16, v81
	v_and_b32_e32 v81, 0xffff0000, v81
	v_and_b32_e32 v97, 0xffff0000, v76
	v_lshlrev_b32_e32 v76, 16, v77
	s_waitcnt lgkmcnt(0)
	v_pk_mul_f32 v[80:81], v[84:85], v[80:81]
	v_and_b32_e32 v77, 0xffff0000, v77
	v_pk_fma_f32 v[16:17], v[16:17], s[44:45], v[80:81] op_sel_hi:[1,0,1]
	s_waitcnt vmcnt(1)
	v_lshlrev_b32_e32 v80, 16, v78
	v_and_b32_e32 v81, 0xffff0000, v78
	v_lshlrev_b32_e32 v78, 16, v79
	v_and_b32_e32 v79, 0xffff0000, v79
	v_pk_mul_f32 v[78:79], v[84:85], v[78:79]
	v_pk_mul_f32 v[80:81], v[82:83], v[80:81]
	v_pk_fma_f32 v[12:13], v[12:13], s[44:45], v[78:79] op_sel_hi:[1,0,1]
	v_pk_fma_f32 v[10:11], v[10:11], s[44:45], v[80:81] op_sel_hi:[1,0,1]
	ds_read_b128 v[78:81], v91 offset:7168
	v_pk_mul_f32 v[92:93], v[82:83], v[92:93]
	v_add_f32_e32 v84, v17, v16
	v_pk_fma_f32 v[14:15], v[14:15], s[44:45], v[92:93] op_sel_hi:[1,0,1]
	v_pk_add_f32 v[30:31], v[30:31], v[30:31] op_sel:[0,1] op_sel_hi:[1,0]
	s_waitcnt lgkmcnt(0)
	v_pk_mul_f32 v[76:77], v[80:81], v[76:77]
	v_pk_mul_f32 v[96:97], v[78:79], v[96:97]
	v_pk_fma_f32 v[8:9], v[8:9], s[44:45], v[76:77] op_sel_hi:[1,0,1]
	v_pk_fma_f32 v[6:7], v[6:7], s[44:45], v[96:97] op_sel_hi:[1,0,1]
	s_waitcnt vmcnt(0)
	v_lshlrev_b32_e32 v76, 16, v74
	v_and_b32_e32 v77, 0xffff0000, v74
	v_lshlrev_b32_e32 v74, 16, v75
	v_and_b32_e32 v75, 0xffff0000, v75
	v_add_f32_e32 v82, v14, v15
	v_pk_mul_f32 v[74:75], v[80:81], v[74:75]
	v_pk_mul_f32 v[76:77], v[78:79], v[76:77]
	v_mov_b32_e32 v33, v6
	v_mov_b32_e32 v87, v7
	v_mov_b32_e32 v83, v9
	v_mov_b32_e32 v85, v8
	v_pk_fma_f32 v[4:5], v[4:5], s[44:45], v[74:75] op_sel_hi:[1,0,1]
	v_pk_fma_f32 v[2:3], v[2:3], s[44:45], v[76:77] op_sel_hi:[1,0,1]
	v_pk_add_f32 v[32:33], v[32:33], v[86:87]
	v_pk_add_f32 v[74:75], v[82:83], v[84:85]
	v_add_f32_e32 v92, v10, v11
	v_add_f32_e32 v94, v12, v13
	v_pk_add_f32 v[32:33], v[32:33], v[74:75]
	v_mov_b32_e32 v31, v2
	v_mov_b32_e32 v89, v3
	v_mov_b32_e32 v93, v4
	v_mov_b32_e32 v95, v5
	v_add_f32_e32 v74, v32, v33
	v_pk_add_f32 v[30:31], v[30:31], v[88:89]
	v_pk_add_f32 v[32:33], v[92:93], v[94:95]
	v_and_b32_e32 v126, 64, v192
	v_pk_add_f32 v[30:31], v[30:31], v[32:33]
	v_xor_b32_e32 v32, 1, v192
	v_add_f32_e32 v30, v30, v31
	v_add_u32_e32 v31, 64, v126
	v_cmp_lt_i32_e32 vcc, v32, v31
	v_xor_b32_e32 v33, 2, v192
	v_add_u32_e32 v98, 0x1a800, v90
	v_cndmask_b32_e32 v32, v192, v32, vcc
	v_lshlrev_b32_e32 v144, 2, v32
	s_nop 1
	v_mov_b32_dpp v32, v74 quad_perm:[1,0,3,2] row_mask:0xf bank_mask:0xf
	v_cmp_lt_i32_e32 vcc, v33, v31
	v_add_u32_e32 v99, 0x1c800, v90
	s_waitcnt lgkmcnt(0)
	v_add_f32_e32 v32, v74, v32
	v_cndmask_b32_e32 v33, v192, v33, vcc
	v_lshlrev_b32_e32 v194, 2, v33
	s_nop 1
	v_mov_b32_dpp v33, v32 quad_perm:[2,3,0,1] row_mask:0xf bank_mask:0xf
	s_waitcnt lgkmcnt(0)
	v_add_f32_e32 v32, v32, v33
	v_xor_b32_e32 v33, 4, v192
	v_cmp_lt_i32_e32 vcc, v33, v31
	s_nop 1
	v_cndmask_b32_e32 v33, v192, v33, vcc
	v_lshlrev_b32_e32 v195, 2, v33
	s_nop 1
	v_mov_b32_dpp v33, v32 row_half_mirror row_mask:0xf bank_mask:0xf
	s_waitcnt lgkmcnt(0)
	v_add_f32_e32 v32, v32, v33
	v_xor_b32_e32 v33, 8, v192
	v_cmp_lt_i32_e32 vcc, v33, v31
	s_nop 1
	v_cndmask_b32_e32 v33, v192, v33, vcc
	v_lshlrev_b32_e32 v196, 2, v33
	s_nop 1
	v_mov_b32_dpp v33, v32 row_mirror row_mask:0xf bank_mask:0xf
	s_waitcnt lgkmcnt(0)
	v_add_f32_e32 v32, v32, v33
	v_xor_b32_e32 v33, 16, v192
	v_cmp_lt_i32_e32 vcc, v33, v31
	s_nop 1
	v_cndmask_b32_e32 v33, v192, v33, vcc
	v_lshlrev_b32_e32 v197, 2, v33
	v_mov_b32_e32 v33, v32
	v_mov_b32_e32 v197, v32
	s_nop 1
	v_permlane16_swap_b32_e32 v33, v197
	s_nop 1
	v_mov_b32_dpp v33, v197 quad_perm:[0,1,2,3] row_mask:0x5 bank_mask:0xf
	s_waitcnt lgkmcnt(0)
	v_add_f32_e32 v32, v32, v33
	v_xor_b32_e32 v33, 32, v192
	v_cmp_lt_i32_e32 vcc, v33, v31
	s_nop 1
	v_cndmask_b32_e32 v31, v192, v33, vcc
	v_lshlrev_b32_e32 v198, 2, v31
	v_mov_b32_e32 v31, v32
	v_mov_b32_e32 v198, v32
	s_nop 1
	v_permlane32_swap_b32_e32 v31, v198
	s_nop 1
	v_mov_b32_dpp v31, v198 quad_perm:[0,1,2,3] row_mask:0x3 bank_mask:0xf
	s_waitcnt lgkmcnt(0)
	v_add_f32_e32 v86, v32, v31
	s_nop 1
	v_mov_b32_dpp v31, v30 quad_perm:[1,0,3,2] row_mask:0xf bank_mask:0xf
	v_fmamk_f32 v53, v86, 0xba000000, v53
	v_fmamk_f32 v57, v86, 0xba000000, v57
	v_fmac_f32_e32 v52, 0xba000000, v86
	v_fmac_f32_e32 v56, 0xba000000, v86
	s_waitcnt lgkmcnt(0)
	v_add_f32_e32 v30, v30, v31
	s_nop 1
	v_mov_b32_dpp v31, v30 quad_perm:[2,3,0,1] row_mask:0xf bank_mask:0xf
	v_mov_b32_e32 v32, v53
	v_mov_b32_e32 v33, v57
	v_fmac_f32_e32 v48, 0xba000000, v86
	v_fmac_f32_e32 v54, 0xba000000, v86
	s_waitcnt lgkmcnt(0)
	v_add_f32_e32 v30, v30, v31
	s_nop 1
	v_mov_b32_dpp v31, v30 row_half_mirror row_mask:0xf bank_mask:0xf
	v_pk_mul_f32 v[32:33], v[32:33], v[32:33]
	v_fmamk_f32 v49, v86, 0xba000000, v49
	v_fmamk_f32 v55, v86, 0xba000000, v55
	v_mov_b32_e32 v74, v49
	s_waitcnt lgkmcnt(0)
	v_add_f32_e32 v30, v30, v31
	s_nop 1
	v_mov_b32_dpp v31, v30 row_mirror row_mask:0xf bank_mask:0xf
	v_mov_b32_e32 v75, v55
	v_fmamk_f32 v63, v86, 0xba000000, v63
	v_fmac_f32_e32 v62, 0xba000000, v86
	v_fmamk_f32 v65, v86, 0xba000000, v65
	s_waitcnt lgkmcnt(0)
	v_add_f32_e32 v30, v30, v31
	v_mov_b32_e32 v31, v30
	v_mov_b32_e32 v197, v30
	s_nop 1
	v_permlane16_swap_b32_e32 v31, v197
	s_nop 1
	v_mov_b32_dpp v31, v197 quad_perm:[0,1,2,3] row_mask:0x5 bank_mask:0xf
	v_fmac_f32_e32 v64, 0xba000000, v86
	v_fmac_f32_e32 v38, 0xba000000, v86
	v_fmamk_f32 v39, v86, 0xba000000, v39
	v_fmac_f32_e32 v40, 0xba000000, v86
	s_waitcnt lgkmcnt(0)
	v_add_f32_e32 v30, v30, v31
	v_mov_b32_e32 v31, v30
	v_mov_b32_e32 v198, v30
	s_nop 1
	v_permlane32_swap_b32_e32 v31, v198
	s_nop 1
	v_mov_b32_dpp v31, v198 quad_perm:[0,1,2,3] row_mask:0x3 bank_mask:0xf
	v_fmamk_f32 v41, v86, 0xba000000, v41
	v_fmamk_f32 v37, v86, 0xba000000, v37
	v_fmac_f32_e32 v36, 0xba000000, v86
	v_fmamk_f32 v35, v86, 0xba000000, v35
	s_waitcnt lgkmcnt(0)
	v_add_f32_e32 v87, v30, v31
	v_mov_b32_e32 v30, v52
	v_mov_b32_e32 v31, v56
	v_pk_fma_f32 v[30:31], v[30:31], v[30:31], v[32:33]
	v_mov_b32_e32 v32, v48
	v_mov_b32_e32 v33, v54
	v_fmamk_f32 v51, v87, 0xba000000, v51
	v_fmamk_f32 v69, v87, 0xba000000, v69
	v_pk_mul_f32 v[32:33], v[32:33], v[32:33]
	v_fmamk_f32 v47, v87, 0xba000000, v47
	v_fmac_f32_e32 v50, 0xba000000, v87
	v_fmamk_f32 v67, v87, 0xba000000, v67
	v_fmac_f32_e32 v68, 0xba000000, v87
	v_pk_fma_f32 v[32:33], v[74:75], v[74:75], v[32:33]
	v_mov_b32_e32 v74, v51
	v_mov_b32_e32 v75, v69
	v_fmac_f32_e32 v46, 0xba000000, v87
	v_fmac_f32_e32 v66, 0xba000000, v87
	v_pk_add_f32 v[30:31], v[30:31], v[32:33]
	v_mov_b32_e32 v32, v50
	v_mov_b32_e32 v33, v68
	v_pk_mul_f32 v[74:75], v[74:75], v[74:75]
	v_mov_b32_e32 v76, v47
	v_mov_b32_e32 v77, v67
	v_pk_fma_f32 v[32:33], v[32:33], v[32:33], v[74:75]
	v_mov_b32_e32 v74, v46
	v_mov_b32_e32 v75, v66
	v_pk_mul_f32 v[76:77], v[76:77], v[76:77]
	v_fmamk_f32 v59, v87, 0xba000000, v59
	v_pk_fma_f32 v[74:75], v[74:75], v[74:75], v[76:77]
	v_pk_mul_f32 v[76:77], v[62:63], v[62:63]
	v_pk_add_f32 v[32:33], v[32:33], v[74:75]
	v_pk_mul_f32 v[74:75], v[64:65], v[64:65]
	v_fmac_f32_e32 v58, 0xba000000, v87
	v_fmamk_f32 v61, v87, 0xba000000, v61
	v_fmac_f32_e32 v60, 0xba000000, v87
	v_pk_mov_b32 v[78:79], v[76:77], v[74:75] op_sel:[1,0]
	v_mov_b32_e32 v77, v75
	v_pk_add_f32 v[30:31], v[30:31], v[30:31] op_sel_hi:[0,1]
	v_pk_add_f32 v[74:75], v[76:77], v[78:79]
	v_pk_mul_f32 v[76:77], v[60:61], v[60:61]
	v_pk_mul_f32 v[78:79], v[58:59], v[58:59]
	v_mul_f32_e32 v30, v38, v38
	v_pk_mov_b32 v[80:81], v[78:79], v[76:77] op_sel:[1,0]
	v_mov_b32_e32 v79, v77
	v_pk_add_f32 v[76:77], v[80:81], v[78:79]
	v_fmac_f32_e32 v70, 0xba000000, v87
	v_pk_fma_f32 v[78:79], v[38:39], v[38:39], v[30:31] op_sel_hi:[1,1,0]
	v_mul_f32_e32 v30, v40, v40
	v_fmamk_f32 v71, v87, 0xba000000, v71
	v_fmac_f32_e32 v72, 0xba000000, v87
	v_pk_fma_f32 v[80:81], v[40:41], v[40:41], v[30:31] op_sel_hi:[1,1,0]
	v_mul_f32_e32 v30, v70, v70
	v_fmamk_f32 v73, v87, 0xba000000, v73
	v_pk_fma_f32 v[82:83], v[70:71], v[70:71], v[30:31] op_sel_hi:[1,1,0]
	v_mul_f32_e32 v30, v72, v72
	v_pk_add_f32 v[32:33], v[32:33], v[32:33] op_sel_hi:[0,1]
	v_pk_add_f32 v[74:75], v[74:75], v[74:75] op_sel_hi:[0,1]
	v_pk_add_f32 v[76:77], v[76:77], v[76:77] op_sel_hi:[0,1]
	v_pk_fma_f32 v[84:85], v[72:73], v[72:73], v[30:31] op_sel_hi:[1,1,0]
	v_fmamk_f32 v29, v87, 0xba000000, v29
	v_fmac_f32_e32 v28, 0xba000000, v87
	v_fmamk_f32 v27, v87, 0xba000000, v27
	v_fmac_f32_e32 v26, 0xba000000, v87
	v_fmac_f32_e32 v34, 0xba000000, v86
	v_mul_f32_e32 v30, v36, v36
	v_mul_f32_e32 v74, v37, v37
	v_mul_f32_e32 v82, v26, v26
	v_mul_f32_e32 v84, v27, v27
	v_mul_f32_e32 v76, v28, v28
	v_mul_f32_e32 v32, v29, v29
	v_mul_f32_e32 v78, v34, v34
	v_mul_f32_e32 v80, v35, v35
	v_pk_add_f32 v[30:31], v[74:75], v[30:31]
	v_pk_add_f32 v[74:75], v[82:83], v[84:85]
	v_pk_add_f32 v[32:33], v[76:77], v[32:33]
	v_fmamk_f32 v23, v86, 0xba000000, v23
	v_fmac_f32_e32 v22, 0xba000000, v86
	v_fmamk_f32 v25, v86, 0xba000000, v25
	v_fmac_f32_e32 v24, 0xba000000, v86
	v_pk_add_f32 v[78:79], v[78:79], v[80:81]
	v_pk_add_f32 v[32:33], v[74:75], v[32:33]
	v_pk_mul_f32 v[74:75], v[24:25], v[24:25]
	v_pk_mul_f32 v[76:77], v[22:23], v[22:23]
	v_pk_add_f32 v[30:31], v[78:79], v[30:31]
	v_fmamk_f32 v19, v87, 0xba000000, v19
	v_fmac_f32_e32 v18, 0xba000000, v87
	v_fmamk_f32 v21, v87, 0xba000000, v21
	v_fmac_f32_e32 v20, 0xba000000, v87
	v_pk_mov_b32 v[78:79], v[76:77], v[74:75] op_sel:[1,0]
	v_mov_b32_e32 v77, v75
	v_pk_add_f32 v[30:31], v[30:31], v[30:31] op_sel_hi:[0,1]
	v_pk_add_f32 v[74:75], v[76:77], v[78:79]
	v_pk_mul_f32 v[76:77], v[20:21], v[20:21]
	v_pk_mul_f32 v[78:79], v[18:19], v[18:19]
	v_fmac_f32_e32 v14, 0xba000000, v86
	v_pk_mov_b32 v[80:81], v[78:79], v[76:77] op_sel:[1,0]
	v_mov_b32_e32 v79, v77
	v_fmamk_f32 v15, v86, 0xba000000, v15
	v_fmac_f32_e32 v16, 0xba000000, v86
	v_mul_f32_e32 v30, v14, v14
	v_pk_add_f32 v[76:77], v[80:81], v[78:79]
	v_fmamk_f32 v17, v86, 0xba000000, v17
	v_fmac_f32_e32 v10, 0xba000000, v87
	v_pk_fma_f32 v[78:79], v[14:15], v[14:15], v[30:31] op_sel_hi:[1,1,0]
	v_mul_f32_e32 v30, v16, v16
	v_fmamk_f32 v11, v87, 0xba000000, v11
	v_fmac_f32_e32 v12, 0xba000000, v87
	v_pk_fma_f32 v[80:81], v[16:17], v[16:17], v[30:31] op_sel_hi:[1,1,0]
	v_mul_f32_e32 v30, v10, v10
	v_pk_add_f32 v[74:75], v[74:75], v[74:75] op_sel_hi:[0,1]
	v_fmamk_f32 v13, v87, 0xba000000, v13
	v_pk_fma_f32 v[82:83], v[10:11], v[10:11], v[30:31] op_sel_hi:[1,1,0]
	v_mul_f32_e32 v30, v12, v12
	v_fmamk_f32 v9, v86, 0xba000000, v9
	v_fmac_f32_e32 v8, 0xba000000, v86
	v_fmamk_f32 v7, v86, 0xba000000, v7
	v_fmac_f32_e32 v6, 0xba000000, v86
	v_pk_fma_f32 v[84:85], v[12:13], v[12:13], v[30:31] op_sel_hi:[1,1,0]
	v_mul_f32_e32 v78, v6, v6
	v_mul_f32_e32 v80, v7, v7
	v_mul_f32_e32 v30, v8, v8
	v_mul_f32_e32 v74, v9, v9
	v_pk_add_f32 v[32:33], v[32:33], v[32:33] op_sel_hi:[0,1]
	v_pk_add_f32 v[76:77], v[76:77], v[76:77] op_sel_hi:[0,1]
	v_fmamk_f32 v5, v87, 0xba000000, v5
	v_fmac_f32_e32 v4, 0xba000000, v87
	v_fmamk_f32 v3, v87, 0xba000000, v3
	v_fmac_f32_e32 v2, 0xba000000, v87
	v_pk_add_f32 v[78:79], v[78:79], v[80:81]
	v_pk_add_f32 v[30:31], v[74:75], v[30:31]
	v_mul_f32_e32 v82, v2, v2
	v_pk_add_f32 v[30:31], v[78:79], v[30:31]
	v_mul_f32_e32 v84, v3, v3
	v_mul_f32_e32 v76, v4, v4
	v_mul_f32_e32 v32, v5, v5
	v_add_f32_e32 v74, v30, v31
	v_pk_add_f32 v[30:31], v[82:83], v[84:85]
	v_pk_add_f32 v[32:33], v[76:77], v[32:33]
	ds_read_b128 v[82:85], v98
	ds_read_b128 v[86:89], v99
	v_pk_add_f32 v[30:31], v[30:31], v[32:33]
	s_nop 0
	v_add_f32_e32 v31, v30, v31
	s_nop 1
	v_mov_b32_dpp v30, v74 quad_perm:[1,0,3,2] row_mask:0xf bank_mask:0xf
	s_waitcnt lgkmcnt(0)
	v_add_f32_e32 v30, v74, v30
	s_nop 1
	v_mov_b32_dpp v32, v30 quad_perm:[2,3,0,1] row_mask:0xf bank_mask:0xf
	s_waitcnt lgkmcnt(0)
	v_add_f32_e32 v30, v30, v32
	s_nop 1
	v_mov_b32_dpp v32, v30 row_half_mirror row_mask:0xf bank_mask:0xf
	s_waitcnt lgkmcnt(0)
	v_add_f32_e32 v30, v30, v32
	s_nop 1
	v_mov_b32_dpp v32, v30 row_mirror row_mask:0xf bank_mask:0xf
	s_waitcnt lgkmcnt(0)
	v_add_f32_e32 v30, v30, v32
	v_mov_b32_e32 v32, v30
	v_mov_b32_e32 v197, v30
	s_nop 1
	v_permlane16_swap_b32_e32 v32, v197
	s_nop 1
	v_mov_b32_dpp v32, v197 quad_perm:[0,1,2,3] row_mask:0x5 bank_mask:0xf
	s_waitcnt lgkmcnt(0)
	v_add_f32_e32 v30, v30, v32
	v_mov_b32_e32 v32, v30
	v_mov_b32_e32 v198, v30
	s_nop 1
	v_permlane32_swap_b32_e32 v32, v198
	s_nop 1
	v_mov_b32_dpp v32, v198 quad_perm:[0,1,2,3] row_mask:0x3 bank_mask:0xf
	s_waitcnt lgkmcnt(0)
	v_add_f32_e32 v30, v30, v32
	v_fmamk_f32 v30, v30, 0x3a000000, v189
	v_cmp_gt_f32_e32 vcc, s75, v30
	v_mul_f32_e32 v32, 0x4f800000, v30
	s_nop 0
	v_cndmask_b32_e32 v30, v30, v32, vcc
	v_sqrt_f32_e32 v32, v30
	s_nop 0
	v_add_u32_e32 v33, -1, v32
	v_fma_f32 v74, -v33, v32, v30
	v_cmp_ge_f32_e64 s[0:1], 0, v74
	v_add_u32_e32 v74, 1, v32
	s_nop 0
	v_cndmask_b32_e64 v33, v32, v33, s[0:1]
	v_fma_f32 v32, -v74, v32, v30
	v_cmp_lt_f32_e64 s[0:1], 0, v32
	s_nop 1
	v_cndmask_b32_e64 v32, v33, v74, s[0:1]
	v_mul_f32_e32 v33, 0x37800000, v32
	v_cndmask_b32_e32 v32, v32, v33, vcc
	v_cmp_class_f32_e32 vcc, v30, v190
	s_nop 1
	v_cndmask_b32_e32 v30, v32, v30, vcc
	v_div_scale_f32 v32, s[0:1], v30, v30, 1.0
	v_rcp_f32_e32 v33, v32
	s_nop 0
	v_fma_f32 v74, -v32, v33, 1.0
	v_fmac_f32_e32 v33, v74, v33
	v_div_scale_f32 v74, vcc, 1.0, v30, 1.0
	v_mul_f32_e32 v75, v74, v33
	v_fma_f32 v76, -v32, v75, v74
	v_fmac_f32_e32 v75, v76, v33
	v_fma_f32 v32, -v32, v75, v74
	v_div_fmas_f32 v32, v32, v33, v75
	v_div_fixup_f32 v30, v32, v30, 1.0
	s_nop 1
	v_mov_b32_dpp v32, v31 quad_perm:[1,0,3,2] row_mask:0xf bank_mask:0xf
	s_waitcnt lgkmcnt(0)
	v_add_f32_e32 v31, v31, v32
	s_nop 1
	v_mov_b32_dpp v32, v31 quad_perm:[2,3,0,1] row_mask:0xf bank_mask:0xf
	s_waitcnt lgkmcnt(0)
	v_add_f32_e32 v31, v31, v32
	s_nop 1
	v_mov_b32_dpp v32, v31 row_half_mirror row_mask:0xf bank_mask:0xf
	s_waitcnt lgkmcnt(0)
	v_add_f32_e32 v31, v31, v32
	s_nop 1
	v_mov_b32_dpp v32, v31 row_mirror row_mask:0xf bank_mask:0xf
	s_waitcnt lgkmcnt(0)
	v_add_f32_e32 v31, v31, v32
	v_mov_b32_e32 v32, v31
	v_mov_b32_e32 v197, v31
	s_nop 1
	v_permlane16_swap_b32_e32 v32, v197
	s_nop 1
	v_mov_b32_dpp v32, v197 quad_perm:[0,1,2,3] row_mask:0x5 bank_mask:0xf
	s_waitcnt lgkmcnt(0)
	v_add_f32_e32 v31, v31, v32
	v_mov_b32_e32 v32, v31
	v_mov_b32_e32 v198, v31
	s_nop 1
	v_permlane32_swap_b32_e32 v32, v198
	s_nop 1
	v_mov_b32_dpp v32, v198 quad_perm:[0,1,2,3] row_mask:0x3 bank_mask:0xf
	s_waitcnt lgkmcnt(0)
	v_add_f32_e32 v31, v31, v32
	v_fmamk_f32 v31, v31, 0x3a000000, v189
	v_cmp_gt_f32_e32 vcc, s75, v31
	v_mul_f32_e32 v32, 0x4f800000, v31
	s_nop 0
	v_cndmask_b32_e32 v31, v31, v32, vcc
	v_sqrt_f32_e32 v32, v31
	s_nop 0
	v_add_u32_e32 v33, -1, v32
	v_fma_f32 v74, -v33, v32, v31
	v_cmp_ge_f32_e64 s[0:1], 0, v74
	v_add_u32_e32 v74, 1, v32
	s_nop 0
	v_cndmask_b32_e64 v33, v32, v33, s[0:1]
	v_fma_f32 v32, -v74, v32, v31
	v_cmp_lt_f32_e64 s[0:1], 0, v32
	s_nop 1
	v_cndmask_b32_e64 v32, v33, v74, s[0:1]
	v_mul_f32_e32 v33, 0x37800000, v32
	v_cndmask_b32_e32 v32, v32, v33, vcc
	v_cmp_class_f32_e32 vcc, v31, v190
	s_nop 1
	v_cndmask_b32_e32 v31, v32, v31, vcc
	v_div_scale_f32 v32, s[0:1], v31, v31, 1.0
	v_rcp_f32_e32 v33, v32
	s_add_u32 s0, s20, s16
	s_addc_u32 s1, s21, s17
	s_add_u32 s16, s20, s52
	v_fma_f32 v74, -v32, v33, 1.0
	v_fmac_f32_e32 v33, v74, v33
	v_div_scale_f32 v74, vcc, 1.0, v31, 1.0
	v_mul_f32_e32 v75, v74, v33
	v_fma_f32 v76, -v32, v75, v74
	v_fmac_f32_e32 v75, v76, v33
	v_fma_f32 v32, -v32, v75, v74
	v_div_fmas_f32 v32, v32, v33, v75
	v_div_fixup_f32 v32, v32, v31, 1.0
	v_add_u32_e32 v31, 0x16800, v90
	v_add_u32_e32 v33, 0x18800, v90
	ds_read_b128 v[74:77], v31
	ds_read_b128 v[78:81], v33
	s_addc_u32 s17, s21, s53
	s_add_u32 s52, s51, s54
	s_addc_u32 s53, s58, s55
	v_pk_mul_f32 v[52:53], v[52:53], v[30:31] op_sel_hi:[1,0]
	v_pk_mul_f32 v[48:49], v[48:49], v[30:31] op_sel_hi:[1,0]
	s_add_u32 s54, s51, s56
	s_waitcnt lgkmcnt(0)
	v_pk_fma_f32 v[92:93], v[76:77], v[48:49], v[80:81]
	v_pk_fma_f32 v[90:91], v[74:75], v[52:53], v[78:79]
	v_pk_mul_f32 v[50:51], v[50:51], v[32:33] op_sel_hi:[1,0]
	v_pk_mul_f32 v[46:47], v[46:47], v[32:33] op_sel_hi:[1,0]
	s_addc_u32 s55, s58, s57
	v_pk_fma_f32 v[48:49], v[76:77], v[46:47], v[80:81]
	v_pk_fma_f32 v[46:47], v[74:75], v[50:51], v[78:79]
	v_lshl_add_u64 v[94:95], s[0:1], 0, v[44:45]
	v_lshl_add_u64 v[96:97], s[16:17], 0, v[44:45]
	v_pk_fma_f32 v[44:45], v[84:85], v[92:93], v[88:89]
	v_pk_fma_f32 v[50:51], v[82:83], v[90:91], v[86:87]
	global_store_dwordx4 v[94:95], v[90:93], off
	global_store_dwordx4 v[96:97], v[46:49], off
	v_cvt_pk_bf16_f32 v50, v50, v51
	v_cvt_pk_bf16_f32 v51, v44, v45
	v_lshl_add_u64 v[44:45], s[52:53], 0, v[42:43]
	v_lshl_add_u64 v[42:43], s[54:55], 0, v[42:43]
	v_pk_fma_f32 v[46:47], v[82:83], v[46:47], v[86:87]
	v_pk_fma_f32 v[48:49], v[84:85], v[48:49], v[88:89]
	global_store_dwordx2 v[44:45], v[50:51], off
	v_cvt_pk_bf16_f32 v46, v46, v47
	v_cvt_pk_bf16_f32 v47, v48, v49
	global_store_dwordx2 v[42:43], v[46:47], off
	ds_read_b128 v[46:49], v31 offset:1024
	ds_read_b128 v[50:53], v33 offset:1024
	ds_read_b128 v[74:77], v98 offset:1024
	ds_read_b128 v[78:81], v99 offset:1024
	v_pk_mul_f32 v[82:83], v[54:55], v[30:31] op_sel_hi:[1,0]
	v_pk_mul_f32 v[54:55], v[56:57], v[30:31] op_sel_hi:[1,0]
	v_pk_mul_f32 v[68:69], v[68:69], v[32:33] op_sel_hi:[1,0]
	s_waitcnt lgkmcnt(2)
	v_pk_fma_f32 v[54:55], v[46:47], v[54:55], v[50:51]
	v_pk_fma_f32 v[56:57], v[48:49], v[82:83], v[52:53]
	v_pk_mul_f32 v[66:67], v[66:67], v[32:33] op_sel_hi:[1,0]
	v_pk_fma_f32 v[46:47], v[46:47], v[68:69], v[50:51]
	v_pk_fma_f32 v[48:49], v[48:49], v[66:67], v[52:53]
	global_store_dwordx4 v[94:95], v[54:57], off offset:1024
	global_store_dwordx4 v[96:97], v[46:49], off offset:1024
	s_waitcnt lgkmcnt(0)
	v_pk_fma_f32 v[52:53], v[74:75], v[54:55], v[78:79]
	v_pk_fma_f32 v[50:51], v[76:77], v[56:57], v[80:81]
	v_pk_fma_f32 v[46:47], v[74:75], v[46:47], v[78:79]
	v_pk_fma_f32 v[48:49], v[76:77], v[48:49], v[80:81]
	v_cvt_pk_bf16_f32 v52, v52, v53
	v_cvt_pk_bf16_f32 v53, v50, v51
	global_store_dwordx2 v[44:45], v[52:53], off offset:512
	v_cvt_pk_bf16_f32 v46, v46, v47
	v_cvt_pk_bf16_f32 v47, v48, v49
	global_store_dwordx2 v[42:43], v[46:47], off offset:512
	ds_read_b128 v[46:49], v31 offset:2048
	ds_read_b128 v[50:53], v33 offset:2048
	ds_read_b128 v[54:57], v98 offset:2048
	ds_read_b128 v[66:69], v99 offset:2048
	v_pk_mul_f32 v[64:65], v[64:65], v[30:31] op_sel_hi:[1,0]
	v_pk_mul_f32 v[62:63], v[62:63], v[30:31] op_sel_hi:[1,0]
	v_pk_mul_f32 v[58:59], v[58:59], v[32:33] op_sel_hi:[1,0]
	s_waitcnt lgkmcnt(2)
	v_pk_fma_f32 v[62:63], v[62:63], v[46:47], v[50:51]
	v_pk_fma_f32 v[64:65], v[64:65], v[48:49], v[52:53]
	v_pk_mul_f32 v[60:61], v[60:61], v[32:33] op_sel_hi:[1,0]
	v_pk_fma_f32 v[46:47], v[58:59], v[46:47], v[50:51]
	v_pk_fma_f32 v[48:49], v[60:61], v[48:49], v[52:53]
	global_store_dwordx4 v[94:95], v[62:65], off offset:2048
	global_store_dwordx4 v[96:97], v[46:49], off offset:2048
	s_waitcnt lgkmcnt(0)
	v_pk_fma_f32 v[52:53], v[62:63], v[54:55], v[66:67]
	v_pk_fma_f32 v[50:51], v[64:65], v[56:57], v[68:69]
	v_pk_fma_f32 v[46:47], v[54:55], v[46:47], v[66:67]
	v_pk_fma_f32 v[48:49], v[56:57], v[48:49], v[68:69]
	v_cvt_pk_bf16_f32 v52, v52, v53
	v_cvt_pk_bf16_f32 v53, v50, v51
	global_store_dwordx2 v[44:45], v[52:53], off offset:1024
	v_cvt_pk_bf16_f32 v46, v46, v47
	v_cvt_pk_bf16_f32 v47, v48, v49
	global_store_dwordx2 v[42:43], v[46:47], off offset:1024
	ds_read_b128 v[46:49], v31 offset:3072
	ds_read_b128 v[50:53], v33 offset:3072
	ds_read_b128 v[54:57], v98 offset:3072
	ds_read_b128 v[58:61], v99 offset:3072
	v_pk_mul_f32 v[40:41], v[40:41], v[30:31] op_sel_hi:[1,0]
	v_pk_mul_f32 v[38:39], v[38:39], v[30:31] op_sel_hi:[1,0]
	s_waitcnt lgkmcnt(2)
	v_pk_fma_f32 v[40:41], v[40:41], v[48:49], v[52:53]
	v_pk_fma_f32 v[38:39], v[38:39], v[46:47], v[50:51]
	v_pk_mul_f32 v[62:63], v[72:73], v[32:33] op_sel_hi:[1,0]
	v_pk_mul_f32 v[64:65], v[70:71], v[32:33] op_sel_hi:[1,0]
	v_pk_fma_f32 v[48:49], v[62:63], v[48:49], v[52:53]
	v_pk_fma_f32 v[46:47], v[64:65], v[46:47], v[50:51]
	global_store_dwordx4 v[94:95], v[38:41], off offset:3072
	global_store_dwordx4 v[96:97], v[46:49], off offset:3072
	v_pk_mul_f32 v[36:37], v[36:37], v[30:31] op_sel_hi:[1,0]
	s_waitcnt lgkmcnt(0)
	v_pk_fma_f32 v[38:39], v[38:39], v[54:55], v[58:59]
	v_pk_fma_f32 v[40:41], v[40:41], v[56:57], v[60:61]
	v_cvt_pk_bf16_f32 v38, v38, v39
	v_pk_fma_f32 v[48:49], v[56:57], v[48:49], v[60:61]
	v_cvt_pk_bf16_f32 v39, v40, v41
	v_pk_fma_f32 v[46:47], v[54:55], v[46:47], v[58:59]
	global_store_dwordx2 v[44:45], v[38:39], off offset:1536
	v_cvt_pk_bf16_f32 v38, v46, v47
	v_cvt_pk_bf16_f32 v39, v48, v49
	global_store_dwordx2 v[42:43], v[38:39], off offset:1536
	ds_read_b128 v[38:41], v31 offset:4096
	ds_read_b128 v[46:49], v33 offset:4096
	ds_read_b128 v[50:53], v98 offset:4096
	ds_read_b128 v[54:57], v99 offset:4096
	v_add_co_u32_e32 v58, vcc, s74, v94
	v_pk_mul_f32 v[34:35], v[34:35], v[30:31] op_sel_hi:[1,0]
	s_nop 0
	v_addc_co_u32_e32 v59, vcc, 0, v95, vcc
	v_pk_mul_f32 v[28:29], v[28:29], v[32:33] op_sel_hi:[1,0]
	v_pk_mul_f32 v[26:27], v[26:27], v[32:33] op_sel_hi:[1,0]
	v_add_co_u32_e32 v60, vcc, s74, v96
	s_waitcnt lgkmcnt(2)
	v_pk_fma_f32 v[34:35], v[34:35], v[38:39], v[46:47]
	v_pk_fma_f32 v[36:37], v[36:37], v[40:41], v[48:49]
	v_pk_fma_f32 v[26:27], v[26:27], v[38:39], v[46:47]
	v_pk_fma_f32 v[28:29], v[28:29], v[40:41], v[48:49]
	v_addc_co_u32_e32 v61, vcc, 0, v97, vcc
	global_store_dwordx4 v[58:59], v[34:37], off
	global_store_dwordx4 v[60:61], v[26:29], off
	v_pk_mul_f32 v[24:25], v[24:25], v[30:31] op_sel_hi:[1,0]
	s_waitcnt lgkmcnt(0)
	v_pk_fma_f32 v[34:35], v[34:35], v[50:51], v[54:55]
	v_pk_fma_f32 v[26:27], v[50:51], v[26:27], v[54:55]
	v_pk_fma_f32 v[36:37], v[36:37], v[52:53], v[56:57]
	v_pk_fma_f32 v[28:29], v[52:53], v[28:29], v[56:57]
	v_cvt_pk_bf16_f32 v34, v34, v35
	v_cvt_pk_bf16_f32 v35, v36, v37
	global_store_dwordx2 v[44:45], v[34:35], off offset:2048
	v_cvt_pk_bf16_f32 v26, v26, v27
	v_cvt_pk_bf16_f32 v27, v28, v29
	global_store_dwordx2 v[42:43], v[26:27], off offset:2048
	ds_read_b128 v[26:29], v31 offset:5120
	ds_read_b128 v[34:37], v33 offset:5120
	ds_read_b128 v[38:41], v98 offset:5120
	ds_read_b128 v[46:49], v99 offset:5120
	v_pk_mul_f32 v[22:23], v[22:23], v[30:31] op_sel_hi:[1,0]
	v_pk_mul_f32 v[18:19], v[18:19], v[32:33] op_sel_hi:[1,0]
	s_waitcnt lgkmcnt(2)
	v_pk_fma_f32 v[22:23], v[22:23], v[26:27], v[34:35]
	v_pk_fma_f32 v[24:25], v[24:25], v[28:29], v[36:37]
	v_pk_mul_f32 v[20:21], v[20:21], v[32:33] op_sel_hi:[1,0]
	v_pk_fma_f32 v[18:19], v[18:19], v[26:27], v[34:35]
	v_pk_fma_f32 v[20:21], v[20:21], v[28:29], v[36:37]
	global_store_dwordx4 v[58:59], v[22:25], off offset:1024
	global_store_dwordx4 v[60:61], v[18:21], off offset:1024
	v_pk_mul_f32 v[16:17], v[16:17], v[30:31] op_sel_hi:[1,0]
	s_waitcnt lgkmcnt(0)
	v_pk_fma_f32 v[22:23], v[22:23], v[38:39], v[46:47]
	v_pk_fma_f32 v[18:19], v[38:39], v[18:19], v[46:47]
	v_pk_fma_f32 v[24:25], v[24:25], v[40:41], v[48:49]
	v_pk_fma_f32 v[20:21], v[40:41], v[20:21], v[48:49]
	v_cvt_pk_bf16_f32 v22, v22, v23
	v_cvt_pk_bf16_f32 v23, v24, v25
	global_store_dwordx2 v[44:45], v[22:23], off offset:2560
	v_cvt_pk_bf16_f32 v18, v18, v19
	v_cvt_pk_bf16_f32 v19, v20, v21
	global_store_dwordx2 v[42:43], v[18:19], off offset:2560
	ds_read_b128 v[18:21], v31 offset:6144
	ds_read_b128 v[22:25], v33 offset:6144
	ds_read_b128 v[26:29], v98 offset:6144
	ds_read_b128 v[34:37], v99 offset:6144
	v_pk_mul_f32 v[14:15], v[14:15], v[30:31] op_sel_hi:[1,0]
	v_pk_mul_f32 v[10:11], v[10:11], v[32:33] op_sel_hi:[1,0]
	s_waitcnt lgkmcnt(2)
	v_pk_fma_f32 v[14:15], v[14:15], v[18:19], v[22:23]
	v_pk_fma_f32 v[16:17], v[16:17], v[20:21], v[24:25]
	v_pk_mul_f32 v[12:13], v[12:13], v[32:33] op_sel_hi:[1,0]
	v_pk_fma_f32 v[10:11], v[10:11], v[18:19], v[22:23]
	v_pk_fma_f32 v[12:13], v[12:13], v[20:21], v[24:25]
	global_store_dwordx4 v[58:59], v[14:17], off offset:2048
	global_store_dwordx4 v[60:61], v[10:13], off offset:2048
	v_pk_mul_f32 v[8:9], v[8:9], v[30:31] op_sel_hi:[1,0]
	s_waitcnt lgkmcnt(0)
	v_pk_fma_f32 v[14:15], v[14:15], v[26:27], v[34:35]
	v_pk_fma_f32 v[10:11], v[26:27], v[10:11], v[34:35]
	v_pk_fma_f32 v[16:17], v[16:17], v[28:29], v[36:37]
	v_pk_fma_f32 v[12:13], v[28:29], v[12:13], v[36:37]
	v_cvt_pk_bf16_f32 v14, v14, v15
	v_cvt_pk_bf16_f32 v15, v16, v17
	global_store_dwordx2 v[44:45], v[14:15], off offset:3072
	v_cvt_pk_bf16_f32 v10, v10, v11
	v_cvt_pk_bf16_f32 v11, v12, v13
	global_store_dwordx2 v[42:43], v[10:11], off offset:3072
	ds_read_b128 v[10:13], v31 offset:7168
	ds_read_b128 v[14:17], v33 offset:7168
	ds_read_b128 v[18:21], v98 offset:7168
	ds_read_b128 v[22:25], v99 offset:7168
	v_pk_mul_f32 v[6:7], v[6:7], v[30:31] op_sel_hi:[1,0]
	v_pk_mul_f32 v[2:3], v[2:3], v[32:33] op_sel_hi:[1,0]
	s_waitcnt lgkmcnt(2)
	v_pk_fma_f32 v[6:7], v[6:7], v[10:11], v[14:15]
	v_pk_fma_f32 v[8:9], v[8:9], v[12:13], v[16:17]
	v_pk_mul_f32 v[4:5], v[4:5], v[32:33] op_sel_hi:[1,0]
	v_pk_fma_f32 v[2:3], v[2:3], v[10:11], v[14:15]
	s_add_i32 s30, s30, 2
	s_add_i32 s14, s14, 16
	v_pk_fma_f32 v[4:5], v[4:5], v[12:13], v[16:17]
	global_store_dwordx4 v[58:59], v[6:9], off offset:3072
	global_store_dwordx4 v[60:61], v[2:5], off offset:3072
	s_cmp_gt_u32 s30, 5
	s_waitcnt lgkmcnt(0)
	v_pk_fma_f32 v[6:7], v[6:7], v[18:19], v[22:23]
	v_pk_fma_f32 v[2:3], v[18:19], v[2:3], v[22:23]
	v_pk_fma_f32 v[8:9], v[8:9], v[20:21], v[24:25]
	v_pk_fma_f32 v[4:5], v[20:21], v[4:5], v[24:25]
	v_cvt_pk_bf16_f32 v6, v6, v7
	v_cvt_pk_bf16_f32 v7, v8, v9
	global_store_dwordx2 v[44:45], v[6:7], off offset:3584
	v_cvt_pk_bf16_f32 v2, v2, v3
	v_cvt_pk_bf16_f32 v3, v4, v5
	global_store_dwordx2 v[42:43], v[2:3], off offset:3584
	s_cbranch_scc0 .LBB0_966
	s_lshl_b32 s15, s77, 2
	s_add_i32 s33, s15, 0x4000
	s_and_b64 vcc, exec, s[22:23]
	s_cbranch_vccz .LBB0_973
	s_or_b32 s14, s33, s91
	v_mov_b32_e32 v116, v164
	s_cmpk_gt_i32 s14, 0x3fff
	s_mov_b64 s[16:17], -1
	s_cbranch_scc0 .LBB0_970
	s_or_b32 s30, s15, s91
	s_lshl_b64 s[0:1], s[30:31], 13
	s_add_u32 s0, s72, s0
	s_addc_u32 s1, s73, s1
	s_mov_b32 s15, s31
	s_mov_b64 s[16:17], 0

.LBB0_972:
	s_lshl_b64 s[16:17], s[14:15], 12
	v_ashrrev_i32_e32 v117, 31, v116
	s_add_u32 s52, s49, s16
	v_lshlrev_b64 v[118:119], 2, v[116:117]
	s_addc_u32 s53, s50, s17
	v_lshl_add_u64 v[18:19], s[24:25], 0, v[118:119]
	v_lshlrev_b64 v[114:115], 1, v[116:117]
	v_lshl_add_u64 v[20:21], s[0:1], 0, v[118:119]
	v_lshl_add_u64 v[22:23], s[52:53], 0, v[114:115]
	global_load_dwordx4 v[2:5], v[18:19], off
	global_load_dwordx4 v[6:9], v[18:19], off offset:1024
	global_load_dwordx4 v[10:13], v[20:21], off nt
	global_load_dwordx4 v[14:17], v[20:21], off offset:1024 nt
	global_load_dwordx4 v[106:109], v[18:19], off offset:2048
	global_load_dwordx4 v[82:85], v[18:19], off offset:3072
	global_load_dwordx4 v[110:113], v[20:21], off offset:2048 nt
	global_load_dwordx4 v[86:89], v[20:21], off offset:3072 nt
	global_load_dwordx2 v[24:25], v[22:23], off nt
	global_load_dwordx2 v[26:27], v[22:23], off offset:512 nt
	global_load_dwordx2 v[158:159], v[22:23], off offset:1024 nt
	global_load_dwordx2 v[154:155], v[22:23], off offset:1536 nt
	v_add_co_u32_e32 v18, vcc, s74, v18
	s_nop 1
	v_addc_co_u32_e32 v19, vcc, 0, v19, vcc
	v_add_co_u32_e32 v20, vcc, s74, v20
	s_nop 1
	v_addc_co_u32_e32 v21, vcc, 0, v21, vcc
	global_load_dwordx4 v[98:101], v[18:19], off
	global_load_dwordx4 v[90:93], v[18:19], off offset:1024
	global_load_dwordx4 v[102:105], v[20:21], off nt
	global_load_dwordx4 v[94:97], v[20:21], off offset:1024 nt
	global_load_dwordx4 v[74:77], v[18:19], off offset:2048
	global_load_dwordx4 v[66:69], v[18:19], off offset:3072
	global_load_dwordx4 v[78:81], v[20:21], off offset:2048 nt
	global_load_dwordx4 v[70:73], v[20:21], off offset:3072 nt
	global_load_dwordx2 v[160:161], v[22:23], off offset:2048 nt
	global_load_dwordx2 v[156:157], v[22:23], off offset:2560 nt
	global_load_dwordx2 v[152:153], v[22:23], off offset:3072 nt
	global_load_dwordx2 v[150:151], v[22:23], off offset:3584 nt
	s_waitcnt vmcnt(15)
	v_lshlrev_b32_e32 v18, 16, v24
	v_and_b32_e32 v19, 0xffff0000, v24
	v_lshlrev_b32_e32 v20, 16, v25
	v_and_b32_e32 v21, 0xffff0000, v25
	v_pk_mul_f32 v[2:3], v[2:3], v[18:19]
	v_pk_mul_f32 v[4:5], v[4:5], v[20:21]
	v_pk_fma_f32 v[146:147], v[10:11], s[44:45], v[2:3] op_sel_hi:[1,0,1]
	s_waitcnt vmcnt(14)
	v_lshlrev_b32_e32 v2, 16, v26
	v_and_b32_e32 v3, 0xffff0000, v26
	v_pk_fma_f32 v[124:125], v[12:13], s[44:45], v[4:5] op_sel_hi:[1,0,1]
	v_lshlrev_b32_e32 v4, 16, v27
	v_and_b32_e32 v5, 0xffff0000, v27
	v_pk_mul_f32 v[2:3], v[6:7], v[2:3]
	v_pk_mul_f32 v[4:5], v[8:9], v[4:5]
	v_pk_fma_f32 v[122:123], v[14:15], s[44:45], v[2:3] op_sel_hi:[1,0,1]
	v_pk_fma_f32 v[120:121], v[16:17], s[44:45], v[4:5] op_sel_hi:[1,0,1]
	v_mov_b32_e32 v2, v146
	v_mov_b32_e32 v3, v122
	v_mov_b32_e32 v4, v147
	v_mov_b32_e32 v5, v123
	v_pk_add_f32 v[2:3], v[2:3], v[4:5]
	v_mov_b32_e32 v4, v124
	v_mov_b32_e32 v5, v120
	v_mov_b32_e32 v6, v125
	v_mov_b32_e32 v7, v121
	v_pk_add_f32 v[4:5], v[4:5], v[6:7]
	s_waitcnt vmcnt(13)
	v_lshlrev_b32_e32 v162, 16, v158
	v_pk_add_f32 v[148:149], v[2:3], v[4:5]
	v_lshl_add_u64 v[2:3], s[26:27], 0, v[118:119]
	v_lshl_add_u64 v[4:5], s[28:29], 0, v[118:119]
	global_load_dwordx4 v[58:61], v[2:3], off
	global_load_dwordx4 v[50:53], v[2:3], off offset:1024
	global_load_dwordx4 v[62:65], v[4:5], off
	global_load_dwordx4 v[54:57], v[4:5], off offset:1024
	global_load_dwordx4 v[42:45], v[2:3], off offset:2048
	global_load_dwordx4 v[34:37], v[2:3], off offset:3072
	global_load_dwordx4 v[46:49], v[4:5], off offset:2048
	global_load_dwordx4 v[38:41], v[4:5], off offset:3072
	v_add_co_u32_e32 v2, vcc, s74, v2
	v_and_b32_e32 v163, 0xffff0000, v158
	s_nop 0
	v_addc_co_u32_e32 v3, vcc, 0, v3, vcc
	v_add_co_u32_e32 v6, vcc, s74, v4
	v_lshlrev_b32_e32 v158, 16, v159
	s_nop 0
	v_addc_co_u32_e32 v7, vcc, 0, v5, vcc
	global_load_dwordx4 v[26:29], v[2:3], off
	global_load_dwordx4 v[18:21], v[2:3], off offset:1024
	global_load_dwordx4 v[30:33], v[6:7], off
	global_load_dwordx4 v[22:25], v[6:7], off offset:1024
	global_load_dwordx4 v[10:13], v[2:3], off offset:2048
	s_nop 0
	global_load_dwordx4 v[2:5], v[2:3], off offset:3072
	s_nop 0
	global_load_dwordx4 v[14:17], v[6:7], off offset:2048
	s_nop 0
	global_load_dwordx4 v[6:9], v[6:7], off offset:3072
	v_and_b32_e32 v159, 0xffff0000, v159
	v_pk_mul_f32 v[106:107], v[106:107], v[162:163]
	v_pk_mul_f32 v[108:109], v[108:109], v[158:159]
	v_pk_fma_f32 v[110:111], v[110:111], s[44:45], v[106:107] op_sel_hi:[1,0,1]
	v_pk_fma_f32 v[112:113], v[112:113], s[44:45], v[108:109] op_sel_hi:[1,0,1]
	v_mov_b32_e32 v108, v110
	v_pk_mov_b32 v[106:107], v[110:111], v[112:113] op_sel:[1,0]
	v_mov_b32_e32 v109, v113
	v_pk_add_f32 v[106:107], v[106:107], v[108:109]
	s_waitcnt vmcnt(28)
	v_lshlrev_b32_e32 v108, 16, v155
	v_pk_add_f32 v[158:159], v[106:107], v[106:107] op_sel:[0,1] op_sel_hi:[1,0]
	v_lshlrev_b32_e32 v106, 16, v154
	v_and_b32_e32 v107, 0xffff0000, v154
	v_and_b32_e32 v109, 0xffff0000, v155
	v_pk_mul_f32 v[82:83], v[82:83], v[106:107]
	v_pk_mul_f32 v[84:85], v[84:85], v[108:109]
	v_pk_fma_f32 v[106:107], v[86:87], s[44:45], v[82:83] op_sel_hi:[1,0,1]
	v_pk_fma_f32 v[108:109], v[88:89], s[44:45], v[84:85] op_sel_hi:[1,0,1]
	s_waitcnt vmcnt(19)
	v_lshlrev_b32_e32 v82, 16, v160
	v_and_b32_e32 v83, 0xffff0000, v160
	v_lshlrev_b32_e32 v84, 16, v161
	v_and_b32_e32 v85, 0xffff0000, v161
	v_pk_mul_f32 v[84:85], v[100:101], v[84:85]
	v_pk_mul_f32 v[82:83], v[98:99], v[82:83]
	v_pk_fma_f32 v[88:89], v[104:105], s[44:45], v[84:85] op_sel_hi:[1,0,1]
	v_pk_fma_f32 v[86:87], v[102:103], s[44:45], v[82:83] op_sel_hi:[1,0,1]
	s_waitcnt vmcnt(18)
	v_lshlrev_b32_e32 v82, 16, v156
	v_and_b32_e32 v83, 0xffff0000, v156
	v_lshlrev_b32_e32 v84, 16, v157
	v_and_b32_e32 v85, 0xffff0000, v157
	v_pk_mul_f32 v[84:85], v[92:93], v[84:85]
	v_pk_mul_f32 v[82:83], v[90:91], v[82:83]
	v_pk_fma_f32 v[84:85], v[96:97], s[44:45], v[84:85] op_sel_hi:[1,0,1]
	v_pk_fma_f32 v[82:83], v[94:95], s[44:45], v[82:83] op_sel_hi:[1,0,1]
	v_mov_b32_e32 v93, v85
	v_pk_mov_b32 v[90:91], v[82:83], v[84:85] op_sel:[1,0]
	v_mov_b32_e32 v92, v82
	v_pk_add_f32 v[90:91], v[90:91], v[92:93]
	s_waitcnt vmcnt(17)
	v_lshlrev_b32_e32 v92, 16, v152
	v_and_b32_e32 v93, 0xffff0000, v152
	v_pk_mul_f32 v[74:75], v[74:75], v[92:93]
	s_waitcnt vmcnt(16)
	v_lshlrev_b32_e32 v92, 16, v150
	v_and_b32_e32 v93, 0xffff0000, v150
	v_lshlrev_b32_e32 v94, 16, v153
	v_and_b32_e32 v95, 0xffff0000, v153
	v_pk_mul_f32 v[66:67], v[66:67], v[92:93]
	v_pk_mul_f32 v[76:77], v[76:77], v[94:95]
	v_lshlrev_b32_e32 v94, 16, v151
	v_and_b32_e32 v95, 0xffff0000, v151
	v_pk_fma_f32 v[66:67], v[70:71], s[44:45], v[66:67] op_sel_hi:[1,0,1]
	v_add_f32_e32 v70, 0, v148
	v_add_f32_e32 v154, v106, v107
	v_add_f32_e32 v162, v108, v109
	v_pk_mul_f32 v[68:69], v[68:69], v[94:95]
	v_add_f32_e32 v70, v70, v149
	v_mov_b32_e32 v155, v88
	v_mov_b32_e32 v163, v89
	v_mov_b32_e32 v71, v86
	v_mov_b32_e32 v159, v87
	v_pk_fma_f32 v[68:69], v[72:73], s[44:45], v[68:69] op_sel_hi:[1,0,1]
	v_pk_add_f32 v[72:73], v[154:155], v[162:163]
	v_pk_add_f32 v[70:71], v[70:71], v[158:159]
	v_pk_add_f32 v[90:91], v[90:91], v[90:91] op_sel:[0,1] op_sel_hi:[1,0]
	v_pk_add_f32 v[70:71], v[70:71], v[72:73]
	v_pk_fma_f32 v[76:77], v[80:81], s[44:45], v[76:77] op_sel_hi:[1,0,1]
	v_pk_fma_f32 v[74:75], v[78:79], s[44:45], v[74:75] op_sel_hi:[1,0,1]
	v_pk_add_f32 v[70:71], v[70:71], v[70:71] op_sel:[0,1] op_sel_hi:[1,0]
	v_add_f32_e32 v78, v74, v75
	v_add_f32_e32 v80, v76, v77
	v_mov_b32_e32 v79, v68
	v_mov_b32_e32 v81, v69
	v_mov_b32_e32 v71, v66
	v_mov_b32_e32 v91, v67
	v_pk_add_f32 v[72:73], v[78:79], v[80:81]
	v_pk_add_f32 v[70:71], v[70:71], v[90:91]
	s_nop 0
	v_pk_add_f32 v[70:71], v[70:71], v[72:73]
	s_nop 0
	v_add_f32_e32 v70, v70, v71
	s_nop 1
	v_mov_b32_dpp v71, v70 quad_perm:[1,0,3,2] row_mask:0xf bank_mask:0xf
	s_waitcnt vmcnt(15)
	v_pk_add_f32 v[60:61], v[60:61], 1.0 op_sel_hi:[1,0]
	v_pk_add_f32 v[58:59], v[58:59], 1.0 op_sel_hi:[1,0]
	s_waitcnt vmcnt(14)
	v_pk_add_f32 v[52:53], v[52:53], 1.0 op_sel_hi:[1,0]
	v_pk_add_f32 v[50:51], v[50:51], 1.0 op_sel_hi:[1,0]
	s_waitcnt lgkmcnt(0)
	v_add_f32_e32 v70, v70, v71
	s_nop 1
	v_mov_b32_dpp v71, v70 quad_perm:[2,3,0,1] row_mask:0xf bank_mask:0xf
	s_waitcnt vmcnt(11)
	v_pk_add_f32 v[44:45], v[44:45], 1.0 op_sel_hi:[1,0]
	v_pk_add_f32 v[42:43], v[42:43], 1.0 op_sel_hi:[1,0]
	s_waitcnt vmcnt(10)
	v_pk_add_f32 v[36:37], v[36:37], 1.0 op_sel_hi:[1,0]
	v_pk_add_f32 v[34:35], v[34:35], 1.0 op_sel_hi:[1,0]
	s_waitcnt lgkmcnt(0)
	v_add_f32_e32 v70, v70, v71
	s_nop 1
	v_mov_b32_dpp v71, v70 row_half_mirror row_mask:0xf bank_mask:0xf
	s_waitcnt vmcnt(7)
	v_pk_add_f32 v[28:29], v[28:29], 1.0 op_sel_hi:[1,0]
	v_pk_add_f32 v[26:27], v[26:27], 1.0 op_sel_hi:[1,0]
	s_waitcnt vmcnt(6)
	v_pk_add_f32 v[20:21], v[20:21], 1.0 op_sel_hi:[1,0]
	v_pk_add_f32 v[18:19], v[18:19], 1.0 op_sel_hi:[1,0]
	s_waitcnt lgkmcnt(0)
	v_add_f32_e32 v70, v70, v71
	s_nop 1
	v_mov_b32_dpp v71, v70 row_mirror row_mask:0xf bank_mask:0xf
	s_waitcnt vmcnt(3)
	v_pk_add_f32 v[12:13], v[12:13], 1.0 op_sel_hi:[1,0]
	v_pk_add_f32 v[10:11], v[10:11], 1.0 op_sel_hi:[1,0]
	s_waitcnt vmcnt(2)
	v_pk_add_f32 v[2:3], v[2:3], 1.0 op_sel_hi:[1,0]
	v_pk_add_f32 v[4:5], v[4:5], 1.0 op_sel_hi:[1,0]
	s_waitcnt lgkmcnt(0)
	v_add_f32_e32 v70, v70, v71
	v_mov_b32_e32 v71, v70
	v_mov_b32_e32 v197, v70
	s_nop 1
	v_permlane16_swap_b32_e32 v71, v197
	s_nop 1
	v_mov_b32_dpp v71, v197 quad_perm:[0,1,2,3] row_mask:0x5 bank_mask:0xf
	s_waitcnt lgkmcnt(0)
	v_add_f32_e32 v70, v70, v71
	v_mov_b32_e32 v71, v70
	v_mov_b32_e32 v198, v70
	s_nop 1
	v_permlane32_swap_b32_e32 v71, v198
	s_nop 1
	v_mov_b32_dpp v71, v198 quad_perm:[0,1,2,3] row_mask:0x3 bank_mask:0xf
	s_waitcnt lgkmcnt(0)
	v_add_f32_e32 v96, v70, v71
	v_fmamk_f32 v125, v96, 0xba000000, v125
	v_fmamk_f32 v147, v96, 0xba000000, v147
	v_fmamk_f32 v121, v96, 0xba000000, v121
	v_fmamk_f32 v123, v96, 0xba000000, v123
	v_fmac_f32_e32 v124, 0xba000000, v96
	v_fmac_f32_e32 v146, 0xba000000, v96
	v_fmac_f32_e32 v120, 0xba000000, v96
	v_fmac_f32_e32 v122, 0xba000000, v96
	v_mov_b32_e32 v72, v147
	v_mov_b32_e32 v73, v123
	v_mov_b32_e32 v80, v125
	v_mov_b32_e32 v81, v121
	v_mov_b32_e32 v70, v146
	v_mov_b32_e32 v71, v122
	v_mov_b32_e32 v78, v124
	v_mov_b32_e32 v79, v120
	v_pk_mul_f32 v[72:73], v[72:73], v[72:73]
	v_pk_mul_f32 v[80:81], v[80:81], v[80:81]
	v_pk_fma_f32 v[70:71], v[70:71], v[70:71], v[72:73]
	v_pk_fma_f32 v[72:73], v[78:79], v[78:79], v[80:81]
	v_fmamk_f32 v111, v96, 0xba000000, v111
	v_fmac_f32_e32 v110, 0xba000000, v96
	v_fmamk_f32 v113, v96, 0xba000000, v113
	v_fmac_f32_e32 v112, 0xba000000, v96
	v_pk_add_f32 v[70:71], v[70:71], v[72:73]
	v_pk_mul_f32 v[90:91], v[112:113], v[112:113]
	v_pk_mul_f32 v[92:93], v[110:111], v[110:111]
	v_pk_add_f32 v[70:71], v[70:71], v[70:71] op_sel_hi:[0,1]
	v_fmac_f32_e32 v106, 0xba000000, v96
	v_pk_mov_b32 v[94:95], v[92:93], v[90:91] op_sel:[1,0]
	v_mov_b32_e32 v93, v91
	v_fmamk_f32 v107, v96, 0xba000000, v107
	v_fmac_f32_e32 v108, 0xba000000, v96
	v_mul_f32_e32 v70, v106, v106
	v_pk_add_f32 v[72:73], v[94:95], v[92:93]
	v_fmamk_f32 v109, v96, 0xba000000, v109
	v_pk_fma_f32 v[78:79], v[106:107], v[106:107], v[70:71] op_sel_hi:[1,1,0]
	v_mul_f32_e32 v70, v108, v108
	v_pk_add_f32 v[72:73], v[72:73], v[72:73] op_sel_hi:[0,1]
	v_pk_fma_f32 v[80:81], v[108:109], v[108:109], v[70:71] op_sel_hi:[1,1,0]
	v_fmamk_f32 v89, v96, 0xba000000, v89
	v_fmac_f32_e32 v88, 0xba000000, v96
	v_fmamk_f32 v87, v96, 0xba000000, v87
	v_fmac_f32_e32 v86, 0xba000000, v96
	v_mul_f32_e32 v78, v86, v86
	v_mul_f32_e32 v80, v87, v87
	v_mul_f32_e32 v72, v88, v88
	v_mul_f32_e32 v70, v89, v89
	v_pk_add_f32 v[78:79], v[78:79], v[80:81]
	v_pk_add_f32 v[70:71], v[72:73], v[70:71]
	v_fmamk_f32 v83, v96, 0xba000000, v83
	v_pk_add_f32 v[70:71], v[78:79], v[70:71]
	v_fmac_f32_e32 v82, 0xba000000, v96
	v_fmamk_f32 v85, v96, 0xba000000, v85
	v_fmac_f32_e32 v84, 0xba000000, v96
	v_pk_add_f32 v[70:71], v[70:71], v[70:71] op_sel_hi:[0,1]
	v_pk_mul_f32 v[72:73], v[84:85], v[84:85]
	v_pk_mul_f32 v[78:79], v[82:83], v[82:83]
	v_fmac_f32_e32 v74, 0xba000000, v96
	v_pk_mov_b32 v[80:81], v[78:79], v[72:73] op_sel:[1,0]
	v_mov_b32_e32 v79, v73
	v_fmamk_f32 v75, v96, 0xba000000, v75
	v_fmac_f32_e32 v76, 0xba000000, v96
	v_mul_f32_e32 v70, v74, v74
	v_pk_add_f32 v[72:73], v[80:81], v[78:79]
	v_fmamk_f32 v77, v96, 0xba000000, v77
	v_pk_fma_f32 v[78:79], v[74:75], v[74:75], v[70:71] op_sel_hi:[1,1,0]
	v_mul_f32_e32 v70, v76, v76
	v_pk_add_f32 v[72:73], v[72:73], v[72:73] op_sel_hi:[0,1]
	v_pk_fma_f32 v[80:81], v[76:77], v[76:77], v[70:71] op_sel_hi:[1,1,0]
	v_fmamk_f32 v69, v96, 0xba000000, v69
	v_fmac_f32_e32 v68, 0xba000000, v96
	v_fmamk_f32 v67, v96, 0xba000000, v67
	v_fmac_f32_e32 v66, 0xba000000, v96
	v_mul_f32_e32 v78, v66, v66
	v_mul_f32_e32 v80, v67, v67
	v_mul_f32_e32 v72, v68, v68
	v_mul_f32_e32 v70, v69, v69
	v_pk_add_f32 v[78:79], v[78:79], v[80:81]
	v_pk_add_f32 v[70:71], v[72:73], v[70:71]
	s_nop 0
	v_pk_add_f32 v[70:71], v[78:79], v[70:71]
	s_nop 0
	v_add_f32_e32 v70, v70, v71
	s_nop 1
	v_mov_b32_dpp v71, v70 quad_perm:[1,0,3,2] row_mask:0xf bank_mask:0xf
	s_waitcnt lgkmcnt(0)
	v_add_f32_e32 v70, v70, v71
	s_nop 1
	v_mov_b32_dpp v71, v70 quad_perm:[2,3,0,1] row_mask:0xf bank_mask:0xf
	s_waitcnt lgkmcnt(0)
	v_add_f32_e32 v70, v70, v71
	s_nop 1
	v_mov_b32_dpp v71, v70 row_half_mirror row_mask:0xf bank_mask:0xf
	s_waitcnt lgkmcnt(0)
	v_add_f32_e32 v70, v70, v71
	s_nop 1
	v_mov_b32_dpp v71, v70 row_mirror row_mask:0xf bank_mask:0xf
	s_waitcnt lgkmcnt(0)
	v_add_f32_e32 v70, v70, v71
	v_mov_b32_e32 v71, v70
	v_mov_b32_e32 v197, v70
	s_nop 1
	v_permlane16_swap_b32_e32 v71, v197
	s_nop 1
	v_mov_b32_dpp v71, v197 quad_perm:[0,1,2,3] row_mask:0x5 bank_mask:0xf
	s_waitcnt lgkmcnt(0)
	v_add_f32_e32 v70, v70, v71
	v_mov_b32_e32 v71, v70
	v_mov_b32_e32 v198, v70
	s_nop 1
	v_permlane32_swap_b32_e32 v71, v198
	s_nop 1
	v_mov_b32_dpp v71, v198 quad_perm:[0,1,2,3] row_mask:0x3 bank_mask:0xf
	s_waitcnt lgkmcnt(0)
	v_add_f32_e32 v70, v70, v71
	v_fmamk_f32 v70, v70, 0x3a000000, v189
	v_mul_f32_e32 v71, 0x4f800000, v70
	v_cmp_gt_f32_e32 vcc, s75, v70
	s_nop 1
	v_cndmask_b32_e32 v70, v70, v71, vcc
	v_sqrt_f32_e32 v71, v70
	s_nop 0
	v_add_u32_e32 v72, -1, v71
	v_fma_f32 v73, -v72, v71, v70
	v_cmp_ge_f32_e64 s[0:1], 0, v73
	v_add_u32_e32 v73, 1, v71
	s_nop 0
	v_cndmask_b32_e64 v72, v71, v72, s[0:1]
	v_fma_f32 v71, -v73, v71, v70
	v_cmp_lt_f32_e64 s[0:1], 0, v71
	s_nop 1
	v_cndmask_b32_e64 v71, v72, v73, s[0:1]
	v_mul_f32_e32 v72, 0x37800000, v71
	v_cndmask_b32_e32 v71, v71, v72, vcc
	v_cmp_class_f32_e32 vcc, v70, v190
	s_nop 1
	v_cndmask_b32_e32 v70, v71, v70, vcc
	v_div_scale_f32 v71, s[0:1], v70, v70, 1.0
	v_rcp_f32_e32 v72, v71
	s_lshl_b64 s[0:1], s[14:15], 13
	s_add_u32 s0, s20, s0
	s_addc_u32 s1, s21, s1
	v_fma_f32 v73, -v71, v72, 1.0
	v_fmac_f32_e32 v72, v73, v72
	v_div_scale_f32 v73, vcc, 1.0, v70, 1.0
	v_mul_f32_e32 v78, v73, v72
	v_fma_f32 v79, -v71, v78, v73
	v_fmac_f32_e32 v78, v79, v72
	v_fma_f32 v71, -v71, v78, v73
	v_div_fmas_f32 v71, v71, v72, v78
	v_div_fixup_f32 v70, v71, v70, 1.0
	v_lshl_add_u32 v71, v116, 2, 0
	v_add_u32_e32 v96, 0x16800, v71
	v_add_u32_e32 v71, 0x18800, v71
	ds_read_b128 v[78:81], v96
	ds_read_b128 v[90:93], v71
	v_pk_mul_f32 v[94:95], v[124:125], v[70:71] op_sel_hi:[1,0]
	v_pk_mul_f32 v[72:73], v[146:147], v[70:71] op_sel_hi:[1,0]
	s_add_u32 s14, s51, s16
	s_addc_u32 s15, s58, s17
	s_waitcnt lgkmcnt(0)
	v_pk_fma_f32 v[80:81], v[80:81], v[94:95], v[92:93]
	v_pk_fma_f32 v[78:79], v[78:79], v[72:73], v[90:91]
	v_lshl_add_u64 v[72:73], s[0:1], 0, v[118:119]
	v_pk_fma_f32 v[60:61], v[60:61], v[80:81], v[64:65]
	global_store_dwordx4 v[72:73], v[78:81], off
	v_pk_fma_f32 v[58:59], v[58:59], v[78:79], v[62:63]
	v_pk_mul_f32 v[90:91], v[122:123], v[70:71] op_sel_hi:[1,0]
	v_cvt_pk_bf16_f32 v64, v58, v59
	v_cvt_pk_bf16_f32 v65, v60, v61
	ds_read_b128 v[60:63], v96 offset:1024
	ds_read_b128 v[78:81], v71 offset:1024
	v_lshl_add_u64 v[58:59], s[14:15], 0, v[114:115]
	global_store_dwordx2 v[58:59], v[64:65], off
	v_pk_mul_f32 v[64:65], v[120:121], v[70:71] op_sel_hi:[1,0]
	s_waitcnt lgkmcnt(0)
	v_pk_fma_f32 v[60:61], v[60:61], v[90:91], v[78:79]
	v_pk_fma_f32 v[62:63], v[62:63], v[64:65], v[80:81]
	v_pk_fma_f32 v[50:51], v[50:51], v[60:61], v[54:55]
	v_pk_fma_f32 v[52:53], v[52:53], v[62:63], v[56:57]
	global_store_dwordx4 v[72:73], v[60:63], off offset:1024
	s_nop 1
	v_cvt_pk_bf16_f32 v60, v50, v51
	v_cvt_pk_bf16_f32 v61, v52, v53
	ds_read_b128 v[50:53], v96 offset:2048
	ds_read_b128 v[54:57], v71 offset:2048
	global_store_dwordx2 v[58:59], v[60:61], off offset:512
	v_pk_mul_f32 v[60:61], v[112:113], v[70:71] op_sel_hi:[1,0]
	v_pk_mul_f32 v[62:63], v[110:111], v[70:71] op_sel_hi:[1,0]
	s_waitcnt lgkmcnt(0)
	v_pk_fma_f32 v[52:53], v[52:53], v[60:61], v[56:57]
	v_pk_fma_f32 v[50:51], v[50:51], v[62:63], v[54:55]
	v_pk_fma_f32 v[44:45], v[44:45], v[52:53], v[48:49]
	v_pk_fma_f32 v[42:43], v[42:43], v[50:51], v[46:47]
	global_store_dwordx4 v[72:73], v[50:53], off offset:2048
	s_nop 1
	v_cvt_pk_bf16_f32 v50, v42, v43
	v_cvt_pk_bf16_f32 v51, v44, v45
	ds_read_b128 v[42:45], v96 offset:3072
	ds_read_b128 v[46:49], v71 offset:3072
	global_store_dwordx2 v[58:59], v[50:51], off offset:1024
	v_pk_mul_f32 v[50:51], v[108:109], v[70:71] op_sel_hi:[1,0]
	v_pk_mul_f32 v[52:53], v[106:107], v[70:71] op_sel_hi:[1,0]
	s_waitcnt lgkmcnt(0)
	v_pk_fma_f32 v[44:45], v[44:45], v[50:51], v[48:49]
	v_pk_fma_f32 v[42:43], v[42:43], v[52:53], v[46:47]
	v_pk_fma_f32 v[36:37], v[36:37], v[44:45], v[40:41]
	v_pk_fma_f32 v[34:35], v[34:35], v[42:43], v[38:39]
	global_store_dwordx4 v[72:73], v[42:45], off offset:3072
	s_nop 1
	v_cvt_pk_bf16_f32 v42, v34, v35
	v_cvt_pk_bf16_f32 v43, v36, v37
	ds_read_b128 v[34:37], v96 offset:4096
	ds_read_b128 v[38:41], v71 offset:4096
	global_store_dwordx2 v[58:59], v[42:43], off offset:1536
	v_pk_mul_f32 v[42:43], v[88:89], v[70:71] op_sel_hi:[1,0]
	v_pk_mul_f32 v[44:45], v[86:87], v[70:71] op_sel_hi:[1,0]
	s_waitcnt lgkmcnt(0)
	v_pk_fma_f32 v[36:37], v[42:43], v[36:37], v[40:41]
	v_pk_fma_f32 v[34:35], v[44:45], v[34:35], v[38:39]
	v_add_co_u32_e32 v38, vcc, s74, v72
	v_pk_fma_f32 v[28:29], v[28:29], v[36:37], v[32:33]
	s_nop 0
	v_addc_co_u32_e32 v39, vcc, 0, v73, vcc
	v_pk_fma_f32 v[26:27], v[26:27], v[34:35], v[30:31]
	global_store_dwordx4 v[38:39], v[34:37], off
	s_nop 1
	v_cvt_pk_bf16_f32 v34, v26, v27
	v_cvt_pk_bf16_f32 v35, v28, v29
	ds_read_b128 v[26:29], v96 offset:5120
	ds_read_b128 v[30:33], v71 offset:5120
	global_store_dwordx2 v[58:59], v[34:35], off offset:2048
	v_pk_mul_f32 v[34:35], v[84:85], v[70:71] op_sel_hi:[1,0]
	v_pk_mul_f32 v[36:37], v[82:83], v[70:71] op_sel_hi:[1,0]
	s_waitcnt lgkmcnt(0)
	v_pk_fma_f32 v[28:29], v[34:35], v[28:29], v[32:33]
	v_pk_fma_f32 v[26:27], v[36:37], v[26:27], v[30:31]
	v_pk_fma_f32 v[20:21], v[20:21], v[28:29], v[24:25]
	v_pk_fma_f32 v[18:19], v[18:19], v[26:27], v[22:23]
	global_store_dwordx4 v[38:39], v[26:29], off offset:1024
	s_nop 1
	v_cvt_pk_bf16_f32 v26, v18, v19
	v_cvt_pk_bf16_f32 v27, v20, v21
	ds_read_b128 v[18:21], v96 offset:6144
	ds_read_b128 v[22:25], v71 offset:6144
	global_store_dwordx2 v[58:59], v[26:27], off offset:2560
	v_pk_mul_f32 v[26:27], v[76:77], v[70:71] op_sel_hi:[1,0]
	v_pk_mul_f32 v[28:29], v[74:75], v[70:71] op_sel_hi:[1,0]
	s_waitcnt lgkmcnt(0)
	v_pk_fma_f32 v[20:21], v[26:27], v[20:21], v[24:25]
	v_pk_fma_f32 v[18:19], v[28:29], v[18:19], v[22:23]
	s_waitcnt vmcnt(13)
	v_pk_fma_f32 v[12:13], v[12:13], v[20:21], v[16:17]
	v_pk_fma_f32 v[10:11], v[10:11], v[18:19], v[14:15]
	global_store_dwordx4 v[38:39], v[18:21], off offset:2048
	s_nop 1
	v_cvt_pk_bf16_f32 v18, v10, v11
	v_cvt_pk_bf16_f32 v19, v12, v13
	ds_read_b128 v[10:13], v96 offset:7168
	ds_read_b128 v[14:17], v71 offset:7168
	v_pk_mul_f32 v[20:21], v[66:67], v[70:71] op_sel_hi:[1,0]
	global_store_dwordx2 v[58:59], v[18:19], off offset:3072
	v_pk_mul_f32 v[18:19], v[68:69], v[70:71] op_sel_hi:[1,0]
	s_waitcnt lgkmcnt(0)
	v_pk_fma_f32 v[10:11], v[20:21], v[10:11], v[14:15]
	v_pk_fma_f32 v[12:13], v[18:19], v[12:13], v[16:17]
	s_waitcnt vmcnt(14)
	v_pk_fma_f32 v[2:3], v[2:3], v[10:11], v[6:7]
	global_store_dwordx4 v[38:39], v[10:13], off offset:3072
	v_pk_fma_f32 v[4:5], v[4:5], v[12:13], v[8:9]
	v_cvt_pk_bf16_f32 v2, v2, v3
	s_nop 0
	v_cvt_pk_bf16_f32 v3, v4, v5
	global_store_dwordx2 v[58:59], v[2:3], off offset:3584

.LBB0_1365:
	s_add_i32 s4, s39, s42
	s_add_i32 s43, s92, s42
	s_add_i32 s0, s41, s42
	s_cmp_lt_i32 s43, s12
	s_cselect_b64 s[20:21], -1, 0
	s_and_b64 s[18:19], s[20:21], exec
	s_cselect_b32 s18, s0, s4
	s_ashr_i32 s5, s4, 31
	s_lshl_b64 s[22:23], s[4:5], 13
	s_add_u32 s24, s2, s22
	s_addc_u32 s25, s17, s23
	s_ashr_i32 s19, s18, 31
	s_lshl_b64 s[18:19], s[18:19], 13
	s_add_u32 s44, s2, s18
	s_addc_u32 s45, s17, s19
	v_mov_b32_e32 v74, v216
	s_add_u32 s22, s26, s22
	s_addc_u32 s23, s27, s23
	v_ashrrev_i32_e32 v75, 31, v74
	v_lshlrev_b64 v[80:81], 1, v[74:75]
	s_add_u32 s18, s26, s18
	v_lshl_add_u64 v[66:67], s[22:23], 0, v[80:81]
	s_addc_u32 s19, s27, s19
	v_add_co_u32_e32 v70, vcc, s36, v66
	v_lshl_add_u64 v[72:73], s[18:19], 0, v[80:81]
	s_nop 0
	v_addc_co_u32_e32 v71, vcc, 0, v67, vcc
	v_lshlrev_b64 v[2:3], 2, v[74:75]
	v_add_co_u32_e32 v94, vcc, s36, v72
	v_lshl_add_u64 v[78:79], s[24:25], 0, v[2:3]
	s_nop 0
	v_addc_co_u32_e32 v95, vcc, 0, v73, vcc
	v_add_co_u32_e32 v76, vcc, s36, v78
	v_lshl_add_u64 v[2:3], s[44:45], 0, v[2:3]
	s_nop 0
	v_addc_co_u32_e32 v77, vcc, 0, v79, vcc
	global_load_dwordx4 v[58:61], v[78:79], off nt
	global_load_dwordx4 v[54:57], v[78:79], off offset:1024 nt
	global_load_dwordx4 v[62:65], v[2:3], off nt
	global_load_dwordx4 v[50:53], v[2:3], off offset:1024 nt
	global_load_dwordx4 v[42:45], v[78:79], off offset:2048 nt
	global_load_dwordx4 v[34:37], v[78:79], off offset:3072 nt
	global_load_dwordx4 v[46:49], v[2:3], off offset:2048 nt
	global_load_dwordx4 v[26:29], v[2:3], off offset:3072 nt
	global_load_dwordx2 v[140:141], v[66:67], off nt
	global_load_dwordx2 v[132:133], v[66:67], off offset:512 nt
	global_load_dwordx2 v[124:125], v[66:67], off offset:1024 nt
	global_load_dwordx2 v[112:113], v[66:67], off offset:1536 nt
	global_load_dwordx2 v[144:145], v[72:73], off nt
	global_load_dwordx2 v[130:131], v[72:73], off offset:512 nt
	global_load_dwordx2 v[122:123], v[72:73], off offset:1024 nt
	global_load_dwordx2 v[110:111], v[72:73], off offset:1536 nt
	v_add_co_u32_e32 v2, vcc, s36, v2
	v_lshl_add_u64 v[68:69], v[66:67], 0, s[14:15]
	v_lshl_add_u64 v[86:87], v[72:73], 0, s[14:15]
	v_addc_co_u32_e32 v3, vcc, 0, v3, vcc
	global_load_dwordx2 v[136:137], v[68:69], off offset:512 nt
	global_load_dwordx2 v[128:129], v[68:69], off offset:1024 nt
	global_load_dwordx2 v[120:121], v[68:69], off offset:1536 nt
	global_load_dwordx2 v[108:109], v[68:69], off offset:2048 nt
	global_load_dwordx2 v[134:135], v[86:87], off offset:512 nt
	global_load_dwordx2 v[126:127], v[86:87], off offset:1024 nt
	global_load_dwordx2 v[118:119], v[86:87], off offset:1536 nt
	global_load_dwordx2 v[106:107], v[86:87], off offset:2048 nt
	global_load_dwordx4 v[38:41], v[76:77], off nt
	global_load_dwordx4 v[22:25], v[76:77], off offset:1024 nt
	global_load_dwordx4 v[30:33], v[2:3], off nt
	global_load_dwordx4 v[18:21], v[2:3], off offset:1024 nt
	global_load_dwordx4 v[10:13], v[76:77], off offset:2048 nt
	global_load_dwordx4 v[6:9], v[76:77], off offset:3072 nt
	global_load_dwordx4 v[14:17], v[2:3], off offset:2048 nt
	s_nop 0
	global_load_dwordx4 v[2:5], v[2:3], off offset:3072 nt
	s_nop 0
	global_load_dwordx2 v[116:117], v[66:67], off offset:2048 nt
	global_load_dwordx2 v[100:101], v[66:67], off offset:2560 nt
	global_load_dwordx2 v[92:93], v[66:67], off offset:3072 nt
	global_load_dwordx2 v[84:85], v[66:67], off offset:3584 nt
	s_nop 0
	global_load_dwordx2 v[70:71], v[70:71], off nt
	s_nop 0
	global_load_dwordx2 v[104:105], v[68:69], off offset:2560 nt
	global_load_dwordx2 v[96:97], v[68:69], off offset:3072 nt
	global_load_dwordx2 v[88:89], v[68:69], off offset:3584 nt
	global_load_dwordx2 v[114:115], v[72:73], off offset:2048 nt
	global_load_dwordx2 v[98:99], v[72:73], off offset:2560 nt
	global_load_dwordx2 v[90:91], v[72:73], off offset:3072 nt
	global_load_dwordx2 v[82:83], v[72:73], off offset:3584 nt
	s_nop 0
	global_load_dwordx2 v[72:73], v[94:95], off nt
	global_load_dwordx2 v[102:103], v[86:87], off offset:2560 nt
	s_nop 0
	global_load_dwordx2 v[94:95], v[86:87], off offset:3072 nt
	s_nop 0
	global_load_dwordx2 v[86:87], v[86:87], off offset:3584 nt
	s_lshl_b64 s[4:5], s[4:5], 12
	s_add_u32 s22, s28, s4
	s_addc_u32 s23, s29, s5
	s_ashr_i32 s1, s0, 31
	s_lshl_b64 s[4:5], s[0:1], 13
	s_add_u32 s18, s2, s4
	s_addc_u32 s19, s17, s5
	s_lshl_b64 s[0:1], s[0:1], 12
	s_add_u32 s24, s28, s0
	s_addc_u32 s25, s29, s1
	s_cmp_ge_i32 s43, s12
	v_lshl_add_u32 v160, v74, 2, 0
	ds_read_b128 v[66:69], v160
	s_waitcnt vmcnt(39)
	v_lshlrev_b32_e32 v138, 16, v140
	v_and_b32_e32 v139, 0xffff0000, v140
	s_waitcnt vmcnt(11)
	v_lshlrev_b32_e32 v142, 16, v70
	v_and_b32_e32 v143, 0xffff0000, v70
	v_lshlrev_b32_e32 v140, 16, v141
	v_and_b32_e32 v141, 0xffff0000, v141
	v_lshlrev_b32_e32 v70, 16, v71
	v_and_b32_e32 v71, 0xffff0000, v71
	v_pk_add_f32 v[138:139], v[138:139], v[142:143]
	v_pk_add_f32 v[140:141], v[140:141], v[70:71]
	v_lshlrev_b32_e32 v70, 16, v144
	v_and_b32_e32 v71, 0xffff0000, v144
	s_waitcnt vmcnt(3)
	v_lshlrev_b32_e32 v142, 16, v72
	v_and_b32_e32 v143, 0xffff0000, v72
	v_pk_add_f32 v[142:143], v[70:71], v[142:143]
	v_lshlrev_b32_e32 v70, 16, v145
	v_and_b32_e32 v71, 0xffff0000, v145
	v_lshlrev_b32_e32 v72, 16, v73
	v_and_b32_e32 v73, 0xffff0000, v73
	v_pk_add_f32 v[144:145], v[70:71], v[72:73]
	ds_read_b128 v[70:73], v160 offset:32768
	s_waitcnt lgkmcnt(1)
	v_pk_mul_f32 v[138:139], v[138:139], v[66:67]
	v_pk_mul_f32 v[140:141], v[140:141], v[68:69]
	v_pk_fma_f32 v[148:149], v[58:59], s[16:17], v[138:139] op_sel_hi:[1,0,1]
	v_pk_fma_f32 v[146:147], v[60:61], s[16:17], v[140:141] op_sel_hi:[1,0,1]
	v_pk_mul_f32 v[58:59], v[142:143], v[66:67]
	v_pk_mul_f32 v[60:61], v[144:145], v[68:69]
	v_pk_fma_f32 v[140:141], v[62:63], s[16:17], v[58:59] op_sel_hi:[1,0,1]
	v_pk_fma_f32 v[138:139], v[64:65], s[16:17], v[60:61] op_sel_hi:[1,0,1]
	ds_read_b128 v[58:61], v160 offset:1024
	v_lshlrev_b32_e32 v62, 16, v132
	v_and_b32_e32 v63, 0xffff0000, v132
	v_lshlrev_b32_e32 v64, 16, v136
	v_and_b32_e32 v65, 0xffff0000, v136
	v_pk_add_f32 v[62:63], v[62:63], v[64:65]
	v_lshlrev_b32_e32 v64, 16, v133
	v_and_b32_e32 v65, 0xffff0000, v133
	v_lshlrev_b32_e32 v66, 16, v137
	v_and_b32_e32 v67, 0xffff0000, v137
	v_pk_add_f32 v[64:65], v[64:65], v[66:67]
	v_lshlrev_b32_e32 v66, 16, v130
	v_and_b32_e32 v67, 0xffff0000, v130
	v_lshlrev_b32_e32 v68, 16, v134
	v_and_b32_e32 v69, 0xffff0000, v134
	v_pk_add_f32 v[66:67], v[66:67], v[68:69]
	v_lshlrev_b32_e32 v68, 16, v131
	v_and_b32_e32 v69, 0xffff0000, v131
	v_lshlrev_b32_e32 v130, 16, v135
	v_and_b32_e32 v131, 0xffff0000, v135
	v_pk_add_f32 v[68:69], v[68:69], v[130:131]
	ds_read_b128 v[134:137], v160 offset:2048
	s_waitcnt lgkmcnt(1)
	v_pk_mul_f32 v[62:63], v[62:63], v[58:59]
	v_pk_mul_f32 v[64:65], v[64:65], v[60:61]
	v_pk_fma_f32 v[130:131], v[54:55], s[16:17], v[62:63] op_sel_hi:[1,0,1]
	v_pk_fma_f32 v[132:133], v[56:57], s[16:17], v[64:65] op_sel_hi:[1,0,1]
	v_pk_mul_f32 v[54:55], v[66:67], v[58:59]
	v_pk_mul_f32 v[56:57], v[68:69], v[60:61]
	v_pk_fma_f32 v[64:65], v[50:51], s[16:17], v[54:55] op_sel_hi:[1,0,1]
	v_pk_fma_f32 v[62:63], v[52:53], s[16:17], v[56:57] op_sel_hi:[1,0,1]
	v_mov_b32_e32 v50, v148
	v_mov_b32_e32 v51, v130
	v_mov_b32_e32 v52, v149
	v_mov_b32_e32 v53, v131
	v_pk_add_f32 v[50:51], v[50:51], v[52:53]
	v_mov_b32_e32 v52, v147
	v_mov_b32_e32 v53, v133
	v_mov_b32_e32 v54, v146
	v_mov_b32_e32 v55, v132
	v_pk_add_f32 v[52:53], v[52:53], v[54:55]
	v_mov_b32_e32 v54, v139
	v_pk_add_f32 v[50:51], v[50:51], v[52:53]
	v_mov_b32_e32 v52, v141
	v_add_f32_e32 v50, 0, v50
	v_add_f32_e32 v142, v50, v51
	v_mov_b32_e32 v50, v140
	v_mov_b32_e32 v51, v64
	v_mov_b32_e32 v53, v65
	v_pk_add_f32 v[50:51], v[50:51], v[52:53]
	v_mov_b32_e32 v52, v138
	v_mov_b32_e32 v53, v62
	v_mov_b32_e32 v55, v63
	v_pk_add_f32 v[52:53], v[52:53], v[54:55]
	v_lshlrev_b32_e32 v54, 16, v129
	v_pk_add_f32 v[50:51], v[50:51], v[52:53]
	v_lshlrev_b32_e32 v52, 16, v128
	v_add_f32_e32 v50, 0, v50
	v_add_f32_e32 v144, v50, v51
	v_lshlrev_b32_e32 v50, 16, v124
	v_and_b32_e32 v51, 0xffff0000, v124
	v_and_b32_e32 v53, 0xffff0000, v128
	v_pk_add_f32 v[50:51], v[50:51], v[52:53]
	v_lshlrev_b32_e32 v52, 16, v125
	v_and_b32_e32 v53, 0xffff0000, v125
	v_and_b32_e32 v55, 0xffff0000, v129
	v_pk_add_f32 v[52:53], v[52:53], v[54:55]
	v_lshlrev_b32_e32 v54, 16, v122
	v_and_b32_e32 v55, 0xffff0000, v122
	v_lshlrev_b32_e32 v56, 16, v126
	v_and_b32_e32 v57, 0xffff0000, v126
	v_pk_add_f32 v[54:55], v[54:55], v[56:57]
	v_lshlrev_b32_e32 v56, 16, v123
	v_and_b32_e32 v57, 0xffff0000, v123
	v_lshlrev_b32_e32 v58, 16, v127
	v_and_b32_e32 v59, 0xffff0000, v127
	v_pk_add_f32 v[56:57], v[56:57], v[58:59]
	s_waitcnt lgkmcnt(0)
	v_pk_mul_f32 v[50:51], v[50:51], v[134:135]
	v_pk_mul_f32 v[52:53], v[52:53], v[136:137]
	v_pk_fma_f32 v[66:67], v[42:43], s[16:17], v[50:51] op_sel_hi:[1,0,1]
	v_pk_fma_f32 v[68:69], v[44:45], s[16:17], v[52:53] op_sel_hi:[1,0,1]
	v_pk_mul_f32 v[42:43], v[54:55], v[134:135]
	v_pk_mul_f32 v[44:45], v[56:57], v[136:137]
	v_pk_fma_f32 v[58:59], v[46:47], s[16:17], v[42:43] op_sel_hi:[1,0,1]
	v_pk_fma_f32 v[56:57], v[48:49], s[16:17], v[44:45] op_sel_hi:[1,0,1]
	v_mov_b32_e32 v42, v66
	v_mov_b32_e32 v43, v69
	v_pk_mov_b32 v[44:45], v[66:67], v[68:69] op_sel:[1,0]
	v_lshlrev_b32_e32 v46, 16, v112
	v_pk_add_f32 v[42:43], v[42:43], v[44:45]
	v_mov_b32_e32 v44, v58
	v_pk_add_f32 v[122:123], v[42:43], v[42:43] op_sel:[0,1] op_sel_hi:[1,0]
	v_pk_mov_b32 v[42:43], v[58:59], v[56:57] op_sel:[1,0]
	v_mov_b32_e32 v45, v57
	v_pk_add_f32 v[42:43], v[42:43], v[44:45]
	v_and_b32_e32 v47, 0xffff0000, v112
	v_pk_add_f32 v[124:125], v[42:43], v[42:43] op_sel:[0,1] op_sel_hi:[1,0]
	ds_read_b128 v[42:45], v160 offset:3072
	v_lshlrev_b32_e32 v48, 16, v120
	v_and_b32_e32 v49, 0xffff0000, v120
	v_pk_add_f32 v[46:47], v[46:47], v[48:49]
	v_lshlrev_b32_e32 v48, 16, v113
	v_and_b32_e32 v49, 0xffff0000, v113
	v_lshlrev_b32_e32 v50, 16, v121
	v_and_b32_e32 v51, 0xffff0000, v121
	v_pk_add_f32 v[48:49], v[48:49], v[50:51]
	v_lshlrev_b32_e32 v50, 16, v110
	v_and_b32_e32 v51, 0xffff0000, v110
	v_lshlrev_b32_e32 v52, 16, v118
	v_and_b32_e32 v53, 0xffff0000, v118
	v_pk_add_f32 v[50:51], v[50:51], v[52:53]
	v_lshlrev_b32_e32 v52, 16, v111
	v_and_b32_e32 v53, 0xffff0000, v111
	v_lshlrev_b32_e32 v54, 16, v119
	v_and_b32_e32 v55, 0xffff0000, v119
	ds_read_b128 v[110:113], v160 offset:4096
	v_pk_add_f32 v[52:53], v[52:53], v[54:55]
	s_waitcnt lgkmcnt(1)
	v_pk_mul_f32 v[46:47], v[46:47], v[42:43]
	v_pk_mul_f32 v[48:49], v[48:49], v[44:45]
	v_pk_fma_f32 v[54:55], v[34:35], s[16:17], v[46:47] op_sel_hi:[1,0,1]
	v_pk_fma_f32 v[60:61], v[36:37], s[16:17], v[48:49] op_sel_hi:[1,0,1]
	v_pk_mul_f32 v[34:35], v[50:51], v[42:43]
	v_pk_mul_f32 v[36:37], v[52:53], v[44:45]
	v_lshlrev_b32_e32 v42, 16, v116
	v_and_b32_e32 v43, 0xffff0000, v116
	v_lshlrev_b32_e32 v44, 16, v108
	v_and_b32_e32 v45, 0xffff0000, v108
	v_pk_add_f32 v[42:43], v[42:43], v[44:45]
	v_lshlrev_b32_e32 v44, 16, v117
	v_and_b32_e32 v45, 0xffff0000, v117
	v_lshlrev_b32_e32 v46, 16, v109
	v_and_b32_e32 v47, 0xffff0000, v109
	v_pk_add_f32 v[44:45], v[44:45], v[46:47]
	v_lshlrev_b32_e32 v46, 16, v114
	v_and_b32_e32 v47, 0xffff0000, v114
	v_lshlrev_b32_e32 v52, 16, v106
	v_and_b32_e32 v53, 0xffff0000, v106
	v_pk_add_f32 v[108:109], v[46:47], v[52:53]
	v_lshlrev_b32_e32 v46, 16, v115
	v_and_b32_e32 v47, 0xffff0000, v115
	v_lshlrev_b32_e32 v52, 16, v107
	v_and_b32_e32 v53, 0xffff0000, v107
	s_waitcnt lgkmcnt(0)
	v_pk_mul_f32 v[42:43], v[42:43], v[110:111]
	v_pk_mul_f32 v[44:45], v[44:45], v[112:113]
	v_pk_add_f32 v[106:107], v[46:47], v[52:53]
	v_pk_fma_f32 v[52:53], v[40:41], s[16:17], v[44:45] op_sel_hi:[1,0,1]
	v_pk_fma_f32 v[46:47], v[38:39], s[16:17], v[42:43] op_sel_hi:[1,0,1]
	v_pk_fma_f32 v[48:49], v[28:29], s[16:17], v[36:37] op_sel_hi:[1,0,1]
	v_pk_fma_f32 v[50:51], v[26:27], s[16:17], v[34:35] op_sel_hi:[1,0,1]
	v_add_f32_e32 v26, v54, v55
	v_add_f32_e32 v28, v61, v60
	v_pk_mul_f32 v[38:39], v[108:109], v[110:111]
	v_pk_mul_f32 v[40:41], v[106:107], v[112:113]
	v_mov_b32_e32 v143, v46
	v_mov_b32_e32 v123, v47
	v_mov_b32_e32 v27, v53
	v_mov_b32_e32 v29, v52
	v_pk_fma_f32 v[40:41], v[32:33], s[16:17], v[40:41] op_sel_hi:[1,0,1]
	v_pk_fma_f32 v[42:43], v[30:31], s[16:17], v[38:39] op_sel_hi:[1,0,1]
	v_pk_add_f32 v[30:31], v[142:143], v[122:123]
	v_pk_add_f32 v[26:27], v[26:27], v[28:29]
	v_add_f32_e32 v34, v50, v51
	v_add_f32_e32 v36, v48, v49
	v_pk_add_f32 v[26:27], v[30:31], v[26:27]
	v_mov_b32_e32 v145, v42
	v_mov_b32_e32 v125, v43
	v_mov_b32_e32 v35, v40
	v_mov_b32_e32 v37, v41
	v_pk_add_f32 v[106:107], v[26:27], v[26:27] op_sel:[0,1] op_sel_hi:[1,0]
	v_pk_add_f32 v[26:27], v[144:145], v[124:125]
	v_pk_add_f32 v[28:29], v[34:35], v[36:37]
	v_lshlrev_b32_e32 v30, 16, v100
	v_pk_add_f32 v[26:27], v[26:27], v[28:29]
	v_and_b32_e32 v31, 0xffff0000, v100
	v_pk_add_f32 v[108:109], v[26:27], v[26:27] op_sel:[0,1] op_sel_hi:[1,0]
	ds_read_b128 v[26:29], v160 offset:5120
	v_lshlrev_b32_e32 v32, 16, v104
	v_and_b32_e32 v33, 0xffff0000, v104
	v_pk_add_f32 v[30:31], v[30:31], v[32:33]
	v_lshlrev_b32_e32 v32, 16, v101
	v_and_b32_e32 v33, 0xffff0000, v101
	v_lshlrev_b32_e32 v34, 16, v105
	v_and_b32_e32 v35, 0xffff0000, v105
	v_pk_add_f32 v[32:33], v[32:33], v[34:35]
	v_lshlrev_b32_e32 v34, 16, v98
	v_and_b32_e32 v35, 0xffff0000, v98
	s_waitcnt vmcnt(2)
	v_lshlrev_b32_e32 v36, 16, v102
	v_and_b32_e32 v37, 0xffff0000, v102
	v_pk_add_f32 v[34:35], v[34:35], v[36:37]
	v_lshlrev_b32_e32 v36, 16, v99
	v_and_b32_e32 v37, 0xffff0000, v99
	v_lshlrev_b32_e32 v38, 16, v103
	v_and_b32_e32 v39, 0xffff0000, v103
	v_pk_add_f32 v[36:37], v[36:37], v[38:39]
	ds_read_b128 v[98:101], v160 offset:6144
	s_waitcnt lgkmcnt(1)
	v_pk_mul_f32 v[30:31], v[30:31], v[26:27]
	v_pk_mul_f32 v[32:33], v[32:33], v[28:29]
	v_pk_fma_f32 v[38:39], v[22:23], s[16:17], v[30:31] op_sel_hi:[1,0,1]
	v_pk_fma_f32 v[44:45], v[24:25], s[16:17], v[32:33] op_sel_hi:[1,0,1]
	v_pk_mul_f32 v[22:23], v[34:35], v[26:27]
	v_pk_mul_f32 v[24:25], v[36:37], v[28:29]
	v_pk_fma_f32 v[34:35], v[18:19], s[16:17], v[22:23] op_sel_hi:[1,0,1]
	v_pk_fma_f32 v[32:33], v[20:21], s[16:17], v[24:25] op_sel_hi:[1,0,1]
	v_mov_b32_e32 v18, v38
	v_mov_b32_e32 v19, v45
	v_pk_mov_b32 v[20:21], v[38:39], v[44:45] op_sel:[1,0]
	v_mov_b32_e32 v22, v34
	v_pk_add_f32 v[18:19], v[18:19], v[20:21]
	v_pk_mov_b32 v[20:21], v[34:35], v[32:33] op_sel:[1,0]
	v_mov_b32_e32 v23, v33
	v_pk_add_f32 v[20:21], v[20:21], v[22:23]
	v_lshlrev_b32_e32 v22, 16, v96
	v_pk_add_f32 v[102:103], v[20:21], v[20:21] op_sel:[0,1] op_sel_hi:[1,0]
	v_lshlrev_b32_e32 v20, 16, v92
	v_and_b32_e32 v21, 0xffff0000, v92
	v_and_b32_e32 v23, 0xffff0000, v96
	v_pk_add_f32 v[20:21], v[20:21], v[22:23]
	v_lshlrev_b32_e32 v22, 16, v93
	v_and_b32_e32 v23, 0xffff0000, v93
	v_lshlrev_b32_e32 v24, 16, v97
	v_and_b32_e32 v25, 0xffff0000, v97
	v_pk_add_f32 v[22:23], v[22:23], v[24:25]
	v_lshlrev_b32_e32 v24, 16, v90
	v_and_b32_e32 v25, 0xffff0000, v90
	s_waitcnt vmcnt(1)
	v_lshlrev_b32_e32 v26, 16, v94
	v_and_b32_e32 v27, 0xffff0000, v94
	v_pk_add_f32 v[24:25], v[24:25], v[26:27]
	v_lshlrev_b32_e32 v26, 16, v91
	v_and_b32_e32 v27, 0xffff0000, v91
	v_lshlrev_b32_e32 v28, 16, v95
	v_and_b32_e32 v29, 0xffff0000, v95
	v_pk_add_f32 v[26:27], v[26:27], v[28:29]
	s_waitcnt lgkmcnt(0)
	v_pk_mul_f32 v[20:21], v[20:21], v[98:99]
	v_pk_mul_f32 v[22:23], v[22:23], v[100:101]
	v_pk_fma_f32 v[30:31], v[10:11], s[16:17], v[20:21] op_sel_hi:[1,0,1]
	v_pk_fma_f32 v[36:37], v[12:13], s[16:17], v[22:23] op_sel_hi:[1,0,1]
	v_pk_mul_f32 v[10:11], v[24:25], v[98:99]
	v_pk_mul_f32 v[12:13], v[26:27], v[100:101]
	v_pk_fma_f32 v[28:29], v[14:15], s[16:17], v[10:11] op_sel_hi:[1,0,1]
	v_pk_fma_f32 v[26:27], v[16:17], s[16:17], v[12:13] op_sel_hi:[1,0,1]
	ds_read_b128 v[14:17], v160 offset:7168
	v_lshlrev_b32_e32 v10, 16, v84
	v_and_b32_e32 v11, 0xffff0000, v84
	v_lshlrev_b32_e32 v12, 16, v88
	v_and_b32_e32 v13, 0xffff0000, v88
	v_pk_add_f32 v[22:23], v[10:11], v[12:13]
	v_lshlrev_b32_e32 v10, 16, v85
	v_and_b32_e32 v11, 0xffff0000, v85
	v_lshlrev_b32_e32 v12, 16, v89
	v_and_b32_e32 v13, 0xffff0000, v89
	v_pk_add_f32 v[24:25], v[10:11], v[12:13]
	v_lshlrev_b32_e32 v10, 16, v82
	v_and_b32_e32 v11, 0xffff0000, v82
	s_waitcnt vmcnt(0)
	v_lshlrev_b32_e32 v12, 16, v86
	v_and_b32_e32 v13, 0xffff0000, v86
	v_pk_add_f32 v[84:85], v[10:11], v[12:13]
	v_lshlrev_b32_e32 v10, 16, v83
	v_and_b32_e32 v11, 0xffff0000, v83
	v_lshlrev_b32_e32 v12, 16, v87
	v_and_b32_e32 v13, 0xffff0000, v87
	v_pk_add_f32 v[82:83], v[10:11], v[12:13]
	ds_read_b128 v[10:13], v160 offset:8192
	s_waitcnt lgkmcnt(1)
	v_pk_mul_f32 v[22:23], v[22:23], v[14:15]
	v_pk_mul_f32 v[24:25], v[24:25], v[16:17]
	v_pk_add_f32 v[18:19], v[18:19], v[18:19] op_sel:[0,1] op_sel_hi:[1,0]
	v_pk_fma_f32 v[24:25], v[8:9], s[16:17], v[24:25] op_sel_hi:[1,0,1]
	v_pk_fma_f32 v[22:23], v[6:7], s[16:17], v[22:23] op_sel_hi:[1,0,1]
	v_add_f32_e32 v20, v30, v31
	v_add_f32_e32 v90, v37, v36
	v_mov_b32_e32 v107, v22
	v_mov_b32_e32 v19, v23
	v_mov_b32_e32 v21, v25
	v_mov_b32_e32 v91, v24
	v_pk_add_f32 v[6:7], v[106:107], v[18:19]
	v_pk_add_f32 v[8:9], v[20:21], v[90:91]
	v_cmp_lt_i32_e32 vcc, v152, v151
	v_pk_add_f32 v[6:7], v[6:7], v[8:9]
	v_pk_mul_f32 v[8:9], v[82:83], v[16:17]
	v_add_f32_e32 v86, v6, v7
	v_cndmask_b32_e32 v6, v150, v152, vcc
	v_lshlrev_b32_e32 v96, 2, v6
	s_nop 1
	v_mov_b32_dpp v87, v86 quad_perm:[1,0,3,2] row_mask:0xf bank_mask:0xf
	v_pk_mul_f32 v[6:7], v[84:85], v[14:15]
	v_cmp_lt_i32_e32 vcc, v153, v151
	v_pk_fma_f32 v[20:21], v[2:3], s[16:17], v[6:7] op_sel_hi:[1,0,1]
	v_pk_fma_f32 v[18:19], v[4:5], s[16:17], v[8:9] op_sel_hi:[1,0,1]
	v_cndmask_b32_e32 v2, v150, v153, vcc
	s_waitcnt lgkmcnt(0)
	v_add_f32_e32 v4, v86, v87
	v_lshlrev_b32_e32 v97, 2, v2
	s_nop 1
	v_mov_b32_dpp v5, v4 quad_perm:[2,3,0,1] row_mask:0xf bank_mask:0xf
	v_cmp_lt_i32_e32 vcc, v154, v151
	v_add_f32_e32 v92, v28, v29
	v_add_f32_e32 v94, v26, v27
	v_mov_b32_e32 v109, v20
	v_mov_b32_e32 v103, v21
	v_mov_b32_e32 v93, v18
	s_waitcnt lgkmcnt(0)
	v_add_f32_e32 v6, v4, v5
	v_cndmask_b32_e32 v4, v150, v154, vcc
	v_mov_b32_e32 v95, v19
	v_pk_add_f32 v[2:3], v[108:109], v[102:103]
	v_lshlrev_b32_e32 v98, 2, v4
	v_pk_add_f32 v[4:5], v[92:93], v[94:95]
	s_nop 1
	v_mov_b32_dpp v7, v6 row_half_mirror row_mask:0xf bank_mask:0xf
	v_pk_add_f32 v[2:3], v[2:3], v[4:5]
	v_cmp_lt_i32_e32 vcc, v155, v151
	v_add_f32_e32 v2, v2, v3
	s_nop 1
	v_mov_b32_dpp v4, v2 quad_perm:[1,0,3,2] row_mask:0xf bank_mask:0xf
	v_cndmask_b32_e32 v5, v150, v155, vcc
	s_waitcnt lgkmcnt(1)
	v_add_f32_e32 v3, v6, v7
	v_lshlrev_b32_e32 v94, 2, v5
	s_nop 1
	v_mov_b32_dpp v5, v3 row_mirror row_mask:0xf bank_mask:0xf
	s_waitcnt lgkmcnt(1)
	v_add_f32_e32 v2, v2, v4
	s_nop 1
	v_mov_b32_dpp v4, v2 quad_perm:[2,3,0,1] row_mask:0xf bank_mask:0xf
	v_cmp_lt_i32_e32 vcc, v156, v151
	s_waitcnt lgkmcnt(1)
	v_add_f32_e32 v3, v3, v5
	v_cndmask_b32_e32 v5, v150, v156, vcc
	s_waitcnt lgkmcnt(0)
	v_add_f32_e32 v2, v2, v4
	s_nop 1
	v_mov_b32_dpp v4, v2 row_half_mirror row_mask:0xf bank_mask:0xf
	v_lshlrev_b32_e32 v95, 2, v5
	v_mov_b32_e32 v5, v3
	v_mov_b32_e32 v95, v3
	s_nop 1
	v_permlane16_swap_b32_e32 v5, v95
	s_nop 1
	v_mov_b32_dpp v5, v95 quad_perm:[0,1,2,3] row_mask:0x5 bank_mask:0xf
	v_cmp_lt_i32_e32 vcc, v157, v151
	s_waitcnt lgkmcnt(1)
	v_add_f32_e32 v2, v2, v4
	s_nop 1
	v_mov_b32_dpp v4, v2 row_mirror row_mask:0xf bank_mask:0xf
	s_waitcnt lgkmcnt(1)
	v_add_f32_e32 v3, v3, v5
	v_cndmask_b32_e32 v5, v150, v157, vcc
	v_lshlrev_b32_e32 v99, 2, v5
	v_mov_b32_e32 v5, v3
	v_mov_b32_e32 v99, v3
	s_nop 1
	v_permlane32_swap_b32_e32 v5, v99
	s_nop 1
	v_mov_b32_dpp v5, v99 quad_perm:[0,1,2,3] row_mask:0x3 bank_mask:0xf
	s_waitcnt lgkmcnt(1)
	v_add_f32_e32 v2, v2, v4
	v_mov_b32_e32 v4, v2
	v_mov_b32_e32 v95, v2
	s_nop 1
	v_permlane16_swap_b32_e32 v4, v95
	s_nop 1
	v_mov_b32_dpp v4, v95 quad_perm:[0,1,2,3] row_mask:0x5 bank_mask:0xf
	s_waitcnt lgkmcnt(1)
	v_add_f32_e32 v100, v3, v5
	v_fmamk_f32 v149, v100, 0xba000000, v149
	s_waitcnt lgkmcnt(0)
	v_add_f32_e32 v2, v2, v4
	v_mov_b32_e32 v4, v2
	v_mov_b32_e32 v99, v2
	s_nop 1
	v_permlane32_swap_b32_e32 v4, v99
	s_nop 1
	v_mov_b32_dpp v4, v99 quad_perm:[0,1,2,3] row_mask:0x3 bank_mask:0xf
	v_fmac_f32_e32 v148, 0xba000000, v100
	v_fmamk_f32 v17, v100, 0xba000000, v131
	v_fmac_f32_e32 v130, 0xba000000, v100
	v_mov_b32_e32 v16, v149
	s_waitcnt lgkmcnt(0)
	v_add_f32_e32 v101, v2, v4
	v_fmac_f32_e32 v146, 0xba000000, v100
	v_fmac_f32_e32 v132, 0xba000000, v100
	v_mov_b32_e32 v2, v148
	v_mov_b32_e32 v3, v130
	v_pk_mul_f32 v[4:5], v[16:17], v[16:17]
	v_fmamk_f32 v147, v100, 0xba000000, v147
	v_pk_fma_f32 v[2:3], v[2:3], v[2:3], v[4:5]
	v_mov_b32_e32 v4, v146
	v_mov_b32_e32 v5, v132
	v_fmamk_f32 v15, v100, 0xba000000, v133
	v_pk_mul_f32 v[4:5], v[4:5], v[4:5]
	v_mov_b32_e32 v14, v147
	v_fmamk_f32 v88, v101, 0xba000000, v139
	v_fmamk_f32 v90, v101, 0xba000000, v141
	v_fmamk_f32 v89, v101, 0xba000000, v63
	v_fmac_f32_e32 v62, 0xba000000, v101
	v_fmamk_f32 v91, v101, 0xba000000, v65
	v_fmac_f32_e32 v64, 0xba000000, v101
	v_pk_fma_f32 v[4:5], v[14:15], v[14:15], v[4:5]
	v_fmac_f32_e32 v138, 0xba000000, v101
	v_fmac_f32_e32 v140, 0xba000000, v101
	v_pk_add_f32 v[2:3], v[2:3], v[4:5]
	v_mov_b32_e32 v141, v64
	v_pk_mul_f32 v[4:5], v[90:91], v[90:91]
	v_mov_b32_e32 v139, v62
	v_pk_mul_f32 v[6:7], v[88:89], v[88:89]
	v_pk_fma_f32 v[4:5], v[140:141], v[140:141], v[4:5]
	v_pk_fma_f32 v[6:7], v[138:139], v[138:139], v[6:7]
	v_fmamk_f32 v69, v100, 0xba000000, v69
	v_fmac_f32_e32 v68, 0xba000000, v100
	v_fmamk_f32 v67, v100, 0xba000000, v67
	v_fmac_f32_e32 v66, 0xba000000, v100
	v_pk_add_f32 v[4:5], v[4:5], v[6:7]
	v_pk_mul_f32 v[6:7], v[68:69], v[68:69]
	v_pk_mul_f32 v[8:9], v[66:67], v[66:67]
	v_fmamk_f32 v57, v101, 0xba000000, v57
	v_fmac_f32_e32 v56, 0xba000000, v101
	v_fmamk_f32 v59, v101, 0xba000000, v59
	v_fmac_f32_e32 v58, 0xba000000, v101
	v_pk_mov_b32 v[82:83], v[8:9], v[6:7] op_sel:[1,0]
	v_mov_b32_e32 v9, v7
	v_pk_add_f32 v[2:3], v[2:3], v[2:3] op_sel_hi:[0,1]
	v_pk_add_f32 v[6:7], v[8:9], v[82:83]
	v_pk_mul_f32 v[8:9], v[56:57], v[56:57]
	v_pk_mul_f32 v[82:83], v[58:59], v[58:59]
	v_fmac_f32_e32 v54, 0xba000000, v100
	v_pk_mov_b32 v[84:85], v[82:83], v[8:9] op_sel:[1,0]
	v_mov_b32_e32 v83, v9
	v_fmac_f32_e32 v60, 0xba000000, v100
	v_fmamk_f32 v55, v100, 0xba000000, v55
	v_mul_f32_e32 v2, v54, v54
	v_pk_add_f32 v[8:9], v[84:85], v[82:83]
	v_fmamk_f32 v61, v100, 0xba000000, v61
	v_fmac_f32_e32 v50, 0xba000000, v101
	v_pk_fma_f32 v[82:83], v[54:55], v[54:55], v[2:3] op_sel_hi:[1,1,0]
	v_mul_f32_e32 v2, v60, v60
	v_fmac_f32_e32 v48, 0xba000000, v101
	v_fmamk_f32 v51, v101, 0xba000000, v51
	v_pk_fma_f32 v[84:85], v[60:61], v[60:61], v[2:3] op_sel_hi:[1,1,0]
	v_mul_f32_e32 v2, v50, v50
	v_pk_add_f32 v[6:7], v[6:7], v[6:7] op_sel_hi:[0,1]
	v_fmamk_f32 v49, v101, 0xba000000, v49
	v_pk_fma_f32 v[86:87], v[50:51], v[50:51], v[2:3] op_sel_hi:[1,1,0]
	v_mul_f32_e32 v2, v48, v48
	v_fmamk_f32 v53, v100, 0xba000000, v53
	v_fmac_f32_e32 v52, 0xba000000, v100
	v_fmamk_f32 v47, v100, 0xba000000, v47
	v_fmac_f32_e32 v46, 0xba000000, v100
	v_pk_add_f32 v[4:5], v[4:5], v[4:5] op_sel_hi:[0,1]
	v_pk_add_f32 v[8:9], v[8:9], v[8:9] op_sel_hi:[0,1]
	v_pk_fma_f32 v[92:93], v[48:49], v[48:49], v[2:3] op_sel_hi:[1,1,0]
	v_fmamk_f32 v41, v101, 0xba000000, v41
	v_fmac_f32_e32 v40, 0xba000000, v101
	v_fmamk_f32 v43, v101, 0xba000000, v43
	v_fmac_f32_e32 v42, 0xba000000, v101
	v_mul_f32_e32 v82, v46, v46
	v_mul_f32_e32 v84, v47, v47
	v_mul_f32_e32 v2, v52, v52
	v_mul_f32_e32 v6, v53, v53
	v_pk_add_f32 v[82:83], v[82:83], v[84:85]
	v_pk_add_f32 v[2:3], v[6:7], v[2:3]
	v_mul_f32_e32 v86, v42, v42
	v_mul_f32_e32 v92, v43, v43
	v_mul_f32_e32 v8, v40, v40
	v_mul_f32_e32 v4, v41, v41
	v_pk_add_f32 v[2:3], v[82:83], v[2:3]
	v_pk_add_f32 v[6:7], v[86:87], v[92:93]
	v_pk_add_f32 v[4:5], v[8:9], v[4:5]
	v_fmamk_f32 v45, v100, 0xba000000, v45
	v_fmac_f32_e32 v44, 0xba000000, v100
	v_fmamk_f32 v39, v100, 0xba000000, v39
	v_fmac_f32_e32 v38, 0xba000000, v100
	v_pk_add_f32 v[2:3], v[2:3], v[2:3] op_sel_hi:[0,1]
	v_pk_add_f32 v[4:5], v[6:7], v[4:5]
	v_pk_mul_f32 v[6:7], v[44:45], v[44:45]
	v_pk_mul_f32 v[8:9], v[38:39], v[38:39]
	v_fmac_f32_e32 v30, 0xba000000, v100
	v_pk_mov_b32 v[82:83], v[8:9], v[6:7] op_sel:[1,0]
	v_mov_b32_e32 v9, v7
	v_fmac_f32_e32 v36, 0xba000000, v100
	v_fmamk_f32 v31, v100, 0xba000000, v31
	v_mul_f32_e32 v2, v30, v30
	v_pk_add_f32 v[6:7], v[8:9], v[82:83]
	v_fmamk_f32 v37, v100, 0xba000000, v37
	v_pk_fma_f32 v[84:85], v[30:31], v[30:31], v[2:3] op_sel_hi:[1,1,0]
	v_mul_f32_e32 v2, v36, v36
	v_pk_add_f32 v[6:7], v[6:7], v[6:7] op_sel_hi:[0,1]
	v_pk_fma_f32 v[86:87], v[36:37], v[36:37], v[2:3] op_sel_hi:[1,1,0]
	v_fmamk_f32 v25, v100, 0xba000000, v25
	v_fmac_f32_e32 v24, 0xba000000, v100
	v_fmamk_f32 v23, v100, 0xba000000, v23
	v_fmac_f32_e32 v22, 0xba000000, v100
	v_mul_f32_e32 v84, v22, v22
	v_mul_f32_e32 v86, v23, v23
	v_mul_f32_e32 v2, v24, v24
	v_mul_f32_e32 v6, v25, v25
	v_pk_add_f32 v[84:85], v[84:85], v[86:87]
	v_pk_add_f32 v[2:3], v[6:7], v[2:3]
	v_pk_add_f32 v[4:5], v[4:5], v[4:5] op_sel_hi:[0,1]
	v_pk_add_f32 v[2:3], v[84:85], v[2:3]
	v_fmamk_f32 v33, v101, 0xba000000, v33
	v_add_f32_e32 v4, v2, v3
	v_fmac_f32_e32 v32, 0xba000000, v101
	v_fmamk_f32 v35, v101, 0xba000000, v35
	v_fmac_f32_e32 v34, 0xba000000, v101
	s_nop 1
	v_mov_b32_dpp v6, v4 quad_perm:[1,0,3,2] row_mask:0xf bank_mask:0xf
	v_pk_mul_f32 v[8:9], v[32:33], v[32:33]
	v_pk_mul_f32 v[82:83], v[34:35], v[34:35]
	v_fmac_f32_e32 v28, 0xba000000, v101
	v_pk_mov_b32 v[2:3], v[82:83], v[8:9] op_sel:[1,0]
	v_mov_b32_e32 v83, v9
	v_pk_add_f32 v[2:3], v[2:3], v[82:83]
	v_fmac_f32_e32 v26, 0xba000000, v101
	v_pk_add_f32 v[2:3], v[2:3], v[2:3] op_sel_hi:[0,1]
	s_waitcnt lgkmcnt(0)
	v_add_f32_e32 v2, v4, v6
	s_nop 1
	v_mov_b32_dpp v4, v2 quad_perm:[2,3,0,1] row_mask:0xf bank_mask:0xf
	v_fmamk_f32 v29, v101, 0xba000000, v29
	v_fmamk_f32 v27, v101, 0xba000000, v27
	v_fmamk_f32 v19, v101, 0xba000000, v19
	v_fmac_f32_e32 v18, 0xba000000, v101
	s_waitcnt lgkmcnt(0)
	v_add_f32_e32 v4, v2, v4
	s_nop 1
	v_mov_b32_dpp v14, v4 row_half_mirror row_mask:0xf bank_mask:0xf
	v_mul_f32_e32 v2, v28, v28
	v_pk_fma_f32 v[6:7], v[28:29], v[28:29], v[2:3] op_sel_hi:[1,1,0]
	v_mul_f32_e32 v2, v26, v26
	v_pk_fma_f32 v[8:9], v[26:27], v[26:27], v[2:3] op_sel_hi:[1,1,0]
	s_waitcnt lgkmcnt(0)
	v_add_f32_e32 v2, v4, v14
	s_nop 1
	v_mov_b32_dpp v4, v2 row_mirror row_mask:0xf bank_mask:0xf
	v_fmamk_f32 v21, v101, 0xba000000, v21
	v_fmac_f32_e32 v20, 0xba000000, v101
	v_mul_f32_e32 v6, v20, v20
	v_mul_f32_e32 v8, v21, v21
	s_waitcnt lgkmcnt(0)
	v_add_f32_e32 v14, v2, v4
	v_mul_f32_e32 v2, v18, v18
	v_mul_f32_e32 v4, v19, v19
	v_pk_add_f32 v[6:7], v[6:7], v[8:9]
	v_pk_add_f32 v[2:3], v[2:3], v[4:5]
	v_mov_b32_e32 v16, v14
	v_mov_b32_e32 v95, v14
	s_nop 1
	v_permlane16_swap_b32_e32 v16, v95
	s_nop 1
	v_mov_b32_dpp v16, v95 quad_perm:[0,1,2,3] row_mask:0x5 bank_mask:0xf
	v_pk_add_f32 v[2:3], v[6:7], v[2:3]
	s_waitcnt lgkmcnt(0)
	v_add_f32_e32 v14, v14, v16
	v_add_f32_e32 v2, v2, v3
	s_nop 1
	v_mov_b32_dpp v5, v2 quad_perm:[1,0,3,2] row_mask:0xf bank_mask:0xf
	v_mov_b32_e32 v16, v14
	v_mov_b32_e32 v99, v14
	s_nop 1
	v_permlane32_swap_b32_e32 v16, v99
	s_nop 1
	v_mov_b32_dpp v16, v99 quad_perm:[0,1,2,3] row_mask:0x3 bank_mask:0xf
	s_waitcnt lgkmcnt(1)
	v_add_f32_e32 v2, v2, v5
	s_nop 1
	v_mov_b32_dpp v5, v2 quad_perm:[2,3,0,1] row_mask:0xf bank_mask:0xf
	s_waitcnt lgkmcnt(1)
	v_add_f32_e32 v3, v14, v16
	v_fmamk_f32 v3, v3, 0x3a000000, v158
	v_mul_f32_e32 v4, 0x4f800000, v3
	v_cmp_gt_f32_e32 vcc, s38, v3
	s_waitcnt lgkmcnt(0)
	v_add_f32_e32 v2, v2, v5
	s_nop 1
	v_mov_b32_dpp v5, v2 row_half_mirror row_mask:0xf bank_mask:0xf
	v_cndmask_b32_e32 v3, v3, v4, vcc
	v_sqrt_f32_e32 v4, v3
	s_waitcnt lgkmcnt(0)
	v_add_f32_e32 v2, v2, v5
	s_nop 1
	v_mov_b32_dpp v5, v2 row_mirror row_mask:0xf bank_mask:0xf
	v_add_u32_e32 v6, -1, v4
	v_fma_f32 v7, -v6, v4, v3
	v_cmp_ge_f32_e64 s[0:1], 0, v7
	v_add_u32_e32 v7, 1, v4
	s_waitcnt lgkmcnt(0)
	v_add_f32_e32 v2, v2, v5
	v_mov_b32_e32 v5, v2
	v_mov_b32_e32 v95, v2
	s_nop 1
	v_permlane16_swap_b32_e32 v5, v95
	s_nop 1
	v_mov_b32_dpp v5, v95 quad_perm:[0,1,2,3] row_mask:0x5 bank_mask:0xf
	v_cndmask_b32_e64 v6, v4, v6, s[0:1]
	v_fma_f32 v4, -v7, v4, v3
	v_cmp_lt_f32_e64 s[0:1], 0, v4
	s_waitcnt lgkmcnt(0)
	v_add_f32_e32 v2, v2, v5
	v_cndmask_b32_e64 v4, v6, v7, s[0:1]
	v_mul_f32_e32 v6, 0x37800000, v4
	v_mov_b32_e32 v5, v2
	v_mov_b32_e32 v99, v2
	s_nop 1
	v_permlane32_swap_b32_e32 v5, v99
	s_nop 1
	v_mov_b32_dpp v5, v99 quad_perm:[0,1,2,3] row_mask:0x3 bank_mask:0xf
	v_cndmask_b32_e32 v4, v4, v6, vcc
	v_cmp_class_f32_e32 vcc, v3, v159
	s_waitcnt lgkmcnt(0)
	v_add_f32_e32 v2, v2, v5
	v_cndmask_b32_e32 v3, v4, v3, vcc
	v_div_scale_f32 v4, s[0:1], v3, v3, 1.0
	v_rcp_f32_e32 v6, v4
	v_fmamk_f32 v2, v2, 0x3a000000, v158
	v_mul_f32_e32 v5, 0x4f800000, v2
	v_cmp_gt_f32_e64 s[0:1], s38, v2
	v_fma_f32 v7, -v4, v6, 1.0
	v_fmac_f32_e32 v6, v7, v6
	v_cndmask_b32_e64 v2, v2, v5, s[0:1]
	v_div_scale_f32 v7, vcc, 1.0, v3, 1.0
	v_sqrt_f32_e32 v5, v2
	v_mul_f32_e32 v8, v7, v6
	v_fma_f32 v9, -v4, v8, v7
	v_fmac_f32_e32 v8, v9, v6
	v_fma_f32 v4, -v4, v8, v7
	v_add_u32_e32 v7, -1, v5
	v_fma_f32 v9, -v7, v5, v2
	v_cmp_ge_f32_e64 s[4:5], 0, v9
	v_add_u32_e32 v9, 1, v5
	v_div_fmas_f32 v4, v4, v6, v8
	v_cndmask_b32_e64 v7, v5, v7, s[4:5]
	v_fma_f32 v5, -v9, v5, v2
	v_cmp_lt_f32_e64 s[4:5], 0, v5
	v_div_fixup_f32 v84, v4, v3, 1.0
	v_pk_mul_f32 v[86:87], v[148:149], v[84:85] op_sel_hi:[1,0]
	v_cndmask_b32_e64 v5, v7, v9, s[4:5]
	v_mul_f32_e32 v7, 0x37800000, v5
	v_cndmask_b32_e64 v5, v5, v7, s[0:1]
	v_cmp_class_f32_e64 s[0:1], v2, v159
	v_pk_mul_f32 v[92:93], v[146:147], v[84:85] op_sel_hi:[1,0]
	s_nop 0
	v_cndmask_b32_e64 v2, v5, v2, s[0:1]
	v_div_scale_f32 v5, s[0:1], v2, v2, 1.0
	v_rcp_f32_e32 v7, v5
	s_nop 0
	v_fma_f32 v3, -v5, v7, 1.0
	v_fmac_f32_e32 v7, v3, v7
	v_div_scale_f32 v3, vcc, 1.0, v2, 1.0
	v_mul_f32_e32 v4, v3, v7
	v_fma_f32 v6, -v5, v4, v3
	v_fmac_f32_e32 v4, v6, v7
	v_fma_f32 v3, -v5, v4, v3
	v_div_fmas_f32 v3, v3, v7, v4
	ds_read_b128 v[6:9], v160 offset:16384
	v_div_fixup_f32 v82, v3, v2, 1.0
	ds_read_b128 v[2:5], v160 offset:24576
	v_mov_b32_e32 v83, v82
	s_waitcnt lgkmcnt(1)
	v_pk_fma_f32 v[94:95], v[12:13], v[92:93], v[8:9]
	v_pk_fma_f32 v[92:93], v[10:11], v[86:87], v[6:7]
	global_store_dwordx4 v[78:79], v[92:95], off
	s_waitcnt lgkmcnt(0)
	v_pk_fma_f32 v[86:87], v[4:5], v[94:95], v[72:73]
	v_pk_fma_f32 v[92:93], v[2:3], v[92:93], v[70:71]
	s_nop 0
	v_cvt_pk_bf16_f32 v92, v92, v93
	v_cvt_pk_bf16_f32 v93, v86, v87
	v_lshl_add_u64 v[86:87], s[22:23], 0, v[80:81]
	global_store_dwordx2 v[86:87], v[92:93], off
	v_lshl_add_u64 v[92:93], v[74:75], 2, s[18:19]
	v_lshl_add_u64 v[80:81], v[74:75], 1, s[24:25]
	s_cbranch_scc1 .LBB0_1367
	v_mov_b32_e32 v141, v90
	v_mov_b32_e32 v94, v82
	v_mov_b32_e32 v95, v82
	v_mov_b32_e32 v139, v88
	v_pk_mul_f32 v[96:97], v[140:141], v[82:83]
	v_pk_mul_f32 v[94:95], v[138:139], v[94:95]
	v_pk_fma_f32 v[6:7], v[10:11], v[96:97], v[6:7]
	v_pk_fma_f32 v[8:9], v[12:13], v[94:95], v[8:9]
	v_pk_fma_f32 v[2:3], v[2:3], v[6:7], v[70:71]
	global_store_dwordx4 v[92:93], v[6:9], off
	v_pk_fma_f32 v[4:5], v[4:5], v[8:9], v[72:73]
	v_cvt_pk_bf16_f32 v2, v2, v3
	s_nop 0
	v_cvt_pk_bf16_f32 v3, v4, v5
	global_store_dwordx2 v[80:81], v[2:3], off

.LBB0_1826:
	s_ashr_i32 s39, s38, 31
	s_add_i32 s0, s38, 8
	s_lshl_b64 s[10:11], s[38:39], 13
	s_add_u32 s10, s2, s10
	s_addc_u32 s11, s31, s11
	s_ashr_i32 s1, s0, 31
	v_mov_b32_e32 v56, v216
	s_lshl_b64 s[40:41], s[0:1], 13
	s_add_u32 s72, s2, s40
	v_ashrrev_i32_e32 v57, 31, v56
	s_addc_u32 s73, s31, s41
	s_lshl_b64 s[40:41], s[38:39], 12
	v_lshlrev_b64 v[2:3], 2, v[56:57]
	s_add_u32 s74, s45, s40
	v_lshl_add_u64 v[40:41], s[10:11], 0, v[2:3]
	s_addc_u32 s75, s47, s41
	s_lshl_b64 s[42:43], s[0:1], 12
	v_add_co_u32_e32 v34, vcc, s54, v40
	s_add_u32 s0, s45, s42
	v_lshl_add_u64 v[38:39], s[72:73], 0, v[2:3]
	v_addc_co_u32_e32 v35, vcc, 0, v41, vcc
	s_addc_u32 s1, s47, s43
	v_lshlrev_b64 v[42:43], 1, v[56:57]
	v_add_co_u32_e32 v36, vcc, s54, v38
	v_lshl_add_u64 v[62:63], s[74:75], 0, v[42:43]
	v_lshl_add_u64 v[64:65], s[0:1], 0, v[42:43]
	global_load_dwordx4 v[44:47], v[40:41], off nt
	global_load_dwordx4 v[48:51], v[40:41], off offset:1024 nt
	global_load_dwordx4 v[52:55], v[38:39], off nt
	global_load_dwordx4 v[58:61], v[38:39], off offset:1024 nt
	global_load_dwordx4 v[68:71], v[40:41], off offset:2048 nt
	global_load_dwordx4 v[92:95], v[40:41], off offset:3072 nt
	global_load_dwordx4 v[96:99], v[38:39], off offset:2048 nt
	global_load_dwordx4 v[100:103], v[38:39], off offset:3072 nt
	global_load_dwordx2 v[66:67], v[62:63], off nt
	global_load_dwordx2 v[104:105], v[62:63], off offset:512 nt
	global_load_dwordx2 v[140:141], v[62:63], off offset:1024 nt
	global_load_dwordx2 v[142:143], v[62:63], off offset:1536 nt
	global_load_dwordx2 v[144:145], v[64:65], off nt
	global_load_dwordx2 v[146:147], v[64:65], off offset:512 nt
	global_load_dwordx2 v[148:149], v[64:65], off offset:1024 nt
	global_load_dwordx2 v[150:151], v[64:65], off offset:1536 nt
	v_addc_co_u32_e32 v37, vcc, 0, v39, vcc
	global_load_dwordx4 v[30:33], v[34:35], off nt
	global_load_dwordx4 v[22:25], v[34:35], off offset:1024 nt
	global_load_dwordx4 v[26:29], v[36:37], off nt
	global_load_dwordx4 v[18:21], v[36:37], off offset:1024 nt
	global_load_dwordx4 v[14:17], v[34:35], off offset:2048 nt
	global_load_dwordx4 v[6:9], v[34:35], off offset:3072 nt
	global_load_dwordx4 v[10:13], v[36:37], off offset:2048 nt
	global_load_dwordx4 v[2:5], v[36:37], off offset:3072 nt
	global_load_dwordx2 v[152:153], v[62:63], off offset:2048 nt
	global_load_dwordx2 v[86:87], v[62:63], off offset:2560 nt
	global_load_dwordx2 v[82:83], v[62:63], off offset:3072 nt
	global_load_dwordx2 v[78:79], v[62:63], off offset:3584 nt
	global_load_dwordx2 v[88:89], v[64:65], off offset:2048 nt
	global_load_dwordx2 v[84:85], v[64:65], off offset:2560 nt
	global_load_dwordx2 v[80:81], v[64:65], off offset:3072 nt
	global_load_dwordx2 v[76:77], v[64:65], off offset:3584 nt
	v_lshl_add_u32 v90, v56, 2, 0
	v_add_u32_e32 v91, 0x14800, v90
	ds_read_b128 v[72:75], v91
	ds_read_b128 v[116:119], v91 offset:1024
	s_waitcnt vmcnt(23)
	v_lshlrev_b32_e32 v56, 16, v66
	v_and_b32_e32 v57, 0xffff0000, v66
	v_lshlrev_b32_e32 v62, 16, v67
	v_and_b32_e32 v63, 0xffff0000, v67
	s_waitcnt lgkmcnt(1)
	v_pk_mul_f32 v[62:63], v[74:75], v[62:63]
	v_pk_mul_f32 v[56:57], v[72:73], v[56:57]
	v_pk_fma_f32 v[62:63], v[46:47], s[30:31], v[62:63] op_sel_hi:[1,0,1]
	v_pk_fma_f32 v[66:67], v[44:45], s[30:31], v[56:57] op_sel_hi:[1,0,1]
	s_waitcnt vmcnt(19)
	v_lshlrev_b32_e32 v44, 16, v144
	v_and_b32_e32 v45, 0xffff0000, v144
	v_lshlrev_b32_e32 v46, 16, v145
	v_and_b32_e32 v47, 0xffff0000, v145
	v_pk_mul_f32 v[46:47], v[74:75], v[46:47]
	v_pk_mul_f32 v[44:45], v[72:73], v[44:45]
	v_pk_fma_f32 v[56:57], v[54:55], s[30:31], v[46:47] op_sel_hi:[1,0,1]
	v_pk_fma_f32 v[64:65], v[52:53], s[30:31], v[44:45] op_sel_hi:[1,0,1]
	v_lshlrev_b32_e32 v44, 16, v104
	v_and_b32_e32 v45, 0xffff0000, v104
	v_lshlrev_b32_e32 v46, 16, v105
	v_and_b32_e32 v47, 0xffff0000, v105
	s_waitcnt lgkmcnt(0)
	v_pk_mul_f32 v[46:47], v[118:119], v[46:47]
	v_pk_mul_f32 v[52:53], v[116:117], v[44:45]
	v_pk_fma_f32 v[44:45], v[50:51], s[30:31], v[46:47] op_sel_hi:[1,0,1]
	v_pk_fma_f32 v[46:47], v[48:49], s[30:31], v[52:53] op_sel_hi:[1,0,1]
	s_waitcnt vmcnt(18)
	v_lshlrev_b32_e32 v48, 16, v146
	v_and_b32_e32 v49, 0xffff0000, v146
	v_lshlrev_b32_e32 v50, 16, v147
	v_and_b32_e32 v51, 0xffff0000, v147
	v_pk_mul_f32 v[50:51], v[118:119], v[50:51]
	v_pk_mul_f32 v[52:53], v[116:117], v[48:49]
	v_pk_fma_f32 v[48:49], v[60:61], s[30:31], v[50:51] op_sel_hi:[1,0,1]
	v_pk_fma_f32 v[50:51], v[58:59], s[30:31], v[52:53] op_sel_hi:[1,0,1]
	v_mov_b32_e32 v52, v66
	v_mov_b32_e32 v53, v46
	v_mov_b32_e32 v54, v67
	v_mov_b32_e32 v55, v47
	v_pk_add_f32 v[52:53], v[52:53], v[54:55]
	v_mov_b32_e32 v54, v63
	v_mov_b32_e32 v55, v45
	v_mov_b32_e32 v58, v62
	v_mov_b32_e32 v59, v44
	v_pk_add_f32 v[54:55], v[54:55], v[58:59]
	v_mov_b32_e32 v58, v57
	v_pk_add_f32 v[52:53], v[52:53], v[54:55]
	v_mov_b32_e32 v54, v65
	v_add_f32_e32 v52, 0, v52
	v_add_f32_e32 v104, v52, v53
	v_mov_b32_e32 v52, v64
	v_mov_b32_e32 v53, v50
	v_mov_b32_e32 v55, v51
	v_pk_add_f32 v[52:53], v[52:53], v[54:55]
	v_mov_b32_e32 v54, v56
	v_mov_b32_e32 v55, v48
	v_mov_b32_e32 v59, v49
	v_pk_add_f32 v[54:55], v[54:55], v[58:59]
	v_lshlrev_b32_e32 v72, 16, v140
	v_pk_add_f32 v[52:53], v[52:53], v[54:55]
	v_and_b32_e32 v73, 0xffff0000, v140
	v_add_f32_e32 v52, 0, v52
	v_add_f32_e32 v116, v52, v53
	ds_read_b128 v[52:55], v91 offset:2048
	ds_read_b128 v[58:61], v91 offset:3072
	v_lshlrev_b32_e32 v74, 16, v141
	v_and_b32_e32 v75, 0xffff0000, v141
	s_waitcnt vmcnt(7)
	v_lshlrev_b32_e32 v146, 16, v152
	s_waitcnt lgkmcnt(1)
	v_pk_mul_f32 v[74:75], v[54:55], v[74:75]
	v_pk_mul_f32 v[72:73], v[52:53], v[72:73]
	v_pk_fma_f32 v[74:75], v[70:71], s[30:31], v[74:75] op_sel_hi:[1,0,1]
	v_pk_fma_f32 v[72:73], v[68:69], s[30:31], v[72:73] op_sel_hi:[1,0,1]
	v_lshlrev_b32_e32 v68, 16, v148
	v_and_b32_e32 v69, 0xffff0000, v148
	v_lshlrev_b32_e32 v70, 16, v149
	v_and_b32_e32 v71, 0xffff0000, v149
	v_pk_mul_f32 v[54:55], v[54:55], v[70:71]
	v_pk_mul_f32 v[52:53], v[52:53], v[68:69]
	v_pk_fma_f32 v[70:71], v[98:99], s[30:31], v[54:55] op_sel_hi:[1,0,1]
	v_pk_fma_f32 v[68:69], v[96:97], s[30:31], v[52:53] op_sel_hi:[1,0,1]
	v_mov_b32_e32 v52, v72
	v_mov_b32_e32 v53, v75
	v_pk_mov_b32 v[54:55], v[72:73], v[74:75] op_sel:[1,0]
	v_and_b32_e32 v147, 0xffff0000, v152
	v_pk_add_f32 v[52:53], v[52:53], v[54:55]
	v_mov_b32_e32 v54, v68
	v_pk_add_f32 v[118:119], v[52:53], v[52:53] op_sel:[0,1] op_sel_hi:[1,0]
	v_pk_mov_b32 v[52:53], v[68:69], v[70:71] op_sel:[1,0]
	v_mov_b32_e32 v55, v71
	v_pk_add_f32 v[52:53], v[52:53], v[54:55]
	v_lshlrev_b32_e32 v54, 16, v143
	v_pk_add_f32 v[140:141], v[52:53], v[52:53] op_sel:[0,1] op_sel_hi:[1,0]
	v_lshlrev_b32_e32 v52, 16, v142
	v_and_b32_e32 v53, 0xffff0000, v142
	v_and_b32_e32 v55, 0xffff0000, v143
	s_waitcnt lgkmcnt(0)
	v_pk_mul_f32 v[54:55], v[60:61], v[54:55]
	v_pk_mul_f32 v[52:53], v[58:59], v[52:53]
	v_pk_fma_f32 v[54:55], v[94:95], s[30:31], v[54:55] op_sel_hi:[1,0,1]
	v_pk_fma_f32 v[52:53], v[92:93], s[30:31], v[52:53] op_sel_hi:[1,0,1]
	v_lshlrev_b32_e32 v92, 16, v150
	v_and_b32_e32 v93, 0xffff0000, v150
	v_lshlrev_b32_e32 v94, 16, v151
	v_and_b32_e32 v95, 0xffff0000, v151
	v_pk_mul_f32 v[60:61], v[60:61], v[94:95]
	v_pk_mul_f32 v[58:59], v[58:59], v[92:93]
	ds_read_b128 v[92:95], v91 offset:4096
	ds_read_b128 v[96:99], v91 offset:5120
	v_lshlrev_b32_e32 v148, 16, v153
	v_and_b32_e32 v149, 0xffff0000, v153
	v_pk_fma_f32 v[60:61], v[102:103], s[30:31], v[60:61] op_sel_hi:[1,0,1]
	s_waitcnt lgkmcnt(1)
	v_pk_mul_f32 v[146:147], v[92:93], v[146:147]
	v_pk_mul_f32 v[148:149], v[94:95], v[148:149]
	v_pk_fma_f32 v[30:31], v[30:31], s[30:31], v[146:147] op_sel_hi:[1,0,1]
	s_waitcnt vmcnt(3)
	v_lshlrev_b32_e32 v146, 16, v88
	v_and_b32_e32 v147, 0xffff0000, v88
	v_lshlrev_b32_e32 v88, 16, v89
	v_and_b32_e32 v89, 0xffff0000, v89
	v_pk_fma_f32 v[32:33], v[32:33], s[30:31], v[148:149] op_sel_hi:[1,0,1]
	v_pk_mul_f32 v[88:89], v[94:95], v[88:89]
	v_pk_mul_f32 v[92:93], v[92:93], v[146:147]
	v_pk_fma_f32 v[58:59], v[100:101], s[30:31], v[58:59] op_sel_hi:[1,0,1]
	v_add_f32_e32 v100, v52, v53
	v_add_f32_e32 v102, v55, v54
	v_pk_fma_f32 v[28:29], v[28:29], s[30:31], v[88:89] op_sel_hi:[1,0,1]
	v_pk_fma_f32 v[26:27], v[26:27], s[30:31], v[92:93] op_sel_hi:[1,0,1]
	v_mov_b32_e32 v105, v30
	v_mov_b32_e32 v119, v31
	v_mov_b32_e32 v101, v33
	v_mov_b32_e32 v103, v32
	v_add_f32_e32 v142, v58, v59
	v_add_f32_e32 v144, v60, v61
	v_pk_add_f32 v[88:89], v[104:105], v[118:119]
	v_pk_add_f32 v[92:93], v[100:101], v[102:103]
	v_mov_b32_e32 v117, v26
	v_mov_b32_e32 v141, v27
	v_mov_b32_e32 v143, v28
	v_mov_b32_e32 v145, v29
	v_pk_add_f32 v[88:89], v[88:89], v[92:93]
	v_pk_add_f32 v[92:93], v[116:117], v[140:141]
	v_pk_add_f32 v[94:95], v[142:143], v[144:145]
	v_lshlrev_b32_e32 v102, 16, v82
	v_pk_add_f32 v[92:93], v[92:93], v[94:95]
	v_and_b32_e32 v103, 0xffff0000, v82
	v_pk_add_f32 v[100:101], v[92:93], v[92:93] op_sel:[0,1] op_sel_hi:[1,0]
	v_lshlrev_b32_e32 v92, 16, v86
	v_and_b32_e32 v93, 0xffff0000, v86
	v_lshlrev_b32_e32 v86, 16, v87
	v_and_b32_e32 v87, 0xffff0000, v87
	s_waitcnt lgkmcnt(0)
	v_pk_mul_f32 v[86:87], v[98:99], v[86:87]
	v_pk_mul_f32 v[92:93], v[96:97], v[92:93]
	v_pk_fma_f32 v[24:25], v[24:25], s[30:31], v[86:87] op_sel_hi:[1,0,1]
	s_waitcnt vmcnt(2)
	v_lshlrev_b32_e32 v86, 16, v84
	v_and_b32_e32 v87, 0xffff0000, v84
	v_lshlrev_b32_e32 v84, 16, v85
	v_and_b32_e32 v85, 0xffff0000, v85
	v_pk_fma_f32 v[22:23], v[22:23], s[30:31], v[92:93] op_sel_hi:[1,0,1]
	v_pk_mul_f32 v[84:85], v[98:99], v[84:85]
	v_pk_mul_f32 v[86:87], v[96:97], v[86:87]
	v_pk_fma_f32 v[20:21], v[20:21], s[30:31], v[84:85] op_sel_hi:[1,0,1]
	v_pk_fma_f32 v[18:19], v[18:19], s[30:31], v[86:87] op_sel_hi:[1,0,1]
	v_mov_b32_e32 v84, v22
	v_mov_b32_e32 v85, v25
	v_pk_mov_b32 v[86:87], v[22:23], v[24:25] op_sel:[1,0]
	ds_read_b128 v[92:95], v91 offset:7168
	v_pk_add_f32 v[84:85], v[84:85], v[86:87]
	v_mov_b32_e32 v86, v18
	v_pk_add_f32 v[96:97], v[84:85], v[84:85] op_sel:[0,1] op_sel_hi:[1,0]
	v_pk_mov_b32 v[84:85], v[18:19], v[20:21] op_sel:[1,0]
	v_mov_b32_e32 v87, v21
	v_pk_add_f32 v[84:85], v[84:85], v[86:87]
	v_lshlrev_b32_e32 v82, 16, v83
	v_pk_add_f32 v[98:99], v[84:85], v[84:85] op_sel:[0,1] op_sel_hi:[1,0]
	ds_read_b128 v[84:87], v91 offset:6144
	v_and_b32_e32 v83, 0xffff0000, v83
	v_pk_add_f32 v[88:89], v[88:89], v[88:89] op_sel:[0,1] op_sel_hi:[1,0]
	v_cmp_lt_i32_e32 vcc, v129, v128
	s_waitcnt lgkmcnt(0)
	v_pk_mul_f32 v[102:103], v[84:85], v[102:103]
	v_pk_mul_f32 v[82:83], v[86:87], v[82:83]
	v_pk_fma_f32 v[14:15], v[14:15], s[30:31], v[102:103] op_sel_hi:[1,0,1]
	v_lshlrev_b32_e32 v102, 16, v78
	v_and_b32_e32 v103, 0xffff0000, v78
	v_lshlrev_b32_e32 v78, 16, v79
	v_and_b32_e32 v79, 0xffff0000, v79
	v_pk_fma_f32 v[16:17], v[16:17], s[30:31], v[82:83] op_sel_hi:[1,0,1]
	s_waitcnt vmcnt(1)
	v_lshlrev_b32_e32 v82, 16, v80
	v_and_b32_e32 v83, 0xffff0000, v80
	v_lshlrev_b32_e32 v80, 16, v81
	v_and_b32_e32 v81, 0xffff0000, v81
	v_pk_mul_f32 v[78:79], v[94:95], v[78:79]
	v_pk_mul_f32 v[102:103], v[92:93], v[102:103]
	v_pk_mul_f32 v[80:81], v[86:87], v[80:81]
	v_pk_mul_f32 v[82:83], v[84:85], v[82:83]
	v_pk_fma_f32 v[8:9], v[8:9], s[30:31], v[78:79] op_sel_hi:[1,0,1]
	v_pk_fma_f32 v[6:7], v[6:7], s[30:31], v[102:103] op_sel_hi:[1,0,1]
	v_pk_fma_f32 v[12:13], v[12:13], s[30:31], v[80:81] op_sel_hi:[1,0,1]
	v_pk_fma_f32 v[10:11], v[10:11], s[30:31], v[82:83] op_sel_hi:[1,0,1]
	v_add_f32_e32 v80, v14, v15
	v_add_f32_e32 v82, v17, v16
	v_mov_b32_e32 v89, v6
	v_mov_b32_e32 v97, v7
	v_mov_b32_e32 v81, v9
	v_mov_b32_e32 v83, v8
	v_pk_add_f32 v[88:89], v[88:89], v[96:97]
	v_pk_add_f32 v[80:81], v[80:81], v[82:83]
	s_waitcnt vmcnt(0)
	v_lshlrev_b32_e32 v78, 16, v76
	v_pk_add_f32 v[80:81], v[88:89], v[80:81]
	v_and_b32_e32 v79, 0xffff0000, v76
	v_add_f32_e32 v80, v80, v81
	v_cndmask_b32_e32 v81, v126, v129, vcc
	v_lshlrev_b32_e32 v91, 2, v81
	s_nop 1
	v_mov_b32_dpp v81, v80 quad_perm:[1,0,3,2] row_mask:0xf bank_mask:0xf
	v_lshlrev_b32_e32 v76, 16, v77
	v_and_b32_e32 v77, 0xffff0000, v77
	v_pk_mul_f32 v[76:77], v[94:95], v[76:77]
	v_cmp_lt_i32_e32 vcc, v130, v128
	v_pk_mul_f32 v[78:79], v[92:93], v[78:79]
	v_pk_fma_f32 v[4:5], v[4:5], s[30:31], v[76:77] op_sel_hi:[1,0,1]
	v_cndmask_b32_e32 v76, v126, v130, vcc
	v_pk_fma_f32 v[2:3], v[2:3], s[30:31], v[78:79] op_sel_hi:[1,0,1]
	s_waitcnt lgkmcnt(0)
	v_add_f32_e32 v78, v80, v81
	v_lshlrev_b32_e32 v94, 2, v76
	s_nop 1
	v_mov_b32_dpp v79, v78 quad_perm:[2,3,0,1] row_mask:0xf bank_mask:0xf
	v_cmp_lt_i32_e32 vcc, v131, v128
	v_add_f32_e32 v84, v10, v11
	v_add_f32_e32 v86, v12, v13
	v_mov_b32_e32 v101, v2
	v_mov_b32_e32 v99, v3
	v_mov_b32_e32 v85, v4
	s_waitcnt lgkmcnt(0)
	v_add_f32_e32 v80, v78, v79
	v_cndmask_b32_e32 v78, v126, v131, vcc
	v_mov_b32_e32 v87, v5
	v_pk_add_f32 v[76:77], v[100:101], v[98:99]
	v_lshlrev_b32_e32 v95, 2, v78
	v_pk_add_f32 v[78:79], v[84:85], v[86:87]
	s_nop 1
	v_mov_b32_dpp v81, v80 row_half_mirror row_mask:0xf bank_mask:0xf
	v_pk_add_f32 v[76:77], v[76:77], v[78:79]
	v_cmp_lt_i32_e32 vcc, v132, v128
	v_add_f32_e32 v76, v76, v77
	s_nop 1
	v_mov_b32_dpp v78, v76 quad_perm:[1,0,3,2] row_mask:0xf bank_mask:0xf
	v_cndmask_b32_e32 v79, v126, v132, vcc
	s_waitcnt lgkmcnt(1)
	v_add_f32_e32 v77, v80, v81
	v_lshlrev_b32_e32 v96, 2, v79
	s_nop 1
	v_mov_b32_dpp v79, v77 row_mirror row_mask:0xf bank_mask:0xf
	s_waitcnt lgkmcnt(1)
	v_add_f32_e32 v76, v76, v78
	s_nop 1
	v_mov_b32_dpp v78, v76 quad_perm:[2,3,0,1] row_mask:0xf bank_mask:0xf
	v_cmp_lt_i32_e32 vcc, v133, v128
	v_add_u32_e32 v101, 0x1c800, v90
	s_waitcnt lgkmcnt(1)
	v_add_f32_e32 v77, v77, v79
	v_cndmask_b32_e32 v79, v126, v133, vcc
	s_waitcnt lgkmcnt(0)
	v_add_f32_e32 v76, v76, v78
	s_nop 1
	v_mov_b32_dpp v78, v76 row_half_mirror row_mask:0xf bank_mask:0xf
	v_lshlrev_b32_e32 v97, 2, v79
	v_mov_b32_e32 v79, v77
	v_mov_b32_e32 v97, v77
	s_nop 1
	v_permlane16_swap_b32_e32 v79, v97
	s_nop 1
	v_mov_b32_dpp v79, v97 quad_perm:[0,1,2,3] row_mask:0x5 bank_mask:0xf
	v_cmp_lt_i32_e32 vcc, v134, v128
	s_waitcnt lgkmcnt(1)
	v_add_f32_e32 v76, v76, v78
	s_nop 1
	v_mov_b32_dpp v78, v76 row_mirror row_mask:0xf bank_mask:0xf
	s_waitcnt lgkmcnt(1)
	v_add_f32_e32 v77, v77, v79
	v_cndmask_b32_e32 v79, v126, v134, vcc
	v_lshlrev_b32_e32 v98, 2, v79
	v_mov_b32_e32 v79, v77
	v_mov_b32_e32 v98, v77
	s_nop 1
	v_permlane32_swap_b32_e32 v79, v98
	s_nop 1
	v_mov_b32_dpp v79, v98 quad_perm:[0,1,2,3] row_mask:0x3 bank_mask:0xf
	s_waitcnt lgkmcnt(1)
	v_add_f32_e32 v76, v76, v78
	v_mov_b32_e32 v78, v76
	v_mov_b32_e32 v97, v76
	s_nop 1
	v_permlane16_swap_b32_e32 v78, v97
	s_nop 1
	v_mov_b32_dpp v78, v97 quad_perm:[0,1,2,3] row_mask:0x5 bank_mask:0xf
	s_waitcnt lgkmcnt(1)
	v_add_f32_e32 v99, v77, v79
	v_fmamk_f32 v67, v99, 0xba000000, v67
	s_waitcnt lgkmcnt(0)
	v_add_f32_e32 v76, v76, v78
	v_mov_b32_e32 v78, v76
	v_mov_b32_e32 v98, v76
	s_nop 1
	v_permlane32_swap_b32_e32 v78, v98
	s_nop 1
	v_mov_b32_dpp v78, v98 quad_perm:[0,1,2,3] row_mask:0x3 bank_mask:0xf
	v_fmamk_f32 v47, v99, 0xba000000, v47
	v_fmac_f32_e32 v66, 0xba000000, v99
	v_fmac_f32_e32 v46, 0xba000000, v99
	v_mov_b32_e32 v79, v47
	s_waitcnt lgkmcnt(0)
	v_add_f32_e32 v100, v76, v78
	v_mov_b32_e32 v78, v67
	v_fmac_f32_e32 v62, 0xba000000, v99
	v_fmac_f32_e32 v44, 0xba000000, v99
	v_mov_b32_e32 v76, v66
	v_mov_b32_e32 v77, v46
	v_pk_mul_f32 v[78:79], v[78:79], v[78:79]
	v_fmamk_f32 v63, v99, 0xba000000, v63
	v_fmamk_f32 v45, v99, 0xba000000, v45
	v_pk_fma_f32 v[76:77], v[76:77], v[76:77], v[78:79]
	v_mov_b32_e32 v78, v62
	v_mov_b32_e32 v79, v44
	v_fmamk_f32 v65, v100, 0xba000000, v65
	v_fmamk_f32 v51, v100, 0xba000000, v51
	v_pk_mul_f32 v[78:79], v[78:79], v[78:79]
	v_mov_b32_e32 v80, v63
	v_mov_b32_e32 v81, v45
	v_fmamk_f32 v57, v100, 0xba000000, v57
	v_fmac_f32_e32 v64, 0xba000000, v100
	v_fmamk_f32 v49, v100, 0xba000000, v49
	v_fmac_f32_e32 v50, 0xba000000, v100
	v_pk_fma_f32 v[78:79], v[80:81], v[80:81], v[78:79]
	v_mov_b32_e32 v80, v65
	v_mov_b32_e32 v81, v51
	v_fmac_f32_e32 v56, 0xba000000, v100
	v_fmac_f32_e32 v48, 0xba000000, v100
	v_pk_add_f32 v[76:77], v[76:77], v[78:79]
	v_mov_b32_e32 v78, v64
	v_mov_b32_e32 v79, v50
	v_pk_mul_f32 v[80:81], v[80:81], v[80:81]
	v_mov_b32_e32 v82, v57
	v_mov_b32_e32 v83, v49
	v_pk_fma_f32 v[78:79], v[78:79], v[78:79], v[80:81]
	v_mov_b32_e32 v80, v56
	v_mov_b32_e32 v81, v48
	v_pk_mul_f32 v[82:83], v[82:83], v[82:83]
	v_fmamk_f32 v73, v99, 0xba000000, v73
	v_pk_fma_f32 v[80:81], v[80:81], v[80:81], v[82:83]
	v_fmac_f32_e32 v72, 0xba000000, v99
	v_fmamk_f32 v75, v99, 0xba000000, v75
	v_fmac_f32_e32 v74, 0xba000000, v99
	v_pk_add_f32 v[78:79], v[78:79], v[80:81]
	v_pk_mul_f32 v[80:81], v[74:75], v[74:75]
	v_pk_mul_f32 v[82:83], v[72:73], v[72:73]
	v_fmamk_f32 v69, v100, 0xba000000, v69
	v_fmac_f32_e32 v68, 0xba000000, v100
	v_fmamk_f32 v71, v100, 0xba000000, v71
	v_fmac_f32_e32 v70, 0xba000000, v100
	v_pk_mov_b32 v[84:85], v[82:83], v[80:81] op_sel:[1,0]
	v_mov_b32_e32 v83, v81
	v_pk_add_f32 v[76:77], v[76:77], v[76:77] op_sel_hi:[0,1]
	v_pk_add_f32 v[80:81], v[82:83], v[84:85]
	v_pk_mul_f32 v[82:83], v[70:71], v[70:71]
	v_pk_mul_f32 v[84:85], v[68:69], v[68:69]
	v_fmac_f32_e32 v52, 0xba000000, v99
	v_pk_mov_b32 v[86:87], v[84:85], v[82:83] op_sel:[1,0]
	v_mov_b32_e32 v85, v83
	v_fmamk_f32 v53, v99, 0xba000000, v53
	v_fmac_f32_e32 v54, 0xba000000, v99
	v_mul_f32_e32 v76, v52, v52
	v_pk_add_f32 v[82:83], v[86:87], v[84:85]
	v_fmamk_f32 v55, v99, 0xba000000, v55
	v_fmac_f32_e32 v58, 0xba000000, v100
	v_pk_fma_f32 v[84:85], v[52:53], v[52:53], v[76:77] op_sel_hi:[1,1,0]
	v_mul_f32_e32 v76, v54, v54
	v_fmamk_f32 v59, v100, 0xba000000, v59
	v_fmac_f32_e32 v60, 0xba000000, v100
	v_pk_fma_f32 v[86:87], v[54:55], v[54:55], v[76:77] op_sel_hi:[1,1,0]
	v_mul_f32_e32 v76, v58, v58
	v_pk_add_f32 v[80:81], v[80:81], v[80:81] op_sel_hi:[0,1]
	v_fmamk_f32 v61, v100, 0xba000000, v61
	v_pk_fma_f32 v[88:89], v[58:59], v[58:59], v[76:77] op_sel_hi:[1,1,0]
	v_mul_f32_e32 v76, v60, v60
	v_fmamk_f32 v33, v99, 0xba000000, v33
	v_fmac_f32_e32 v32, 0xba000000, v99
	v_fmamk_f32 v31, v99, 0xba000000, v31
	v_fmac_f32_e32 v30, 0xba000000, v99
	v_pk_add_f32 v[78:79], v[78:79], v[78:79] op_sel_hi:[0,1]
	v_pk_add_f32 v[82:83], v[82:83], v[82:83] op_sel_hi:[0,1]
	v_pk_fma_f32 v[92:93], v[60:61], v[60:61], v[76:77] op_sel_hi:[1,1,0]
	v_fmamk_f32 v29, v100, 0xba000000, v29
	v_fmac_f32_e32 v28, 0xba000000, v100
	v_fmamk_f32 v27, v100, 0xba000000, v27
	v_fmac_f32_e32 v26, 0xba000000, v100
	v_mul_f32_e32 v84, v30, v30
	v_mul_f32_e32 v86, v31, v31
	v_mul_f32_e32 v76, v32, v32
	v_mul_f32_e32 v80, v33, v33
	v_pk_add_f32 v[84:85], v[84:85], v[86:87]
	v_pk_add_f32 v[76:77], v[80:81], v[76:77]
	v_mul_f32_e32 v88, v26, v26
	v_mul_f32_e32 v92, v27, v27
	v_mul_f32_e32 v82, v28, v28
	v_mul_f32_e32 v78, v29, v29
	v_pk_add_f32 v[76:77], v[84:85], v[76:77]
	v_pk_add_f32 v[80:81], v[88:89], v[92:93]
	v_pk_add_f32 v[78:79], v[82:83], v[78:79]
	v_fmamk_f32 v23, v99, 0xba000000, v23
	v_fmac_f32_e32 v22, 0xba000000, v99
	v_fmamk_f32 v25, v99, 0xba000000, v25
	v_fmac_f32_e32 v24, 0xba000000, v99
	v_pk_add_f32 v[76:77], v[76:77], v[76:77] op_sel_hi:[0,1]
	v_pk_add_f32 v[78:79], v[80:81], v[78:79]
	v_pk_mul_f32 v[80:81], v[24:25], v[24:25]
	v_pk_mul_f32 v[82:83], v[22:23], v[22:23]
	v_fmac_f32_e32 v14, 0xba000000, v99
	v_pk_mov_b32 v[84:85], v[82:83], v[80:81] op_sel:[1,0]
	v_mov_b32_e32 v83, v81
	v_fmamk_f32 v15, v99, 0xba000000, v15
	v_fmac_f32_e32 v16, 0xba000000, v99
	v_mul_f32_e32 v76, v14, v14
	v_pk_add_f32 v[80:81], v[82:83], v[84:85]
	v_fmamk_f32 v17, v99, 0xba000000, v17
	v_pk_fma_f32 v[86:87], v[14:15], v[14:15], v[76:77] op_sel_hi:[1,1,0]
	v_mul_f32_e32 v76, v16, v16
	v_pk_add_f32 v[80:81], v[80:81], v[80:81] op_sel_hi:[0,1]
	v_pk_fma_f32 v[88:89], v[16:17], v[16:17], v[76:77] op_sel_hi:[1,1,0]
	v_fmamk_f32 v9, v99, 0xba000000, v9
	v_fmac_f32_e32 v8, 0xba000000, v99
	v_fmamk_f32 v7, v99, 0xba000000, v7
	v_fmac_f32_e32 v6, 0xba000000, v99
	v_mul_f32_e32 v86, v6, v6
	v_mul_f32_e32 v88, v7, v7
	v_mul_f32_e32 v76, v8, v8
	v_mul_f32_e32 v80, v9, v9
	v_pk_add_f32 v[86:87], v[86:87], v[88:89]
	v_pk_add_f32 v[76:77], v[80:81], v[76:77]
	v_pk_add_f32 v[78:79], v[78:79], v[78:79] op_sel_hi:[0,1]
	v_pk_add_f32 v[76:77], v[86:87], v[76:77]
	v_fmamk_f32 v19, v100, 0xba000000, v19
	v_add_f32_e32 v78, v76, v77
	v_fmac_f32_e32 v18, 0xba000000, v100
	v_fmamk_f32 v21, v100, 0xba000000, v21
	v_fmac_f32_e32 v20, 0xba000000, v100
	s_nop 1
	v_mov_b32_dpp v80, v78 quad_perm:[1,0,3,2] row_mask:0xf bank_mask:0xf
	v_pk_mul_f32 v[82:83], v[20:21], v[20:21]
	v_pk_mul_f32 v[84:85], v[18:19], v[18:19]
	v_fmac_f32_e32 v10, 0xba000000, v100
	v_pk_mov_b32 v[76:77], v[84:85], v[82:83] op_sel:[1,0]
	v_mov_b32_e32 v85, v83
	v_pk_add_f32 v[76:77], v[76:77], v[84:85]
	v_fmamk_f32 v11, v100, 0xba000000, v11
	v_pk_add_f32 v[76:77], v[76:77], v[76:77] op_sel_hi:[0,1]
	s_waitcnt lgkmcnt(0)
	v_add_f32_e32 v76, v78, v80
	s_nop 1
	v_mov_b32_dpp v78, v76 quad_perm:[2,3,0,1] row_mask:0xf bank_mask:0xf
	v_fmac_f32_e32 v12, 0xba000000, v100
	v_fmamk_f32 v13, v100, 0xba000000, v13
	v_fmamk_f32 v5, v100, 0xba000000, v5
	v_fmac_f32_e32 v4, 0xba000000, v100
	s_waitcnt lgkmcnt(0)
	v_add_f32_e32 v78, v76, v78
	s_nop 1
	v_mov_b32_dpp v84, v78 row_half_mirror row_mask:0xf bank_mask:0xf
	v_mul_f32_e32 v76, v10, v10
	v_pk_fma_f32 v[80:81], v[10:11], v[10:11], v[76:77] op_sel_hi:[1,1,0]
	v_mul_f32_e32 v76, v12, v12
	v_pk_fma_f32 v[82:83], v[12:13], v[12:13], v[76:77] op_sel_hi:[1,1,0]
	s_waitcnt lgkmcnt(0)
	v_add_f32_e32 v76, v78, v84
	s_nop 1
	v_mov_b32_dpp v78, v76 row_mirror row_mask:0xf bank_mask:0xf
	v_fmamk_f32 v3, v100, 0xba000000, v3
	v_fmac_f32_e32 v2, 0xba000000, v100
	v_mul_f32_e32 v80, v2, v2
	v_mul_f32_e32 v82, v3, v3
	s_waitcnt lgkmcnt(0)
	v_add_f32_e32 v84, v76, v78
	v_mul_f32_e32 v76, v4, v4
	v_mul_f32_e32 v78, v5, v5
	v_pk_add_f32 v[80:81], v[80:81], v[82:83]
	v_pk_add_f32 v[76:77], v[76:77], v[78:79]
	v_mov_b32_e32 v85, v84
	v_mov_b32_e32 v97, v84
	s_nop 1
	v_permlane16_swap_b32_e32 v85, v97
	s_nop 1
	v_mov_b32_dpp v85, v97 quad_perm:[0,1,2,3] row_mask:0x5 bank_mask:0xf
	v_pk_add_f32 v[76:77], v[80:81], v[76:77]
	v_add_u32_e32 v100, 0x1a800, v90
	v_add_f32_e32 v76, v76, v77
	s_nop 1
	v_mov_b32_dpp v79, v76 quad_perm:[1,0,3,2] row_mask:0xf bank_mask:0xf
	s_waitcnt lgkmcnt(1)
	v_add_f32_e32 v84, v84, v85
	v_mov_b32_e32 v85, v84
	v_mov_b32_e32 v98, v84
	s_nop 1
	v_permlane32_swap_b32_e32 v85, v98
	s_nop 1
	v_mov_b32_dpp v85, v98 quad_perm:[0,1,2,3] row_mask:0x3 bank_mask:0xf
	s_waitcnt lgkmcnt(1)
	v_add_f32_e32 v76, v76, v79
	s_nop 1
	v_mov_b32_dpp v79, v76 quad_perm:[2,3,0,1] row_mask:0xf bank_mask:0xf
	s_waitcnt lgkmcnt(1)
	v_add_f32_e32 v77, v84, v85
	v_fmamk_f32 v77, v77, 0x3a000000, v135
	v_mul_f32_e32 v78, 0x4f800000, v77
	v_cmp_gt_f32_e32 vcc, s55, v77
	s_waitcnt lgkmcnt(0)
	v_add_f32_e32 v76, v76, v79
	s_nop 1
	v_mov_b32_dpp v79, v76 row_half_mirror row_mask:0xf bank_mask:0xf
	v_cndmask_b32_e32 v77, v77, v78, vcc
	v_sqrt_f32_e32 v78, v77
	s_waitcnt lgkmcnt(0)
	v_add_f32_e32 v76, v76, v79
	s_nop 1
	v_mov_b32_dpp v79, v76 row_mirror row_mask:0xf bank_mask:0xf
	v_add_u32_e32 v80, -1, v78
	v_fma_f32 v81, -v80, v78, v77
	v_cmp_ge_f32_e64 s[0:1], 0, v81
	v_add_u32_e32 v81, 1, v78
	s_waitcnt lgkmcnt(0)
	v_add_f32_e32 v76, v76, v79
	v_mov_b32_e32 v79, v76
	v_mov_b32_e32 v97, v76
	s_nop 1
	v_permlane16_swap_b32_e32 v79, v97
	s_nop 1
	v_mov_b32_dpp v79, v97 quad_perm:[0,1,2,3] row_mask:0x5 bank_mask:0xf
	v_cndmask_b32_e64 v80, v78, v80, s[0:1]
	v_fma_f32 v78, -v81, v78, v77
	v_cmp_lt_f32_e64 s[0:1], 0, v78
	s_waitcnt lgkmcnt(0)
	v_add_f32_e32 v76, v76, v79
	v_cndmask_b32_e64 v78, v80, v81, s[0:1]
	v_mul_f32_e32 v80, 0x37800000, v78
	v_mov_b32_e32 v79, v76
	v_mov_b32_e32 v98, v76
	s_nop 1
	v_permlane32_swap_b32_e32 v79, v98
	s_nop 1
	v_mov_b32_dpp v79, v98 quad_perm:[0,1,2,3] row_mask:0x3 bank_mask:0xf
	v_cndmask_b32_e32 v78, v78, v80, vcc
	v_cmp_class_f32_e32 vcc, v77, v136
	s_waitcnt lgkmcnt(0)
	v_add_f32_e32 v76, v76, v79
	v_cndmask_b32_e32 v77, v78, v77, vcc
	v_div_scale_f32 v78, s[0:1], v77, v77, 1.0
	v_rcp_f32_e32 v80, v78
	v_fmamk_f32 v76, v76, 0x3a000000, v135
	v_mul_f32_e32 v79, 0x4f800000, v76
	v_cmp_gt_f32_e64 s[0:1], s55, v76
	v_fma_f32 v81, -v78, v80, 1.0
	v_fmac_f32_e32 v80, v81, v80
	v_cndmask_b32_e64 v76, v76, v79, s[0:1]
	v_div_scale_f32 v81, vcc, 1.0, v77, 1.0
	v_sqrt_f32_e32 v79, v76
	v_mul_f32_e32 v82, v81, v80
	v_fma_f32 v83, -v78, v82, v81
	v_fmac_f32_e32 v82, v83, v80
	v_fma_f32 v78, -v78, v82, v81
	v_add_u32_e32 v81, -1, v79
	v_fma_f32 v83, -v81, v79, v76
	v_cmp_ge_f32_e64 s[10:11], 0, v83
	v_add_u32_e32 v83, 1, v79
	s_nop 0
	v_cndmask_b32_e64 v81, v79, v81, s[10:11]
	v_fma_f32 v79, -v83, v79, v76
	v_cmp_lt_f32_e64 s[10:11], 0, v79
	s_nop 1
	v_cndmask_b32_e64 v79, v81, v83, s[10:11]
	v_mul_f32_e32 v81, 0x37800000, v79
	v_cndmask_b32_e64 v79, v79, v81, s[0:1]
	v_cmp_class_f32_e64 s[0:1], v76, v136
	s_nop 1
	v_cndmask_b32_e64 v79, v79, v76, s[0:1]
	v_div_scale_f32 v81, s[0:1], v79, v79, 1.0
	v_rcp_f32_e32 v83, v81
	v_div_fmas_f32 v76, v78, v80, v82
	v_div_fixup_f32 v76, v76, v77, 1.0
	s_add_u32 s0, s48, s40
	v_fma_f32 v77, -v81, v83, 1.0
	v_fmac_f32_e32 v83, v77, v83
	v_div_scale_f32 v77, vcc, 1.0, v79, 1.0
	v_mul_f32_e32 v78, v77, v83
	v_fma_f32 v80, -v81, v78, v77
	v_fmac_f32_e32 v78, v80, v83
	v_fma_f32 v77, -v81, v78, v77
	v_div_fmas_f32 v77, v77, v83, v78
	v_div_fixup_f32 v78, v77, v79, 1.0
	v_add_u32_e32 v77, 0x16800, v90
	v_add_u32_e32 v79, 0x18800, v90
	ds_read_b128 v[80:83], v77
	ds_read_b128 v[84:87], v79
	ds_read_b128 v[88:91], v100
	ds_read_b128 v[92:95], v101
	s_addc_u32 s1, s49, s41
	v_pk_mul_f32 v[66:67], v[66:67], v[76:77] op_sel_hi:[1,0]
	v_pk_mul_f32 v[62:63], v[62:63], v[76:77] op_sel_hi:[1,0]
	s_add_u32 s10, s48, s42
	s_waitcnt lgkmcnt(2)
	v_pk_fma_f32 v[98:99], v[82:83], v[62:63], v[86:87]
	v_pk_fma_f32 v[96:97], v[80:81], v[66:67], v[84:85]
	v_pk_mul_f32 v[62:63], v[64:65], v[78:79] op_sel_hi:[1,0]
	v_pk_mul_f32 v[56:57], v[56:57], v[78:79] op_sel_hi:[1,0]
	s_addc_u32 s11, s49, s43
	v_pk_fma_f32 v[64:65], v[82:83], v[56:57], v[86:87]
	v_pk_fma_f32 v[62:63], v[80:81], v[62:63], v[84:85]
	s_waitcnt lgkmcnt(0)
	v_pk_fma_f32 v[56:57], v[90:91], v[98:99], v[94:95]
	v_pk_fma_f32 v[66:67], v[88:89], v[96:97], v[92:93]
	global_store_dwordx4 v[40:41], v[96:99], off
	global_store_dwordx4 v[38:39], v[62:65], off
	v_cvt_pk_bf16_f32 v66, v66, v67
	v_cvt_pk_bf16_f32 v67, v56, v57
	v_lshl_add_u64 v[56:57], s[0:1], 0, v[42:43]
	v_lshl_add_u64 v[42:43], s[10:11], 0, v[42:43]
	v_pk_fma_f32 v[62:63], v[88:89], v[62:63], v[92:93]
	v_pk_fma_f32 v[64:65], v[90:91], v[64:65], v[94:95]
	global_store_dwordx2 v[56:57], v[66:67], off
	v_cvt_pk_bf16_f32 v62, v62, v63
	v_cvt_pk_bf16_f32 v63, v64, v65
	global_store_dwordx2 v[42:43], v[62:63], off
	ds_read_b128 v[62:65], v77 offset:1024
	ds_read_b128 v[80:83], v79 offset:1024
	ds_read_b128 v[84:87], v100 offset:1024
	ds_read_b128 v[88:91], v101 offset:1024
	v_pk_mul_f32 v[66:67], v[44:45], v[76:77] op_sel_hi:[1,0]
	v_pk_mul_f32 v[44:45], v[46:47], v[76:77] op_sel_hi:[1,0]
	s_waitcnt lgkmcnt(2)
	v_pk_fma_f32 v[46:47], v[64:65], v[66:67], v[82:83]
	v_pk_fma_f32 v[44:45], v[62:63], v[44:45], v[80:81]
	v_pk_mul_f32 v[66:67], v[48:49], v[78:79] op_sel_hi:[1,0]
	v_pk_mul_f32 v[48:49], v[50:51], v[78:79] op_sel_hi:[1,0]
	v_pk_fma_f32 v[50:51], v[64:65], v[66:67], v[82:83]
	v_pk_fma_f32 v[48:49], v[62:63], v[48:49], v[80:81]
	global_store_dwordx4 v[40:41], v[44:47], off offset:1024
	global_store_dwordx4 v[38:39], v[48:51], off offset:1024
	v_pk_mul_f32 v[66:67], v[74:75], v[76:77] op_sel_hi:[1,0]
	s_waitcnt lgkmcnt(0)
	v_pk_fma_f32 v[44:45], v[84:85], v[44:45], v[88:89]
	v_pk_fma_f32 v[46:47], v[86:87], v[46:47], v[90:91]
	v_cvt_pk_bf16_f32 v44, v44, v45
	v_pk_fma_f32 v[50:51], v[86:87], v[50:51], v[90:91]
	v_cvt_pk_bf16_f32 v45, v46, v47
	v_pk_fma_f32 v[48:49], v[84:85], v[48:49], v[88:89]
	global_store_dwordx2 v[56:57], v[44:45], off offset:512
	v_cvt_pk_bf16_f32 v44, v48, v49
	v_cvt_pk_bf16_f32 v45, v50, v51
	global_store_dwordx2 v[42:43], v[44:45], off offset:512
	ds_read_b128 v[44:47], v77 offset:2048
	ds_read_b128 v[48:51], v79 offset:2048
	ds_read_b128 v[62:65], v100 offset:2048
	ds_read_b128 v[80:83], v101 offset:2048
	v_pk_mul_f32 v[72:73], v[72:73], v[76:77] op_sel_hi:[1,0]
	v_pk_mul_f32 v[68:69], v[68:69], v[78:79] op_sel_hi:[1,0]
	s_waitcnt lgkmcnt(2)
	v_pk_fma_f32 v[72:73], v[72:73], v[44:45], v[48:49]
	v_pk_fma_f32 v[74:75], v[66:67], v[46:47], v[50:51]
	v_pk_mul_f32 v[66:67], v[70:71], v[78:79] op_sel_hi:[1,0]
	v_pk_fma_f32 v[44:45], v[68:69], v[44:45], v[48:49]
	v_pk_fma_f32 v[46:47], v[66:67], v[46:47], v[50:51]
	global_store_dwordx4 v[40:41], v[72:75], off offset:2048
	global_store_dwordx4 v[38:39], v[44:47], off offset:2048
	s_waitcnt lgkmcnt(0)
	v_pk_fma_f32 v[50:51], v[72:73], v[62:63], v[80:81]
	v_pk_fma_f32 v[48:49], v[74:75], v[64:65], v[82:83]
	v_pk_fma_f32 v[44:45], v[62:63], v[44:45], v[80:81]
	v_pk_fma_f32 v[46:47], v[64:65], v[46:47], v[82:83]
	v_cvt_pk_bf16_f32 v50, v50, v51
	v_cvt_pk_bf16_f32 v51, v48, v49
	global_store_dwordx2 v[56:57], v[50:51], off offset:1024
	v_cvt_pk_bf16_f32 v44, v44, v45
	v_cvt_pk_bf16_f32 v45, v46, v47
	global_store_dwordx2 v[42:43], v[44:45], off offset:1024
	ds_read_b128 v[44:47], v77 offset:3072
	ds_read_b128 v[48:51], v79 offset:3072
	ds_read_b128 v[62:65], v100 offset:3072
	ds_read_b128 v[66:69], v101 offset:3072
	v_pk_mul_f32 v[54:55], v[54:55], v[76:77] op_sel_hi:[1,0]
	v_pk_mul_f32 v[52:53], v[52:53], v[76:77] op_sel_hi:[1,0]
	s_waitcnt lgkmcnt(2)
	v_pk_fma_f32 v[54:55], v[54:55], v[46:47], v[50:51]
	v_pk_fma_f32 v[52:53], v[52:53], v[44:45], v[48:49]
	v_pk_mul_f32 v[60:61], v[60:61], v[78:79] op_sel_hi:[1,0]
	v_pk_mul_f32 v[58:59], v[58:59], v[78:79] op_sel_hi:[1,0]
	v_pk_fma_f32 v[46:47], v[60:61], v[46:47], v[50:51]
	v_pk_fma_f32 v[44:45], v[58:59], v[44:45], v[48:49]
	global_store_dwordx4 v[40:41], v[52:55], off offset:3072
	global_store_dwordx4 v[38:39], v[44:47], off offset:3072
	s_waitcnt lgkmcnt(0)
	v_pk_fma_f32 v[38:39], v[54:55], v[64:65], v[68:69]
	v_pk_fma_f32 v[40:41], v[52:53], v[62:63], v[66:67]
	v_pk_fma_f32 v[46:47], v[64:65], v[46:47], v[68:69]
	v_pk_fma_f32 v[44:45], v[62:63], v[44:45], v[66:67]
	v_cvt_pk_bf16_f32 v40, v40, v41
	v_cvt_pk_bf16_f32 v41, v38, v39
	global_store_dwordx2 v[56:57], v[40:41], off offset:1536
	v_cvt_pk_bf16_f32 v38, v44, v45
	v_cvt_pk_bf16_f32 v39, v46, v47
	global_store_dwordx2 v[42:43], v[38:39], off offset:1536
	ds_read_b128 v[38:41], v77 offset:4096
	ds_read_b128 v[44:47], v79 offset:4096
	ds_read_b128 v[48:51], v100 offset:4096
	ds_read_b128 v[52:55], v101 offset:4096
	v_pk_mul_f32 v[32:33], v[32:33], v[76:77] op_sel_hi:[1,0]
	v_pk_mul_f32 v[30:31], v[30:31], v[76:77] op_sel_hi:[1,0]
	v_pk_mul_f32 v[26:27], v[26:27], v[78:79] op_sel_hi:[1,0]
	s_waitcnt lgkmcnt(2)
	v_pk_fma_f32 v[30:31], v[30:31], v[38:39], v[44:45]
	v_pk_fma_f32 v[32:33], v[32:33], v[40:41], v[46:47]
	v_pk_mul_f32 v[28:29], v[28:29], v[78:79] op_sel_hi:[1,0]
	v_pk_fma_f32 v[26:27], v[26:27], v[38:39], v[44:45]
	v_pk_fma_f32 v[28:29], v[28:29], v[40:41], v[46:47]
	global_store_dwordx4 v[34:35], v[30:33], off
	global_store_dwordx4 v[36:37], v[26:29], off
	v_pk_mul_f32 v[24:25], v[24:25], v[76:77] op_sel_hi:[1,0]
	s_waitcnt lgkmcnt(0)
	v_pk_fma_f32 v[30:31], v[30:31], v[48:49], v[52:53]
	v_pk_fma_f32 v[26:27], v[48:49], v[26:27], v[52:53]
	v_pk_fma_f32 v[32:33], v[32:33], v[50:51], v[54:55]
	v_pk_fma_f32 v[28:29], v[50:51], v[28:29], v[54:55]
	v_cvt_pk_bf16_f32 v30, v30, v31
	v_cvt_pk_bf16_f32 v31, v32, v33
	global_store_dwordx2 v[56:57], v[30:31], off offset:2048
	v_cvt_pk_bf16_f32 v26, v26, v27
	v_cvt_pk_bf16_f32 v27, v28, v29
	global_store_dwordx2 v[42:43], v[26:27], off offset:2048
	ds_read_b128 v[26:29], v77 offset:5120
	ds_read_b128 v[30:33], v79 offset:5120
	ds_read_b128 v[38:41], v100 offset:5120
	ds_read_b128 v[44:47], v101 offset:5120
	v_pk_mul_f32 v[22:23], v[22:23], v[76:77] op_sel_hi:[1,0]
	v_pk_mul_f32 v[18:19], v[18:19], v[78:79] op_sel_hi:[1,0]
	s_waitcnt lgkmcnt(2)
	v_pk_fma_f32 v[22:23], v[22:23], v[26:27], v[30:31]
	v_pk_fma_f32 v[24:25], v[24:25], v[28:29], v[32:33]
	v_pk_mul_f32 v[20:21], v[20:21], v[78:79] op_sel_hi:[1,0]
	v_pk_fma_f32 v[18:19], v[18:19], v[26:27], v[30:31]
	v_pk_fma_f32 v[20:21], v[20:21], v[28:29], v[32:33]
	global_store_dwordx4 v[34:35], v[22:25], off offset:1024
	global_store_dwordx4 v[36:37], v[18:21], off offset:1024
	v_pk_mul_f32 v[16:17], v[16:17], v[76:77] op_sel_hi:[1,0]
	s_waitcnt lgkmcnt(0)
	v_pk_fma_f32 v[22:23], v[22:23], v[38:39], v[44:45]
	v_pk_fma_f32 v[18:19], v[38:39], v[18:19], v[44:45]
	v_pk_fma_f32 v[24:25], v[24:25], v[40:41], v[46:47]
	v_pk_fma_f32 v[20:21], v[40:41], v[20:21], v[46:47]
	v_cvt_pk_bf16_f32 v22, v22, v23
	v_cvt_pk_bf16_f32 v23, v24, v25
	global_store_dwordx2 v[56:57], v[22:23], off offset:2560
	v_cvt_pk_bf16_f32 v18, v18, v19
	v_cvt_pk_bf16_f32 v19, v20, v21
	global_store_dwordx2 v[42:43], v[18:19], off offset:2560
	ds_read_b128 v[18:21], v77 offset:6144
	ds_read_b128 v[22:25], v79 offset:6144
	ds_read_b128 v[26:29], v100 offset:6144
	ds_read_b128 v[30:33], v101 offset:6144
	v_pk_mul_f32 v[14:15], v[14:15], v[76:77] op_sel_hi:[1,0]
	v_pk_mul_f32 v[10:11], v[10:11], v[78:79] op_sel_hi:[1,0]
	s_waitcnt lgkmcnt(2)
	v_pk_fma_f32 v[14:15], v[14:15], v[18:19], v[22:23]
	v_pk_fma_f32 v[16:17], v[16:17], v[20:21], v[24:25]
	v_pk_mul_f32 v[12:13], v[12:13], v[78:79] op_sel_hi:[1,0]
	v_pk_fma_f32 v[10:11], v[10:11], v[18:19], v[22:23]
	v_pk_fma_f32 v[12:13], v[12:13], v[20:21], v[24:25]
	global_store_dwordx4 v[34:35], v[14:17], off offset:2048
	global_store_dwordx4 v[36:37], v[10:13], off offset:2048
	v_pk_mul_f32 v[8:9], v[8:9], v[76:77] op_sel_hi:[1,0]
	s_waitcnt lgkmcnt(0)
	v_pk_fma_f32 v[14:15], v[14:15], v[26:27], v[30:31]
	v_pk_fma_f32 v[10:11], v[26:27], v[10:11], v[30:31]
	v_pk_fma_f32 v[16:17], v[16:17], v[28:29], v[32:33]
	v_pk_fma_f32 v[12:13], v[28:29], v[12:13], v[32:33]
	v_cvt_pk_bf16_f32 v14, v14, v15
	v_cvt_pk_bf16_f32 v15, v16, v17
	global_store_dwordx2 v[56:57], v[14:15], off offset:3072
	v_cvt_pk_bf16_f32 v10, v10, v11
	v_cvt_pk_bf16_f32 v11, v12, v13
	global_store_dwordx2 v[42:43], v[10:11], off offset:3072
	ds_read_b128 v[10:13], v77 offset:7168
	ds_read_b128 v[14:17], v79 offset:7168
	ds_read_b128 v[18:21], v100 offset:7168
	ds_read_b128 v[22:25], v101 offset:7168
	v_pk_mul_f32 v[6:7], v[6:7], v[76:77] op_sel_hi:[1,0]
	v_pk_mul_f32 v[2:3], v[2:3], v[78:79] op_sel_hi:[1,0]
	s_waitcnt lgkmcnt(2)
	v_pk_fma_f32 v[6:7], v[6:7], v[10:11], v[14:15]
	v_pk_fma_f32 v[8:9], v[8:9], v[12:13], v[16:17]
	v_pk_mul_f32 v[4:5], v[4:5], v[78:79] op_sel_hi:[1,0]
	v_pk_fma_f32 v[2:3], v[2:3], v[10:11], v[14:15]
	s_add_i32 s15, s15, 2
	s_add_i32 s38, s38, 16
	v_pk_fma_f32 v[4:5], v[4:5], v[12:13], v[16:17]
	global_store_dwordx4 v[34:35], v[6:9], off offset:3072
	global_store_dwordx4 v[36:37], v[2:5], off offset:3072
	s_cmp_gt_u32 s15, 5
	s_waitcnt lgkmcnt(0)
	v_pk_fma_f32 v[6:7], v[6:7], v[18:19], v[22:23]
	v_pk_fma_f32 v[2:3], v[18:19], v[2:3], v[22:23]
	v_pk_fma_f32 v[8:9], v[8:9], v[20:21], v[24:25]
	v_pk_fma_f32 v[4:5], v[20:21], v[4:5], v[24:25]
	v_cvt_pk_bf16_f32 v6, v6, v7
	v_cvt_pk_bf16_f32 v7, v8, v9
	global_store_dwordx2 v[56:57], v[6:7], off offset:3584
	v_cvt_pk_bf16_f32 v2, v2, v3
	v_cvt_pk_bf16_f32 v3, v4, v5
	global_store_dwordx2 v[42:43], v[2:3], off offset:3584
	s_cbranch_scc0 .LBB0_1826
	v_add_u32_e32 v2, s70, v122
	s_waitcnt vmcnt(0)
	s_ashr_i32 s15, s14, 31
	v_ashrrev_i32_e32 v3, 31, v2
	s_lshl_b64 s[0:1], s[14:15], 17
	v_lshlrev_b64 v[2:3], 13, v[2:3]
	v_mov_b32_e32 v82, 0
	v_lshl_add_u64 v[116:117], v[110:111], 0, s[0:1]
	v_lshl_add_u64 v[118:119], v[112:113], 0, v[2:3]
	s_mov_b32 s0, -2
	v_mov_b32_e32 v83, v82
	v_mov_b32_e32 v84, v82
	v_mov_b32_e32 v85, v82
	v_mov_b32_e32 v86, v82
	v_mov_b32_e32 v87, v82
	v_mov_b32_e32 v88, v82
	v_mov_b32_e32 v89, v82
	v_mov_b32_e32 v94, v82
	v_mov_b32_e32 v95, v82
	v_mov_b32_e32 v96, v82
	v_mov_b32_e32 v97, v82
	v_mov_b32_e32 v90, v82
	v_mov_b32_e32 v91, v82
	v_mov_b32_e32 v92, v82
	v_mov_b32_e32 v93, v82
	v_mov_b32_e32 v62, v82
	v_mov_b32_e32 v63, v82
	v_mov_b32_e32 v64, v82
	v_mov_b32_e32 v65, v82
	v_mov_b32_e32 v58, v82
	v_mov_b32_e32 v59, v82
	v_mov_b32_e32 v60, v82
	v_mov_b32_e32 v61, v82
	v_mov_b32_e32 v38, v82
	v_mov_b32_e32 v39, v82
	v_mov_b32_e32 v40, v82
	v_mov_b32_e32 v41, v82
	v_mov_b32_e32 v34, v82
	v_mov_b32_e32 v35, v82
	v_mov_b32_e32 v36, v82
	v_mov_b32_e32 v37, v82
	s_barrier

.LBB0_2076:
	s_add_i32 s0, s31, s12
	s_add_i32 s1, s92, s12
	s_cmpk_gt_i32 s1, 0xfff
	s_cselect_b64 s[20:21], -1, 0
	s_cmpk_lt_i32 s1, 0x1000
	s_cselect_b32 s1, s92, 0
	s_add_i32 s4, s0, s1
	s_ashr_i32 s1, s0, 31
	s_lshl_b64 s[22:23], s[0:1], 13
	s_add_u32 s0, s17, s22
	s_addc_u32 s1, s24, s23
	s_ashr_i32 s5, s4, 31
	s_lshl_b64 s[18:19], s[4:5], 13
	s_add_u32 s4, s17, s18
	v_mov_b32_e32 v50, v216
	s_addc_u32 s5, s24, s19
	s_add_u32 s34, s25, s22
	v_ashrrev_i32_e32 v51, 31, v50
	s_addc_u32 s35, s26, s23
	v_lshlrev_b64 v[6:7], 1, v[50:51]
	s_add_u32 s36, s25, s18
	v_lshl_add_u64 v[62:63], s[34:35], 0, v[6:7]
	s_addc_u32 s37, s26, s19
	v_add_co_u32_e32 v66, vcc, s27, v62
	v_lshl_add_u64 v[72:73], s[36:37], 0, v[6:7]
	s_nop 0
	v_addc_co_u32_e32 v67, vcc, 0, v63, vcc
	v_lshlrev_b64 v[52:53], 2, v[50:51]
	v_add_co_u32_e32 v86, vcc, s27, v72
	v_lshl_add_u64 v[2:3], s[0:1], 0, v[52:53]
	s_nop 0
	v_addc_co_u32_e32 v87, vcc, 0, v73, vcc
	v_lshl_add_u64 v[4:5], s[4:5], 0, v[52:53]
	global_load_dwordx4 v[54:57], v[2:3], off nt
	global_load_dwordx4 v[58:61], v[2:3], off offset:1024 nt
	global_load_dwordx4 v[68:71], v[4:5], off nt
	global_load_dwordx4 v[124:127], v[4:5], off offset:1024 nt
	global_load_dwordx4 v[42:45], v[2:3], off offset:2048 nt
	global_load_dwordx4 v[38:41], v[2:3], off offset:3072 nt
	global_load_dwordx4 v[46:49], v[4:5], off offset:2048 nt
	global_load_dwordx4 v[34:37], v[4:5], off offset:3072 nt
	global_load_dwordx2 v[132:133], v[62:63], off nt
	global_load_dwordx2 v[136:137], v[62:63], off offset:512 nt
	global_load_dwordx2 v[138:139], v[62:63], off offset:1024 nt
	global_load_dwordx2 v[108:109], v[62:63], off offset:1536 nt
	global_load_dwordx2 v[134:135], v[72:73], off nt
	global_load_dwordx2 v[140:141], v[72:73], off offset:512 nt
	global_load_dwordx2 v[142:143], v[72:73], off offset:1024 nt
	global_load_dwordx2 v[104:105], v[72:73], off offset:1536 nt
	v_add_co_u32_e32 v2, vcc, s27, v2
	v_lshl_add_u64 v[64:65], v[62:63], 0, s[14:15]
	s_nop 0
	v_addc_co_u32_e32 v3, vcc, 0, v3, vcc
	v_add_co_u32_e32 v74, vcc, s27, v4
	v_lshl_add_u64 v[78:79], v[72:73], 0, s[14:15]
	s_nop 0
	v_addc_co_u32_e32 v75, vcc, 0, v5, vcc
	global_load_dwordx2 v[144:145], v[64:65], off offset:512 nt
	global_load_dwordx2 v[146:147], v[64:65], off offset:1024 nt
	global_load_dwordx2 v[112:113], v[64:65], off offset:1536 nt
	global_load_dwordx2 v[100:101], v[64:65], off offset:2048 nt
	global_load_dwordx2 v[148:149], v[78:79], off offset:512 nt
	global_load_dwordx2 v[150:151], v[78:79], off offset:1024 nt
	global_load_dwordx2 v[110:111], v[78:79], off offset:1536 nt
	global_load_dwordx2 v[98:99], v[78:79], off offset:2048 nt
	global_load_dwordx4 v[30:33], v[2:3], off nt
	global_load_dwordx4 v[22:25], v[2:3], off offset:1024 nt
	global_load_dwordx4 v[26:29], v[74:75], off nt
	global_load_dwordx4 v[18:21], v[74:75], off offset:1024 nt
	global_load_dwordx4 v[10:13], v[2:3], off offset:2048 nt
	global_load_dwordx4 v[6:9], v[2:3], off offset:3072 nt
	global_load_dwordx4 v[14:17], v[74:75], off offset:2048 nt
	s_nop 0
	global_load_dwordx4 v[2:5], v[74:75], off offset:3072 nt
	global_load_dwordx2 v[106:107], v[62:63], off offset:2048 nt
	global_load_dwordx2 v[94:95], v[62:63], off offset:2560 nt
	global_load_dwordx2 v[88:89], v[62:63], off offset:3072 nt
	global_load_dwordx2 v[80:81], v[62:63], off offset:3584 nt
	s_nop 0
	global_load_dwordx2 v[62:63], v[66:67], off nt
	global_load_dwordx2 v[96:97], v[64:65], off offset:2560 nt
	global_load_dwordx2 v[90:91], v[64:65], off offset:3072 nt
	global_load_dwordx2 v[82:83], v[64:65], off offset:3584 nt
	global_load_dwordx2 v[102:103], v[72:73], off offset:2048 nt
	global_load_dwordx2 v[76:77], v[72:73], off offset:2560 nt
	global_load_dwordx2 v[84:85], v[72:73], off offset:3072 nt
	global_load_dwordx2 v[74:75], v[72:73], off offset:3584 nt
	s_nop 0
	global_load_dwordx2 v[64:65], v[86:87], off nt
	global_load_dwordx2 v[92:93], v[78:79], off offset:2560 nt
	s_nop 0
	global_load_dwordx2 v[86:87], v[78:79], off offset:3072 nt
	s_nop 0
	global_load_dwordx2 v[78:79], v[78:79], off offset:3584 nt
	v_lshl_add_u32 v123, v50, 2, s99
	ds_read_b128 v[128:131], v123
	s_waitcnt vmcnt(39)
	v_lshlrev_b32_e32 v66, 16, v132
	v_and_b32_e32 v67, 0xffff0000, v132
	s_waitcnt vmcnt(11)
	v_lshlrev_b32_e32 v72, 16, v62
	v_and_b32_e32 v73, 0xffff0000, v62
	v_pk_add_f32 v[66:67], v[66:67], v[72:73]
	v_lshlrev_b32_e32 v72, 16, v133
	v_and_b32_e32 v73, 0xffff0000, v133
	v_lshlrev_b32_e32 v62, 16, v63
	v_and_b32_e32 v63, 0xffff0000, v63
	v_pk_add_f32 v[62:63], v[72:73], v[62:63]
	v_lshlrev_b32_e32 v72, 16, v134
	v_and_b32_e32 v73, 0xffff0000, v134
	s_waitcnt vmcnt(3)
	v_lshlrev_b32_e32 v132, 16, v64
	v_and_b32_e32 v133, 0xffff0000, v64
	v_pk_add_f32 v[72:73], v[72:73], v[132:133]
	v_lshlrev_b32_e32 v132, 16, v135
	v_and_b32_e32 v133, 0xffff0000, v135
	v_lshlrev_b32_e32 v64, 16, v65
	v_and_b32_e32 v65, 0xffff0000, v65
	v_pk_add_f32 v[152:153], v[132:133], v[64:65]
	ds_read_b128 v[132:135], v123 offset:1024
	s_waitcnt lgkmcnt(1)
	v_pk_mul_f32 v[62:63], v[62:63], v[130:131]
	v_pk_mul_f32 v[66:67], v[66:67], v[128:129]
	v_pk_fma_f32 v[64:65], v[56:57], s[16:17], v[62:63] op_sel_hi:[1,0,1]
	v_pk_mul_f32 v[56:57], v[72:73], v[128:129]
	v_pk_fma_f32 v[66:67], v[54:55], s[16:17], v[66:67] op_sel_hi:[1,0,1]
	v_pk_mul_f32 v[54:55], v[152:153], v[130:131]
	v_pk_fma_f32 v[56:57], v[68:69], s[16:17], v[56:57] op_sel_hi:[1,0,1]
	v_lshlrev_b32_e32 v62, 16, v136
	v_and_b32_e32 v63, 0xffff0000, v136
	v_lshlrev_b32_e32 v68, 16, v144
	v_and_b32_e32 v69, 0xffff0000, v144
	v_pk_fma_f32 v[54:55], v[70:71], s[16:17], v[54:55] op_sel_hi:[1,0,1]
	v_pk_add_f32 v[62:63], v[62:63], v[68:69]
	v_lshlrev_b32_e32 v68, 16, v137
	v_and_b32_e32 v69, 0xffff0000, v137
	v_lshlrev_b32_e32 v70, 16, v145
	v_and_b32_e32 v71, 0xffff0000, v145
	v_pk_add_f32 v[68:69], v[68:69], v[70:71]
	v_lshlrev_b32_e32 v70, 16, v140
	v_and_b32_e32 v71, 0xffff0000, v140
	v_lshlrev_b32_e32 v72, 16, v148
	v_and_b32_e32 v73, 0xffff0000, v148
	v_pk_add_f32 v[70:71], v[70:71], v[72:73]
	v_lshlrev_b32_e32 v72, 16, v141
	v_and_b32_e32 v73, 0xffff0000, v141
	v_lshlrev_b32_e32 v128, 16, v149
	v_and_b32_e32 v129, 0xffff0000, v149
	v_pk_add_f32 v[128:129], v[72:73], v[128:129]
	s_waitcnt lgkmcnt(0)
	v_pk_mul_f32 v[72:73], v[62:63], v[132:133]
	v_pk_mul_f32 v[62:63], v[68:69], v[134:135]
	v_pk_fma_f32 v[72:73], v[58:59], s[16:17], v[72:73] op_sel_hi:[1,0,1]
	v_pk_fma_f32 v[62:63], v[60:61], s[16:17], v[62:63] op_sel_hi:[1,0,1]
	v_pk_mul_f32 v[60:61], v[70:71], v[132:133]
	v_mov_b32_e32 v68, v66
	v_mov_b32_e32 v69, v72
	v_mov_b32_e32 v70, v67
	v_mov_b32_e32 v71, v73
	v_pk_fma_f32 v[60:61], v[124:125], s[16:17], v[60:61] op_sel_hi:[1,0,1]
	v_pk_add_f32 v[68:69], v[68:69], v[70:71]
	v_mov_b32_e32 v70, v65
	v_mov_b32_e32 v71, v63
	v_mov_b32_e32 v124, v64
	v_mov_b32_e32 v125, v62
	v_pk_add_f32 v[70:71], v[70:71], v[124:125]
	v_pk_mul_f32 v[58:59], v[128:129], v[134:135]
	v_pk_add_f32 v[68:69], v[68:69], v[70:71]
	v_pk_fma_f32 v[58:59], v[126:127], s[16:17], v[58:59] op_sel_hi:[1,0,1]
	v_add_f32_e32 v68, 0, v68
	v_add_f32_e32 v132, v68, v69
	v_mov_b32_e32 v68, v56
	v_mov_b32_e32 v69, v60
	v_mov_b32_e32 v70, v57
	v_mov_b32_e32 v71, v61
	v_pk_add_f32 v[68:69], v[68:69], v[70:71]
	v_mov_b32_e32 v70, v54
	v_mov_b32_e32 v71, v58
	v_mov_b32_e32 v124, v55
	v_mov_b32_e32 v125, v59
	v_pk_add_f32 v[70:71], v[70:71], v[124:125]
	ds_read_b128 v[124:127], v123 offset:2048
	v_pk_add_f32 v[68:69], v[68:69], v[70:71]
	v_lshlrev_b32_e32 v70, 16, v146
	v_add_f32_e32 v68, 0, v68
	v_add_f32_e32 v134, v68, v69
	v_lshlrev_b32_e32 v68, 16, v138
	v_and_b32_e32 v69, 0xffff0000, v138
	v_and_b32_e32 v71, 0xffff0000, v146
	v_pk_add_f32 v[68:69], v[68:69], v[70:71]
	v_lshlrev_b32_e32 v70, 16, v139
	v_and_b32_e32 v71, 0xffff0000, v139
	v_lshlrev_b32_e32 v128, 16, v147
	v_and_b32_e32 v129, 0xffff0000, v147
	v_pk_add_f32 v[70:71], v[70:71], v[128:129]
	v_lshlrev_b32_e32 v128, 16, v142
	v_and_b32_e32 v129, 0xffff0000, v142
	v_lshlrev_b32_e32 v130, 16, v150
	v_and_b32_e32 v131, 0xffff0000, v150
	v_pk_add_f32 v[136:137], v[128:129], v[130:131]
	v_lshlrev_b32_e32 v128, 16, v143
	v_and_b32_e32 v129, 0xffff0000, v143
	v_lshlrev_b32_e32 v130, 16, v151
	v_and_b32_e32 v131, 0xffff0000, v151
	v_pk_add_f32 v[138:139], v[128:129], v[130:131]
	ds_read_b128 v[128:131], v123 offset:3072
	s_waitcnt lgkmcnt(1)
	v_pk_mul_f32 v[140:141], v[68:69], v[124:125]
	v_pk_mul_f32 v[68:69], v[70:71], v[126:127]
	v_pk_fma_f32 v[70:71], v[42:43], s[16:17], v[140:141] op_sel_hi:[1,0,1]
	v_pk_fma_f32 v[68:69], v[44:45], s[16:17], v[68:69] op_sel_hi:[1,0,1]
	v_pk_mul_f32 v[44:45], v[136:137], v[124:125]
	v_pk_mul_f32 v[42:43], v[138:139], v[126:127]
	v_pk_fma_f32 v[44:45], v[46:47], s[16:17], v[44:45] op_sel_hi:[1,0,1]
	v_pk_fma_f32 v[42:43], v[48:49], s[16:17], v[42:43] op_sel_hi:[1,0,1]
	v_mov_b32_e32 v46, v70
	v_mov_b32_e32 v47, v69
	v_pk_mov_b32 v[48:49], v[70:71], v[68:69] op_sel:[1,0]
	v_cmp_lt_i32_e32 vcc, v115, v114
	v_pk_add_f32 v[46:47], v[46:47], v[48:49]
	v_mov_b32_e32 v48, v44
	v_pk_add_f32 v[124:125], v[46:47], v[46:47] op_sel:[0,1] op_sel_hi:[1,0]
	v_pk_mov_b32 v[46:47], v[44:45], v[42:43] op_sel:[1,0]
	v_mov_b32_e32 v49, v43
	v_pk_add_f32 v[46:47], v[46:47], v[48:49]
	v_lshlrev_b32_e32 v48, 16, v112
	v_pk_add_f32 v[126:127], v[46:47], v[46:47] op_sel:[0,1] op_sel_hi:[1,0]
	v_lshlrev_b32_e32 v46, 16, v108
	v_and_b32_e32 v47, 0xffff0000, v108
	v_and_b32_e32 v49, 0xffff0000, v112
	v_pk_add_f32 v[46:47], v[46:47], v[48:49]
	v_lshlrev_b32_e32 v48, 16, v109
	v_and_b32_e32 v49, 0xffff0000, v109
	v_lshlrev_b32_e32 v108, 16, v113
	v_and_b32_e32 v109, 0xffff0000, v113
	v_pk_add_f32 v[48:49], v[48:49], v[108:109]
	v_lshlrev_b32_e32 v108, 16, v104
	v_and_b32_e32 v109, 0xffff0000, v104
	v_lshlrev_b32_e32 v112, 16, v110
	v_and_b32_e32 v113, 0xffff0000, v110
	v_lshlrev_b32_e32 v104, 16, v105
	v_and_b32_e32 v105, 0xffff0000, v105
	v_lshlrev_b32_e32 v110, 16, v111
	v_and_b32_e32 v111, 0xffff0000, v111
	v_pk_add_f32 v[108:109], v[108:109], v[112:113]
	v_pk_add_f32 v[104:105], v[104:105], v[110:111]
	s_waitcnt lgkmcnt(0)
	v_pk_mul_f32 v[46:47], v[46:47], v[128:129]
	v_pk_mul_f32 v[48:49], v[48:49], v[130:131]
	s_nop 0
	v_pk_fma_f32 v[40:41], v[40:41], s[16:17], v[48:49] op_sel_hi:[1,0,1]
	v_pk_fma_f32 v[48:49], v[38:39], s[16:17], v[46:47] op_sel_hi:[1,0,1]
	v_pk_mul_f32 v[38:39], v[108:109], v[128:129]
	v_pk_mul_f32 v[46:47], v[104:105], v[130:131]
	ds_read_b128 v[108:111], v123 offset:4096
	v_pk_fma_f32 v[36:37], v[36:37], s[16:17], v[46:47] op_sel_hi:[1,0,1]
	v_pk_fma_f32 v[34:35], v[34:35], s[16:17], v[38:39] op_sel_hi:[1,0,1]
	v_lshlrev_b32_e32 v38, 16, v106
	v_and_b32_e32 v39, 0xffff0000, v106
	v_lshlrev_b32_e32 v46, 16, v100
	v_and_b32_e32 v47, 0xffff0000, v100
	v_pk_add_f32 v[38:39], v[38:39], v[46:47]
	v_lshlrev_b32_e32 v46, 16, v107
	v_and_b32_e32 v47, 0xffff0000, v107
	v_lshlrev_b32_e32 v100, 16, v101
	v_and_b32_e32 v101, 0xffff0000, v101
	v_pk_add_f32 v[46:47], v[46:47], v[100:101]
	v_lshlrev_b32_e32 v100, 16, v102
	v_and_b32_e32 v101, 0xffff0000, v102
	v_lshlrev_b32_e32 v106, 16, v98
	v_and_b32_e32 v107, 0xffff0000, v98
	v_pk_add_f32 v[106:107], v[100:101], v[106:107]
	v_lshlrev_b32_e32 v100, 16, v103
	v_and_b32_e32 v101, 0xffff0000, v103
	v_lshlrev_b32_e32 v98, 16, v99
	v_and_b32_e32 v99, 0xffff0000, v99
	v_pk_add_f32 v[102:103], v[100:101], v[98:99]
	ds_read_b128 v[98:101], v123 offset:5120
	s_waitcnt lgkmcnt(1)
	v_pk_mul_f32 v[136:137], v[38:39], v[108:109]
	v_pk_mul_f32 v[38:39], v[46:47], v[110:111]
	v_pk_fma_f32 v[46:47], v[30:31], s[16:17], v[136:137] op_sel_hi:[1,0,1]
	v_pk_fma_f32 v[38:39], v[32:33], s[16:17], v[38:39] op_sel_hi:[1,0,1]
	v_add_f32_e32 v104, v48, v49
	v_add_f32_e32 v112, v41, v40
	v_pk_mul_f32 v[30:31], v[106:107], v[108:109]
	v_pk_mul_f32 v[32:33], v[102:103], v[110:111]
	v_mov_b32_e32 v133, v46
	v_mov_b32_e32 v125, v47
	v_mov_b32_e32 v105, v39
	v_mov_b32_e32 v113, v38
	v_pk_fma_f32 v[28:29], v[28:29], s[16:17], v[32:33] op_sel_hi:[1,0,1]
	v_pk_fma_f32 v[26:27], v[26:27], s[16:17], v[30:31] op_sel_hi:[1,0,1]
	v_pk_add_f32 v[30:31], v[132:133], v[124:125]
	v_pk_add_f32 v[32:33], v[104:105], v[112:113]
	v_add_f32_e32 v128, v34, v35
	v_add_f32_e32 v130, v36, v37
	v_pk_add_f32 v[30:31], v[30:31], v[32:33]
	v_mov_b32_e32 v135, v26
	v_mov_b32_e32 v127, v27
	v_mov_b32_e32 v129, v28
	v_mov_b32_e32 v131, v29
	v_pk_add_f32 v[102:103], v[30:31], v[30:31] op_sel:[0,1] op_sel_hi:[1,0]
	v_pk_add_f32 v[30:31], v[134:135], v[126:127]
	v_pk_add_f32 v[32:33], v[128:129], v[130:131]
	s_nop 0
	v_pk_add_f32 v[30:31], v[30:31], v[32:33]
	v_lshlrev_b32_e32 v32, 16, v96
	v_pk_add_f32 v[104:105], v[30:31], v[30:31] op_sel:[0,1] op_sel_hi:[1,0]
	v_lshlrev_b32_e32 v30, 16, v94
	v_and_b32_e32 v31, 0xffff0000, v94
	v_and_b32_e32 v33, 0xffff0000, v96
	v_pk_add_f32 v[30:31], v[30:31], v[32:33]
	v_lshlrev_b32_e32 v32, 16, v95
	v_and_b32_e32 v33, 0xffff0000, v95
	v_lshlrev_b32_e32 v94, 16, v97
	v_and_b32_e32 v95, 0xffff0000, v97
	v_pk_add_f32 v[32:33], v[32:33], v[94:95]
	v_lshlrev_b32_e32 v94, 16, v76
	v_and_b32_e32 v95, 0xffff0000, v76
	s_waitcnt vmcnt(2)
	v_lshlrev_b32_e32 v96, 16, v92
	v_and_b32_e32 v97, 0xffff0000, v92
	v_lshlrev_b32_e32 v76, 16, v77
	v_and_b32_e32 v77, 0xffff0000, v77
	v_lshlrev_b32_e32 v92, 16, v93
	v_and_b32_e32 v93, 0xffff0000, v93
	v_pk_add_f32 v[94:95], v[94:95], v[96:97]
	v_pk_add_f32 v[92:93], v[76:77], v[92:93]
	s_waitcnt lgkmcnt(0)
	v_pk_mul_f32 v[30:31], v[30:31], v[98:99]
	v_pk_mul_f32 v[32:33], v[32:33], v[100:101]
	v_pk_fma_f32 v[76:77], v[22:23], s[16:17], v[30:31] op_sel_hi:[1,0,1]
	v_pk_fma_f32 v[24:25], v[24:25], s[16:17], v[32:33] op_sel_hi:[1,0,1]
	v_pk_mul_f32 v[22:23], v[94:95], v[98:99]
	v_pk_mul_f32 v[30:31], v[92:93], v[100:101]
	v_pk_fma_f32 v[18:19], v[18:19], s[16:17], v[22:23] op_sel_hi:[1,0,1]
	v_pk_fma_f32 v[20:21], v[20:21], s[16:17], v[30:31] op_sel_hi:[1,0,1]
	v_mov_b32_e32 v22, v76
	v_mov_b32_e32 v23, v25
	v_pk_mov_b32 v[30:31], v[76:77], v[24:25] op_sel:[1,0]
	v_mov_b32_e32 v32, v18
	v_pk_add_f32 v[22:23], v[22:23], v[30:31]
	v_pk_mov_b32 v[30:31], v[18:19], v[20:21] op_sel:[1,0]
	v_mov_b32_e32 v33, v21
	v_pk_add_f32 v[30:31], v[30:31], v[32:33]
	ds_read_b128 v[92:95], v123 offset:6144
	v_pk_add_f32 v[96:97], v[30:31], v[30:31] op_sel:[0,1] op_sel_hi:[1,0]
	v_lshlrev_b32_e32 v30, 16, v88
	v_and_b32_e32 v31, 0xffff0000, v88
	v_lshlrev_b32_e32 v32, 16, v90
	v_and_b32_e32 v33, 0xffff0000, v90
	v_pk_add_f32 v[30:31], v[30:31], v[32:33]
	v_lshlrev_b32_e32 v32, 16, v89
	v_and_b32_e32 v33, 0xffff0000, v89
	v_lshlrev_b32_e32 v88, 16, v91
	v_and_b32_e32 v89, 0xffff0000, v91
	v_pk_add_f32 v[32:33], v[32:33], v[88:89]
	v_lshlrev_b32_e32 v88, 16, v84
	v_and_b32_e32 v89, 0xffff0000, v84
	s_waitcnt vmcnt(1)
	v_lshlrev_b32_e32 v90, 16, v86
	v_and_b32_e32 v91, 0xffff0000, v86
	v_lshlrev_b32_e32 v84, 16, v85
	v_and_b32_e32 v85, 0xffff0000, v85
	v_lshlrev_b32_e32 v86, 16, v87
	v_and_b32_e32 v87, 0xffff0000, v87
	v_pk_add_f32 v[88:89], v[88:89], v[90:91]
	v_pk_add_f32 v[90:91], v[84:85], v[86:87]
	ds_read_b128 v[84:87], v123 offset:7168
	s_waitcnt lgkmcnt(1)
	v_pk_mul_f32 v[98:99], v[30:31], v[92:93]
	v_pk_mul_f32 v[30:31], v[32:33], v[94:95]
	v_pk_fma_f32 v[32:33], v[10:11], s[16:17], v[98:99] op_sel_hi:[1,0,1]
	v_pk_fma_f32 v[30:31], v[12:13], s[16:17], v[30:31] op_sel_hi:[1,0,1]
	v_pk_mul_f32 v[12:13], v[88:89], v[92:93]
	v_pk_mul_f32 v[10:11], v[90:91], v[94:95]
	v_pk_fma_f32 v[12:13], v[14:15], s[16:17], v[12:13] op_sel_hi:[1,0,1]
	v_lshlrev_b32_e32 v14, 16, v80
	v_and_b32_e32 v15, 0xffff0000, v80
	v_lshlrev_b32_e32 v94, 16, v82
	v_and_b32_e32 v95, 0xffff0000, v82
	v_lshlrev_b32_e32 v80, 16, v81
	v_and_b32_e32 v81, 0xffff0000, v81
	v_lshlrev_b32_e32 v82, 16, v83
	v_and_b32_e32 v83, 0xffff0000, v83
	v_pk_add_f32 v[14:15], v[14:15], v[94:95]
	v_pk_add_f32 v[80:81], v[80:81], v[82:83]
	v_lshlrev_b32_e32 v82, 16, v74
	v_and_b32_e32 v83, 0xffff0000, v74
	s_waitcnt vmcnt(0)
	v_lshlrev_b32_e32 v94, 16, v78
	v_and_b32_e32 v95, 0xffff0000, v78
	v_lshlrev_b32_e32 v74, 16, v75
	v_and_b32_e32 v75, 0xffff0000, v75
	v_lshlrev_b32_e32 v78, 16, v79
	v_and_b32_e32 v79, 0xffff0000, v79
	v_pk_add_f32 v[78:79], v[74:75], v[78:79]
	s_waitcnt lgkmcnt(0)
	v_pk_mul_f32 v[74:75], v[14:15], v[84:85]
	v_pk_mul_f32 v[14:15], v[80:81], v[86:87]
	v_pk_add_f32 v[22:23], v[22:23], v[22:23] op_sel:[0,1] op_sel_hi:[1,0]
	v_pk_fma_f32 v[14:15], v[8:9], s[16:17], v[14:15] op_sel_hi:[1,0,1]
	v_pk_fma_f32 v[74:75], v[6:7], s[16:17], v[74:75] op_sel_hi:[1,0,1]
	v_pk_fma_f32 v[10:11], v[16:17], s[16:17], v[10:11] op_sel_hi:[1,0,1]
	v_add_f32_e32 v16, v32, v33
	v_add_f32_e32 v88, v31, v30
	v_mov_b32_e32 v103, v74
	v_mov_b32_e32 v23, v75
	v_mov_b32_e32 v17, v15
	v_mov_b32_e32 v89, v14
	v_pk_add_f32 v[6:7], v[102:103], v[22:23]
	v_pk_add_f32 v[8:9], v[16:17], v[88:89]
	v_pk_add_f32 v[82:83], v[82:83], v[94:95]
	v_pk_add_f32 v[6:7], v[6:7], v[8:9]
	v_pk_mul_f32 v[8:9], v[78:79], v[86:87]
	v_add_f32_e32 v80, v6, v7
	v_cndmask_b32_e32 v6, v1, v115, vcc
	v_lshlrev_b32_e32 v94, 2, v6
	s_nop 1
	v_mov_b32_dpp v81, v80 quad_perm:[1,0,3,2] row_mask:0xf bank_mask:0xf
	v_pk_mul_f32 v[6:7], v[82:83], v[84:85]
	v_cmp_lt_i32_e32 vcc, v116, v114
	v_pk_fma_f32 v[22:23], v[2:3], s[16:17], v[6:7] op_sel_hi:[1,0,1]
	v_pk_fma_f32 v[16:17], v[4:5], s[16:17], v[8:9] op_sel_hi:[1,0,1]
	v_cndmask_b32_e32 v2, v1, v116, vcc
	s_waitcnt lgkmcnt(0)
	v_add_f32_e32 v4, v80, v81
	v_lshlrev_b32_e32 v95, 2, v2
	s_nop 1
	v_mov_b32_dpp v5, v4 quad_perm:[2,3,0,1] row_mask:0xf bank_mask:0xf
	v_cmp_lt_i32_e32 vcc, v117, v114
	v_add_f32_e32 v90, v12, v13
	v_add_f32_e32 v92, v10, v11
	v_mov_b32_e32 v105, v22
	v_mov_b32_e32 v97, v23
	v_mov_b32_e32 v91, v16
	s_waitcnt lgkmcnt(0)
	v_add_f32_e32 v6, v4, v5
	v_cndmask_b32_e32 v4, v1, v117, vcc
	v_mov_b32_e32 v93, v17
	v_pk_add_f32 v[2:3], v[104:105], v[96:97]
	v_lshlrev_b32_e32 v96, 2, v4
	v_pk_add_f32 v[4:5], v[90:91], v[92:93]
	s_nop 1
	v_mov_b32_dpp v7, v6 row_half_mirror row_mask:0xf bank_mask:0xf
	v_pk_add_f32 v[2:3], v[2:3], v[4:5]
	v_cmp_lt_i32_e32 vcc, v118, v114
	v_add_f32_e32 v2, v2, v3
	s_nop 1
	v_mov_b32_dpp v4, v2 quad_perm:[1,0,3,2] row_mask:0xf bank_mask:0xf
	v_cndmask_b32_e32 v5, v1, v118, vcc
	s_waitcnt lgkmcnt(1)
	v_add_f32_e32 v3, v6, v7
	v_lshlrev_b32_e32 v92, 2, v5
	s_nop 1
	v_mov_b32_dpp v5, v3 row_mirror row_mask:0xf bank_mask:0xf
	s_waitcnt lgkmcnt(1)
	v_add_f32_e32 v2, v2, v4
	s_nop 1
	v_mov_b32_dpp v4, v2 quad_perm:[2,3,0,1] row_mask:0xf bank_mask:0xf
	v_cmp_lt_i32_e32 vcc, v119, v114
	s_waitcnt lgkmcnt(1)
	v_add_f32_e32 v3, v3, v5
	v_cndmask_b32_e32 v5, v1, v119, vcc
	s_waitcnt lgkmcnt(0)
	v_add_f32_e32 v2, v2, v4
	s_nop 1
	v_mov_b32_dpp v4, v2 row_half_mirror row_mask:0xf bank_mask:0xf
	v_lshlrev_b32_e32 v93, 2, v5
	v_mov_b32_e32 v5, v3
	v_mov_b32_e32 v93, v3
	s_nop 1
	v_permlane16_swap_b32_e32 v5, v93
	s_nop 1
	v_mov_b32_dpp v5, v93 quad_perm:[0,1,2,3] row_mask:0x5 bank_mask:0xf
	v_cmp_lt_i32_e32 vcc, v120, v114
	s_waitcnt lgkmcnt(1)
	v_add_f32_e32 v2, v2, v4
	s_nop 1
	v_mov_b32_dpp v4, v2 row_mirror row_mask:0xf bank_mask:0xf
	s_waitcnt lgkmcnt(1)
	v_add_f32_e32 v3, v3, v5
	v_cndmask_b32_e32 v5, v1, v120, vcc
	v_lshlrev_b32_e32 v97, 2, v5
	v_mov_b32_e32 v5, v3
	v_mov_b32_e32 v97, v3
	s_nop 1
	v_permlane32_swap_b32_e32 v5, v97
	s_nop 1
	v_mov_b32_dpp v5, v97 quad_perm:[0,1,2,3] row_mask:0x3 bank_mask:0xf
	s_waitcnt lgkmcnt(1)
	v_add_f32_e32 v2, v2, v4
	v_mov_b32_e32 v4, v2
	v_mov_b32_e32 v93, v2
	s_nop 1
	v_permlane16_swap_b32_e32 v4, v93
	s_nop 1
	v_mov_b32_dpp v4, v93 quad_perm:[0,1,2,3] row_mask:0x5 bank_mask:0xf
	s_waitcnt lgkmcnt(1)
	v_add_f32_e32 v98, v3, v5
	v_fmamk_f32 v67, v98, 0xba000000, v67
	s_waitcnt lgkmcnt(0)
	v_add_f32_e32 v2, v2, v4
	v_mov_b32_e32 v4, v2
	v_mov_b32_e32 v97, v2
	s_nop 1
	v_permlane32_swap_b32_e32 v4, v97
	s_nop 1
	v_mov_b32_dpp v4, v97 quad_perm:[0,1,2,3] row_mask:0x3 bank_mask:0xf
	v_fmamk_f32 v73, v98, 0xba000000, v73
	v_fmac_f32_e32 v66, 0xba000000, v98
	v_fmac_f32_e32 v72, 0xba000000, v98
	v_mov_b32_e32 v5, v73
	s_waitcnt lgkmcnt(0)
	v_add_f32_e32 v99, v2, v4
	v_mov_b32_e32 v4, v67
	v_fmac_f32_e32 v64, 0xba000000, v98
	v_fmac_f32_e32 v62, 0xba000000, v98
	v_mov_b32_e32 v2, v66
	v_mov_b32_e32 v3, v72
	v_pk_mul_f32 v[4:5], v[4:5], v[4:5]
	v_fmamk_f32 v65, v98, 0xba000000, v65
	v_pk_fma_f32 v[2:3], v[2:3], v[2:3], v[4:5]
	v_mov_b32_e32 v4, v64
	v_mov_b32_e32 v5, v62
	v_fmamk_f32 v83, v98, 0xba000000, v63
	v_pk_mul_f32 v[4:5], v[4:5], v[4:5]
	v_mov_b32_e32 v82, v65
	v_fmamk_f32 v78, v99, 0xba000000, v55
	v_fmamk_f32 v84, v99, 0xba000000, v57
	v_fmamk_f32 v79, v99, 0xba000000, v59
	v_fmac_f32_e32 v58, 0xba000000, v99
	v_fmamk_f32 v85, v99, 0xba000000, v61
	v_fmac_f32_e32 v60, 0xba000000, v99
	v_pk_fma_f32 v[4:5], v[82:83], v[82:83], v[4:5]
	v_fmac_f32_e32 v54, 0xba000000, v99
	v_fmac_f32_e32 v56, 0xba000000, v99
	v_pk_add_f32 v[2:3], v[2:3], v[4:5]
	v_mov_b32_e32 v57, v60
	v_pk_mul_f32 v[4:5], v[84:85], v[84:85]
	v_mov_b32_e32 v55, v58
	v_pk_mul_f32 v[6:7], v[78:79], v[78:79]
	v_pk_fma_f32 v[4:5], v[56:57], v[56:57], v[4:5]
	v_pk_fma_f32 v[6:7], v[54:55], v[54:55], v[6:7]
	v_fmamk_f32 v69, v98, 0xba000000, v69
	v_fmac_f32_e32 v68, 0xba000000, v98
	v_fmamk_f32 v71, v98, 0xba000000, v71
	v_fmac_f32_e32 v70, 0xba000000, v98
	v_pk_add_f32 v[4:5], v[4:5], v[6:7]
	v_pk_mul_f32 v[6:7], v[68:69], v[68:69]
	v_pk_mul_f32 v[8:9], v[70:71], v[70:71]
	v_fmamk_f32 v43, v99, 0xba000000, v43
	v_fmac_f32_e32 v42, 0xba000000, v99
	v_fmamk_f32 v45, v99, 0xba000000, v45
	v_fmac_f32_e32 v44, 0xba000000, v99
	v_pk_mov_b32 v[80:81], v[8:9], v[6:7] op_sel:[1,0]
	v_mov_b32_e32 v9, v7
	v_pk_add_f32 v[2:3], v[2:3], v[2:3] op_sel_hi:[0,1]
	v_pk_add_f32 v[6:7], v[8:9], v[80:81]
	v_pk_mul_f32 v[8:9], v[42:43], v[42:43]
	v_pk_mul_f32 v[80:81], v[44:45], v[44:45]
	v_fmac_f32_e32 v48, 0xba000000, v98
	v_pk_mov_b32 v[86:87], v[80:81], v[8:9] op_sel:[1,0]
	v_mov_b32_e32 v81, v9
	v_fmac_f32_e32 v40, 0xba000000, v98
	v_fmamk_f32 v49, v98, 0xba000000, v49
	v_mul_f32_e32 v2, v48, v48
	v_pk_add_f32 v[8:9], v[86:87], v[80:81]
	v_fmamk_f32 v41, v98, 0xba000000, v41
	v_fmac_f32_e32 v34, 0xba000000, v99
	v_pk_fma_f32 v[80:81], v[48:49], v[48:49], v[2:3] op_sel_hi:[1,1,0]
	v_mul_f32_e32 v2, v40, v40
	v_fmac_f32_e32 v36, 0xba000000, v99
	v_fmamk_f32 v35, v99, 0xba000000, v35
	v_pk_fma_f32 v[86:87], v[40:41], v[40:41], v[2:3] op_sel_hi:[1,1,0]
	v_mul_f32_e32 v2, v34, v34
	v_pk_add_f32 v[6:7], v[6:7], v[6:7] op_sel_hi:[0,1]
	v_fmamk_f32 v37, v99, 0xba000000, v37
	v_pk_fma_f32 v[88:89], v[34:35], v[34:35], v[2:3] op_sel_hi:[1,1,0]
	v_mul_f32_e32 v2, v36, v36
	v_fmamk_f32 v39, v98, 0xba000000, v39
	v_fmac_f32_e32 v38, 0xba000000, v98
	v_fmamk_f32 v47, v98, 0xba000000, v47
	v_fmac_f32_e32 v46, 0xba000000, v98
	v_pk_add_f32 v[4:5], v[4:5], v[4:5] op_sel_hi:[0,1]
	v_pk_add_f32 v[8:9], v[8:9], v[8:9] op_sel_hi:[0,1]
	v_pk_fma_f32 v[90:91], v[36:37], v[36:37], v[2:3] op_sel_hi:[1,1,0]
	v_fmamk_f32 v29, v99, 0xba000000, v29
	v_fmac_f32_e32 v28, 0xba000000, v99
	v_fmamk_f32 v27, v99, 0xba000000, v27
	v_fmac_f32_e32 v26, 0xba000000, v99
	v_mul_f32_e32 v80, v46, v46
	v_mul_f32_e32 v86, v47, v47
	v_mul_f32_e32 v2, v38, v38
	v_mul_f32_e32 v6, v39, v39
	v_pk_add_f32 v[80:81], v[80:81], v[86:87]
	v_pk_add_f32 v[2:3], v[6:7], v[2:3]
	v_mul_f32_e32 v88, v26, v26
	v_mul_f32_e32 v90, v27, v27
	v_mul_f32_e32 v8, v28, v28
	v_mul_f32_e32 v4, v29, v29
	v_pk_add_f32 v[2:3], v[80:81], v[2:3]
	v_pk_add_f32 v[6:7], v[88:89], v[90:91]
	v_pk_add_f32 v[4:5], v[8:9], v[4:5]
	v_fmamk_f32 v25, v98, 0xba000000, v25
	v_fmac_f32_e32 v24, 0xba000000, v98
	v_fmamk_f32 v77, v98, 0xba000000, v77
	v_fmac_f32_e32 v76, 0xba000000, v98
	v_pk_add_f32 v[2:3], v[2:3], v[2:3] op_sel_hi:[0,1]
	v_pk_add_f32 v[4:5], v[6:7], v[4:5]
	v_pk_mul_f32 v[6:7], v[24:25], v[24:25]
	v_pk_mul_f32 v[8:9], v[76:77], v[76:77]
	v_fmac_f32_e32 v32, 0xba000000, v98
	v_pk_mov_b32 v[80:81], v[8:9], v[6:7] op_sel:[1,0]
	v_mov_b32_e32 v9, v7
	v_fmac_f32_e32 v30, 0xba000000, v98
	v_fmamk_f32 v33, v98, 0xba000000, v33
	v_mul_f32_e32 v2, v32, v32
	v_pk_add_f32 v[6:7], v[8:9], v[80:81]
	v_fmamk_f32 v31, v98, 0xba000000, v31
	v_pk_fma_f32 v[86:87], v[32:33], v[32:33], v[2:3] op_sel_hi:[1,1,0]
	v_mul_f32_e32 v2, v30, v30
	v_pk_add_f32 v[6:7], v[6:7], v[6:7] op_sel_hi:[0,1]
	v_pk_fma_f32 v[88:89], v[30:31], v[30:31], v[2:3] op_sel_hi:[1,1,0]
	v_fmamk_f32 v15, v98, 0xba000000, v15
	v_fmac_f32_e32 v14, 0xba000000, v98
	v_fmamk_f32 v75, v98, 0xba000000, v75
	v_fmac_f32_e32 v74, 0xba000000, v98
	v_mul_f32_e32 v86, v74, v74
	v_mul_f32_e32 v88, v75, v75
	v_mul_f32_e32 v2, v14, v14
	v_mul_f32_e32 v6, v15, v15
	v_pk_add_f32 v[86:87], v[86:87], v[88:89]
	v_pk_add_f32 v[2:3], v[6:7], v[2:3]
	v_pk_add_f32 v[4:5], v[4:5], v[4:5] op_sel_hi:[0,1]
	v_pk_add_f32 v[2:3], v[86:87], v[2:3]
	v_fmamk_f32 v21, v99, 0xba000000, v21
	v_add_f32_e32 v4, v2, v3
	v_fmac_f32_e32 v20, 0xba000000, v99
	v_fmamk_f32 v19, v99, 0xba000000, v19
	v_fmac_f32_e32 v18, 0xba000000, v99
	s_nop 1
	v_mov_b32_dpp v6, v4 quad_perm:[1,0,3,2] row_mask:0xf bank_mask:0xf
	v_pk_mul_f32 v[8:9], v[20:21], v[20:21]
	v_pk_mul_f32 v[80:81], v[18:19], v[18:19]
	v_fmac_f32_e32 v12, 0xba000000, v99
	v_pk_mov_b32 v[2:3], v[80:81], v[8:9] op_sel:[1,0]
	v_mov_b32_e32 v81, v9
	v_pk_add_f32 v[2:3], v[2:3], v[80:81]
	v_fmac_f32_e32 v10, 0xba000000, v99
	v_pk_add_f32 v[2:3], v[2:3], v[2:3] op_sel_hi:[0,1]
	s_waitcnt lgkmcnt(0)
	v_add_f32_e32 v2, v4, v6
	s_nop 1
	v_mov_b32_dpp v4, v2 quad_perm:[2,3,0,1] row_mask:0xf bank_mask:0xf
	v_fmamk_f32 v13, v99, 0xba000000, v13
	v_fmamk_f32 v11, v99, 0xba000000, v11
	v_fmamk_f32 v17, v99, 0xba000000, v17
	v_fmac_f32_e32 v16, 0xba000000, v99
	s_waitcnt lgkmcnt(0)
	v_add_f32_e32 v4, v2, v4
	s_nop 1
	v_mov_b32_dpp v55, v4 row_half_mirror row_mask:0xf bank_mask:0xf
	v_mul_f32_e32 v2, v12, v12
	v_pk_fma_f32 v[6:7], v[12:13], v[12:13], v[2:3] op_sel_hi:[1,1,0]
	v_mul_f32_e32 v2, v10, v10
	v_pk_fma_f32 v[8:9], v[10:11], v[10:11], v[2:3] op_sel_hi:[1,1,0]
	s_waitcnt lgkmcnt(0)
	v_add_f32_e32 v2, v4, v55
	s_nop 1
	v_mov_b32_dpp v4, v2 row_mirror row_mask:0xf bank_mask:0xf
	v_fmamk_f32 v23, v99, 0xba000000, v23
	v_fmac_f32_e32 v22, 0xba000000, v99
	v_mul_f32_e32 v6, v22, v22
	v_mul_f32_e32 v8, v23, v23
	s_waitcnt lgkmcnt(0)
	v_add_f32_e32 v55, v2, v4
	v_mul_f32_e32 v2, v16, v16
	v_mul_f32_e32 v4, v17, v17
	v_pk_add_f32 v[6:7], v[6:7], v[8:9]
	v_pk_add_f32 v[2:3], v[2:3], v[4:5]
	v_mov_b32_e32 v57, v55
	v_mov_b32_e32 v93, v55
	s_nop 1
	v_permlane16_swap_b32_e32 v57, v93
	s_nop 1
	v_mov_b32_dpp v57, v93 quad_perm:[0,1,2,3] row_mask:0x5 bank_mask:0xf
	v_pk_add_f32 v[2:3], v[6:7], v[2:3]
	s_waitcnt lgkmcnt(0)
	v_add_f32_e32 v55, v55, v57
	v_add_f32_e32 v2, v2, v3
	s_nop 1
	v_mov_b32_dpp v5, v2 quad_perm:[1,0,3,2] row_mask:0xf bank_mask:0xf
	v_mov_b32_e32 v57, v55
	v_mov_b32_e32 v97, v55
	s_nop 1
	v_permlane32_swap_b32_e32 v57, v97
	s_nop 1
	v_mov_b32_dpp v57, v97 quad_perm:[0,1,2,3] row_mask:0x3 bank_mask:0xf
	s_waitcnt lgkmcnt(1)
	v_add_f32_e32 v2, v2, v5
	s_nop 1
	v_mov_b32_dpp v5, v2 quad_perm:[2,3,0,1] row_mask:0xf bank_mask:0xf
	s_waitcnt lgkmcnt(1)
	v_add_f32_e32 v3, v55, v57
	v_fmamk_f32 v3, v3, 0x3a000000, v121
	v_mul_f32_e32 v4, 0x4f800000, v3
	v_cmp_gt_f32_e32 vcc, s30, v3
	s_waitcnt lgkmcnt(0)
	v_add_f32_e32 v2, v2, v5
	s_nop 1
	v_mov_b32_dpp v5, v2 row_half_mirror row_mask:0xf bank_mask:0xf
	v_cndmask_b32_e32 v3, v3, v4, vcc
	v_sqrt_f32_e32 v4, v3
	s_waitcnt lgkmcnt(0)
	v_add_f32_e32 v2, v2, v5
	s_nop 1
	v_mov_b32_dpp v5, v2 row_mirror row_mask:0xf bank_mask:0xf
	v_add_u32_e32 v6, -1, v4
	v_fma_f32 v7, -v6, v4, v3
	v_cmp_ge_f32_e64 s[0:1], 0, v7
	v_add_u32_e32 v7, 1, v4
	s_waitcnt lgkmcnt(0)
	v_add_f32_e32 v2, v2, v5
	v_mov_b32_e32 v5, v2
	v_mov_b32_e32 v93, v2
	s_nop 1
	v_permlane16_swap_b32_e32 v5, v93
	s_nop 1
	v_mov_b32_dpp v5, v93 quad_perm:[0,1,2,3] row_mask:0x5 bank_mask:0xf
	v_cndmask_b32_e64 v6, v4, v6, s[0:1]
	v_fma_f32 v4, -v7, v4, v3
	v_cmp_lt_f32_e64 s[0:1], 0, v4
	s_waitcnt lgkmcnt(0)
	v_add_f32_e32 v2, v2, v5
	v_cndmask_b32_e64 v4, v6, v7, s[0:1]
	v_mul_f32_e32 v6, 0x37800000, v4
	v_mov_b32_e32 v5, v2
	v_mov_b32_e32 v97, v2
	s_nop 1
	v_permlane32_swap_b32_e32 v5, v97
	s_nop 1
	v_mov_b32_dpp v5, v97 quad_perm:[0,1,2,3] row_mask:0x3 bank_mask:0xf
	v_cndmask_b32_e32 v4, v4, v6, vcc
	v_cmp_class_f32_e32 vcc, v3, v122
	s_waitcnt lgkmcnt(0)
	v_add_f32_e32 v2, v2, v5
	v_cndmask_b32_e32 v3, v4, v3, vcc
	v_div_scale_f32 v4, s[0:1], v3, v3, 1.0
	v_rcp_f32_e32 v6, v4
	v_fmamk_f32 v2, v2, 0x3a000000, v121
	v_mul_f32_e32 v5, 0x4f800000, v2
	v_cmp_gt_f32_e64 s[0:1], s30, v2
	v_fma_f32 v7, -v4, v6, 1.0
	v_fmac_f32_e32 v6, v7, v6
	v_cndmask_b32_e64 v2, v2, v5, s[0:1]
	v_div_scale_f32 v7, vcc, 1.0, v3, 1.0
	v_sqrt_f32_e32 v5, v2
	v_mul_f32_e32 v8, v7, v6
	v_fma_f32 v9, -v4, v8, v7
	v_fmac_f32_e32 v8, v9, v6
	v_fma_f32 v4, -v4, v8, v7
	v_add_u32_e32 v7, -1, v5
	v_fma_f32 v9, -v7, v5, v2
	v_cmp_ge_f32_e64 s[4:5], 0, v9
	v_add_u32_e32 v9, 1, v5
	v_div_fmas_f32 v4, v4, v6, v8
	v_cndmask_b32_e64 v7, v5, v7, s[4:5]
	v_fma_f32 v5, -v9, v5, v2
	v_cmp_lt_f32_e64 s[4:5], 0, v5
	v_div_fixup_f32 v80, v4, v3, 1.0
	v_mov_b32_e32 v81, v80
	v_cndmask_b32_e64 v5, v7, v9, s[4:5]
	v_mul_f32_e32 v7, 0x37800000, v5
	v_cndmask_b32_e64 v5, v5, v7, s[0:1]
	v_cmp_class_f32_e64 s[0:1], v2, v122
	v_pk_mul_f32 v[86:87], v[66:67], v[80:81] op_sel_hi:[1,0]
	v_pk_mul_f32 v[64:65], v[64:65], v[80:81] op_sel_hi:[1,0]
	v_cndmask_b32_e64 v55, v5, v2, s[0:1]
	v_div_scale_f32 v2, s[0:1], v55, v55, 1.0
	v_rcp_f32_e32 v57, v2
	s_add_u32 s0, s66, s22
	s_addc_u32 s1, s67, s23
	v_lshl_add_u64 v[52:53], s[0:1], 0, v[52:53]
	v_fma_f32 v3, -v2, v57, 1.0
	v_fmac_f32_e32 v57, v3, v57
	v_div_scale_f32 v3, vcc, 1.0, v55, 1.0
	v_mul_f32_e32 v59, v3, v57
	v_fma_f32 v4, -v2, v59, v3
	v_fmac_f32_e32 v59, v4, v57
	v_fma_f32 v61, -v2, v59, v3
	ds_read_b128 v[2:5], v123 offset:8192
	ds_read_b128 v[6:9], v123 offset:16384
	v_div_fmas_f32 v57, v61, v57, v59
	s_mov_b64 s[0:1], -1
	s_and_b64 vcc, exec, s[20:21]
	s_waitcnt lgkmcnt(0)
	v_pk_fma_f32 v[66:67], v[4:5], v[64:65], v[8:9]
	v_pk_fma_f32 v[64:65], v[2:3], v[86:87], v[6:7]
	global_store_dwordx4 v[52:53], v[64:67], off
	s_nop 1
	v_pk_mul_f32 v[66:67], v[72:73], v[80:81]
	s_cbranch_vccz .LBB0_2078
	ds_read_b128 v[86:89], v123 offset:9216
	ds_read_b128 v[90:93], v123 offset:17408
	v_mov_b32_e32 v64, v80
	v_mov_b32_e32 v65, v80
	v_mov_b32_e32 v63, v83
	v_pk_mul_f32 v[64:65], v[62:63], v[64:65]
	s_waitcnt lgkmcnt(0)
	v_pk_fma_f32 v[86:87], v[66:67], v[86:87], v[90:91]
	v_pk_fma_f32 v[88:89], v[64:65], v[88:89], v[92:93]
	global_store_dwordx4 v[52:53], v[86:89], off offset:1024
	s_mov_b64 s[0:1], 0
